# v3: + hoisted row-scale loads in P6/P14 epilogues; EpiResT epilogues (P4a,P7a,P12) software-pipelined 8-16 base loads deep with counted vmcnt
# speedup vs baseline: 1.0156x; 1.0013x over previous
; __device__ __forceinline__ void st4_bf(bf16_t* p, const f32x4 v) { u32x2 w; w.x = cvt_pk_bf16(v[0], v[1]); w.y = cvt_pk_bf16(v[2], v[3]); *(u32x2*)p = w; }
;     static __device__ __forceinline__ f32x4 ldb(const bf16_t* p) { return ld4_bf(p); }
;     __device__ __forceinline__ void operator()(const AccT& acc, const Unit& u, int wr, int wc, int fr, int fq) const { if (u.g == 0) q(acc, u, wr, wc, fr, fq); else kv(acc, u, wr, wc, fr, fq); }
;     __device__ __forceinline__ void operator()(const AccT& acc, const Unit& u, int wr, int wc, int fr, int fq) const {
;         const int cnd = cond_of(u.orow0);
;         const BT* bp = (u.orow0 < ML) ? bl + (size_t)u.orow0 * DM : bc + (size_t)(u.orow0 - ML) * DM;
;         bf16_t* op = out + (size_t)u.orow0 * DM;
;         const int rl0 = wr * 64 + fr, col0 = u.pn * BM + wc * 32 + 4 * fq;
;         f32x4 gv[2][2];
; #pragma unroll
;         for (int bj = 0; bj < 2; ++bj)
; #pragma unroll
;             for (int n = 0; n < 2; ++n) gv[bj][n] = *(const f32x4*)(gate + (size_t)cnd * NMOD + col0 + bj * HALF + n * 16) * scale;
; #pragma unroll
;         for (int ai = 0; ai < 2; ++ai)
; #pragma unroll
;             for (int m = 0; m < 4; ++m) { const size_t off = (size_t)(rl0 + ai * HALF + m * 16) * DM + col0;
; #pragma unroll
;                 for (int bj = 0; bj < 2; ++bj)
; #pragma unroll
;                     for (int n = 0; n < 2; ++n) { const f32x4 bs = ldb(bp + off + bj * HALF + n * 16); st4_bf(op + off + bj * HALF + n * 16, bs + gv[bj][n] * acc[ai][bj][m][n]); }
;                 asm volatile("" ::: "memory"); }
;     }
.LBB0_1209:
	s_min_i32 s6, s26, 0x4000
	s_ashr_i32 s6, s6, 12
	v_lshl_or_b32 v148, s61, 8, v199
	s_lshl_b64 s[26:27], s[26:27], 12
	s_mul_hi_i32 s21, s6, 0xc000
	s_mul_i32 s6, s6, 0xc000
	v_ashrrev_i32_e32 v149, 31, v148
	s_add_u32 s28, s54, s6
	v_lshl_add_u64 v[154:155], v[168:169], 0, v[148:149]
	s_addc_u32 s29, s55, s21
	v_lshl_add_u64 v[156:157], v[154:155], 2, v[146:147]
	v_lshl_add_u64 v[130:131], v[148:149], 2, s[28:29]
	global_load_dwordx4 v[208:211], v[156:157], off
	global_load_dwordx4 v[142:145], v[130:131], off
	s_add_u32 s26, s51, s26
	s_addc_u32 s27, s53, s27
	v_lshl_add_u64 v[154:155], v[154:155], 1, s[26:27]
	global_load_dwordx4 v[138:141], v[130:131], off offset:64
	global_load_dwordx4 v[134:137], v[130:131], off offset:512
	s_nop 0
	global_load_dwordx4 v[130:133], v[130:131], off offset:576
	s_andn2_b64 vcc, exec, s[22:23]
	s_mov_b64 s[22:23], -1
	global_load_dwordx4 v[212:215], v[156:157], off offset:64
	global_load_dwordx4 v[216:219], v[156:157], off offset:512
	global_load_dwordx4 v[220:223], v[156:157], off offset:576
	v_lshl_add_u64 v[158:159], v[170:171], 0, v[148:149]
	v_lshl_add_u64 v[158:159], v[158:159], 2, v[146:147]
	global_load_dwordx4 v[224:227], v[158:159], off
	global_load_dwordx4 v[228:231], v[158:159], off offset:64
	global_load_dwordx4 v[232:235], v[158:159], off offset:512
	global_load_dwordx4 v[236:239], v[158:159], off offset:576
	s_waitcnt vmcnt(7)
	v_pk_fma_f32 v[126:127], v[126:127], v[142:143], v[208:209]
	v_pk_fma_f32 v[128:129], v[128:129], v[144:145], v[210:211]
	v_cvt_pk_bf16_f32 v126, v126, v127
	s_nop 0
	v_cvt_pk_bf16_f32 v127, v128, v129
	global_store_dwordx2 v[154:155], v[126:127], off
	v_lshl_add_u64 v[158:159], v[172:173], 0, v[148:149]
	v_lshl_add_u64 v[158:159], v[158:159], 2, v[146:147]
	global_load_dwordx4 v[208:211], v[158:159], off
	s_waitcnt vmcnt(8)
	v_pk_fma_f32 v[122:123], v[122:123], v[138:139], v[212:213]
	v_pk_fma_f32 v[124:125], v[124:125], v[140:141], v[214:215]
	v_cvt_pk_bf16_f32 v122, v122, v123
	s_nop 0
	v_cvt_pk_bf16_f32 v123, v124, v125
	global_store_dwordx2 v[154:155], v[122:123], off offset:32
	global_load_dwordx4 v[212:215], v[158:159], off offset:64
	s_waitcnt vmcnt(9)
	v_pk_fma_f32 v[118:119], v[118:119], v[134:135], v[216:217]
	v_pk_fma_f32 v[120:121], v[120:121], v[136:137], v[218:219]
	v_cvt_pk_bf16_f32 v118, v118, v119
	v_lshl_add_u64 v[122:123], v[170:171], 0, v[148:149]
	v_cvt_pk_bf16_f32 v119, v120, v121
	global_store_dwordx2 v[154:155], v[118:119], off offset:256
	global_load_dwordx4 v[216:219], v[158:159], off offset:512
	v_lshl_add_u64 v[124:125], v[122:123], 2, v[146:147]
	s_waitcnt vmcnt(10)
	v_pk_fma_f32 v[110:111], v[110:111], v[130:131], v[220:221]
	v_pk_fma_f32 v[112:113], v[112:113], v[132:133], v[222:223]
	v_cvt_pk_bf16_f32 v110, v110, v111
	v_lshl_add_u64 v[118:119], v[122:123], 1, s[26:27]
	v_cvt_pk_bf16_f32 v111, v112, v113
	global_store_dwordx2 v[154:155], v[110:111], off offset:288
	global_load_dwordx4 v[220:223], v[158:159], off offset:576
	s_waitcnt vmcnt(11)
	v_pk_fma_f32 v[110:111], v[114:115], v[142:143], v[224:225]
	v_pk_fma_f32 v[112:113], v[116:117], v[144:145], v[226:227]
	v_cvt_pk_bf16_f32 v110, v110, v111
	s_nop 0
	v_cvt_pk_bf16_f32 v111, v112, v113
	global_store_dwordx2 v[118:119], v[110:111], off
	v_lshl_add_u64 v[158:159], v[174:175], 0, v[148:149]
	v_lshl_add_u64 v[158:159], v[158:159], 2, v[146:147]
	global_load_dwordx4 v[224:227], v[158:159], off
	s_waitcnt vmcnt(12)
	v_pk_fma_f32 v[106:107], v[106:107], v[138:139], v[228:229]
	v_pk_fma_f32 v[108:109], v[108:109], v[140:141], v[230:231]
	v_cvt_pk_bf16_f32 v106, v106, v107
	s_nop 0
	v_cvt_pk_bf16_f32 v107, v108, v109
	global_store_dwordx2 v[118:119], v[106:107], off offset:32
	global_load_dwordx4 v[228:231], v[158:159], off offset:64
	s_waitcnt vmcnt(13)
	v_pk_fma_f32 v[102:103], v[102:103], v[134:135], v[232:233]
	v_pk_fma_f32 v[104:105], v[104:105], v[136:137], v[234:235]
	v_cvt_pk_bf16_f32 v102, v102, v103
	v_lshl_add_u64 v[106:107], v[172:173], 0, v[148:149]
	v_cvt_pk_bf16_f32 v103, v104, v105
	global_store_dwordx2 v[118:119], v[102:103], off offset:256
	global_load_dwordx4 v[232:235], v[158:159], off offset:512
	v_lshl_add_u64 v[108:109], v[106:107], 2, v[146:147]
	s_waitcnt vmcnt(14)
	v_pk_fma_f32 v[94:95], v[94:95], v[130:131], v[236:237]
	v_pk_fma_f32 v[96:97], v[96:97], v[132:133], v[238:239]
	v_cvt_pk_bf16_f32 v94, v94, v95
	v_lshl_add_u64 v[102:103], v[106:107], 1, s[26:27]
	v_cvt_pk_bf16_f32 v95, v96, v97
	global_store_dwordx2 v[118:119], v[94:95], off offset:288
	global_load_dwordx4 v[236:239], v[158:159], off offset:576
	s_waitcnt vmcnt(14)
	v_pk_fma_f32 v[94:95], v[98:99], v[142:143], v[208:209]
	v_pk_fma_f32 v[96:97], v[100:101], v[144:145], v[210:211]
	v_cvt_pk_bf16_f32 v94, v94, v95
	s_nop 0
	v_cvt_pk_bf16_f32 v95, v96, v97
	global_store_dwordx2 v[102:103], v[94:95], off
	v_lshl_add_u64 v[158:159], v[176:177], 0, v[148:149]
	v_lshl_add_u64 v[158:159], v[158:159], 2, v[146:147]
	global_load_dwordx4 v[208:211], v[158:159], off
	s_waitcnt vmcnt(14)
	v_pk_fma_f32 v[90:91], v[90:91], v[138:139], v[212:213]
	v_pk_fma_f32 v[92:93], v[92:93], v[140:141], v[214:215]
	v_cvt_pk_bf16_f32 v90, v90, v91
	s_nop 0
	v_cvt_pk_bf16_f32 v91, v92, v93
	global_store_dwordx2 v[102:103], v[90:91], off offset:32
	global_load_dwordx4 v[212:215], v[158:159], off offset:64
	s_waitcnt vmcnt(14)
	v_pk_fma_f32 v[86:87], v[86:87], v[134:135], v[216:217]
	v_pk_fma_f32 v[88:89], v[88:89], v[136:137], v[218:219]
	v_cvt_pk_bf16_f32 v86, v86, v87
	v_lshl_add_u64 v[90:91], v[174:175], 0, v[148:149]
	v_cvt_pk_bf16_f32 v87, v88, v89
	global_store_dwordx2 v[102:103], v[86:87], off offset:256
	global_load_dwordx4 v[216:219], v[158:159], off offset:512
	v_lshl_add_u64 v[92:93], v[90:91], 2, v[146:147]
	s_waitcnt vmcnt(14)
; __device__ __forceinline__ void st4_bf(bf16_t* p, const f32x4 v) { u32x2 w; w.x = cvt_pk_bf16(v[0], v[1]); w.y = cvt_pk_bf16(v[2], v[3]); *(u32x2*)p = w; }
;     static __device__ __forceinline__ f32x4 ldb(const bf16_t* p) { return ld4_bf(p); }
;     __device__ __forceinline__ void operator()(const AccT& acc, const Unit& u, int wr, int wc, int fr, int fq) const { if (u.g == 0) q(acc, u, wr, wc, fr, fq); else kv(acc, u, wr, wc, fr, fq); }
;     __device__ __forceinline__ void operator()(const AccT& acc, const Unit& u, int wr, int wc, int fr, int fq) const {
;         const int cnd = cond_of(u.orow0);
;         const BT* bp = (u.orow0 < ML) ? bl + (size_t)u.orow0 * DM : bc + (size_t)(u.orow0 - ML) * DM;
;         bf16_t* op = out + (size_t)u.orow0 * DM;
;         const int rl0 = wr * 64 + fr, col0 = u.pn * BM + wc * 32 + 4 * fq;
;         f32x4 gv[2][2];
; #pragma unroll
;         for (int bj = 0; bj < 2; ++bj)
; #pragma unroll
;             for (int n = 0; n < 2; ++n) gv[bj][n] = *(const f32x4*)(gate + (size_t)cnd * NMOD + col0 + bj * HALF + n * 16) * scale;
; #pragma unroll
;         for (int ai = 0; ai < 2; ++ai)
; #pragma unroll
;             for (int m = 0; m < 4; ++m) { const size_t off = (size_t)(rl0 + ai * HALF + m * 16) * DM + col0;
; #pragma unroll
;                 for (int bj = 0; bj < 2; ++bj)
; #pragma unroll
;                     for (int n = 0; n < 2; ++n) { const f32x4 bs = ldb(bp + off + bj * HALF + n * 16); st4_bf(op + off + bj * HALF + n * 16, bs + gv[bj][n] * acc[ai][bj][m][n]); }
;                 asm volatile("" ::: "memory"); }
;     }
	v_pk_fma_f32 v[78:79], v[78:79], v[130:131], v[220:221]
	v_pk_fma_f32 v[80:81], v[80:81], v[132:133], v[222:223]
	v_cvt_pk_bf16_f32 v78, v78, v79
	v_lshl_add_u64 v[86:87], v[90:91], 1, s[26:27]
	v_cvt_pk_bf16_f32 v79, v80, v81
	global_store_dwordx2 v[102:103], v[78:79], off offset:288
	global_load_dwordx4 v[220:223], v[158:159], off offset:576
	s_waitcnt vmcnt(14)
	v_pk_fma_f32 v[78:79], v[82:83], v[142:143], v[224:225]
	v_pk_fma_f32 v[80:81], v[84:85], v[144:145], v[226:227]
	v_cvt_pk_bf16_f32 v78, v78, v79
	s_nop 0
	v_cvt_pk_bf16_f32 v79, v80, v81
	global_store_dwordx2 v[86:87], v[78:79], off
	v_lshl_add_u64 v[158:159], v[178:179], 0, v[148:149]
	v_lshl_add_u64 v[158:159], v[158:159], 2, v[146:147]
	global_load_dwordx4 v[224:227], v[158:159], off
	s_waitcnt vmcnt(14)
	v_pk_fma_f32 v[74:75], v[74:75], v[138:139], v[228:229]
	v_pk_fma_f32 v[76:77], v[76:77], v[140:141], v[230:231]
	v_cvt_pk_bf16_f32 v74, v74, v75
	s_nop 0
	v_cvt_pk_bf16_f32 v75, v76, v77
	global_store_dwordx2 v[86:87], v[74:75], off offset:32
	global_load_dwordx4 v[228:231], v[158:159], off offset:64
	s_waitcnt vmcnt(14)
	v_pk_fma_f32 v[70:71], v[70:71], v[134:135], v[232:233]
	v_pk_fma_f32 v[72:73], v[72:73], v[136:137], v[234:235]
	v_cvt_pk_bf16_f32 v70, v70, v71
	v_lshl_add_u64 v[74:75], v[176:177], 0, v[148:149]
	v_cvt_pk_bf16_f32 v71, v72, v73
	global_store_dwordx2 v[86:87], v[70:71], off offset:256
	global_load_dwordx4 v[232:235], v[158:159], off offset:512
	v_lshl_add_u64 v[76:77], v[74:75], 2, v[146:147]
	s_waitcnt vmcnt(14)
	v_pk_fma_f32 v[66:67], v[66:67], v[130:131], v[236:237]
	v_pk_fma_f32 v[68:69], v[68:69], v[132:133], v[238:239]
	v_cvt_pk_bf16_f32 v66, v66, v67
	v_lshl_add_u64 v[70:71], v[74:75], 1, s[26:27]
	v_cvt_pk_bf16_f32 v67, v68, v69
	global_store_dwordx2 v[86:87], v[66:67], off offset:288
	global_load_dwordx4 v[236:239], v[158:159], off offset:576
	s_waitcnt vmcnt(14)
	v_pk_fma_f32 v[62:63], v[62:63], v[142:143], v[208:209]
	v_pk_fma_f32 v[64:65], v[64:65], v[144:145], v[210:211]
	v_cvt_pk_bf16_f32 v62, v62, v63
	s_nop 0
	v_cvt_pk_bf16_f32 v63, v64, v65
	global_store_dwordx2 v[70:71], v[62:63], off
	v_lshl_add_u64 v[158:159], v[180:181], 0, v[148:149]
	v_lshl_add_u64 v[158:159], v[158:159], 2, v[146:147]
	global_load_dwordx4 v[208:211], v[158:159], off
	s_waitcnt vmcnt(14)
	v_pk_fma_f32 v[58:59], v[58:59], v[138:139], v[212:213]
	v_pk_fma_f32 v[60:61], v[60:61], v[140:141], v[214:215]
	v_cvt_pk_bf16_f32 v58, v58, v59
	s_nop 0
	v_cvt_pk_bf16_f32 v59, v60, v61
	global_store_dwordx2 v[70:71], v[58:59], off offset:32
	global_load_dwordx4 v[212:215], v[158:159], off offset:64
	s_waitcnt vmcnt(14)
	v_pk_fma_f32 v[54:55], v[54:55], v[134:135], v[216:217]
	v_pk_fma_f32 v[56:57], v[56:57], v[136:137], v[218:219]
	v_cvt_pk_bf16_f32 v54, v54, v55
	v_lshl_add_u64 v[58:59], v[178:179], 0, v[148:149]
	v_cvt_pk_bf16_f32 v55, v56, v57
	global_store_dwordx2 v[70:71], v[54:55], off offset:256
	global_load_dwordx4 v[216:219], v[158:159], off offset:512
	v_lshl_add_u64 v[60:61], v[58:59], 2, v[146:147]
	s_waitcnt vmcnt(14)
	v_pk_fma_f32 v[46:47], v[46:47], v[130:131], v[220:221]
	v_pk_fma_f32 v[48:49], v[48:49], v[132:133], v[222:223]
	v_cvt_pk_bf16_f32 v46, v46, v47
	v_lshl_add_u64 v[54:55], v[58:59], 1, s[26:27]
	v_cvt_pk_bf16_f32 v47, v48, v49
	global_store_dwordx2 v[70:71], v[46:47], off offset:288
	global_load_dwordx4 v[220:223], v[158:159], off offset:576
	s_waitcnt vmcnt(14)
	v_pk_fma_f32 v[46:47], v[50:51], v[142:143], v[224:225]
	v_pk_fma_f32 v[48:49], v[52:53], v[144:145], v[226:227]
	v_cvt_pk_bf16_f32 v46, v46, v47
	s_nop 0
	v_cvt_pk_bf16_f32 v47, v48, v49
	global_store_dwordx2 v[54:55], v[46:47], off
	v_lshl_add_u64 v[158:159], v[182:183], 0, v[148:149]
	v_lshl_add_u64 v[158:159], v[158:159], 2, v[146:147]
	global_load_dwordx4 v[224:227], v[158:159], off
	s_waitcnt vmcnt(14)
; __device__ __forceinline__ void st4_bf(bf16_t* p, const f32x4 v) { u32x2 w; w.x = cvt_pk_bf16(v[0], v[1]); w.y = cvt_pk_bf16(v[2], v[3]); *(u32x2*)p = w; }
;     static __device__ __forceinline__ f32x4 ldb(const bf16_t* p) { return ld4_bf(p); }
;     __device__ __forceinline__ void operator()(const AccT& acc, const Unit& u, int wr, int wc, int fr, int fq) const { if (u.g == 0) q(acc, u, wr, wc, fr, fq); else kv(acc, u, wr, wc, fr, fq); }
;     __device__ __forceinline__ void operator()(const AccT& acc, const Unit& u, int wr, int wc, int fr, int fq) const {
;         const int cnd = cond_of(u.orow0);
;         const BT* bp = (u.orow0 < ML) ? bl + (size_t)u.orow0 * DM : bc + (size_t)(u.orow0 - ML) * DM;
;         bf16_t* op = out + (size_t)u.orow0 * DM;
;         const int rl0 = wr * 64 + fr, col0 = u.pn * BM + wc * 32 + 4 * fq;
;         f32x4 gv[2][2];
; #pragma unroll
;         for (int bj = 0; bj < 2; ++bj)
; #pragma unroll
;             for (int n = 0; n < 2; ++n) gv[bj][n] = *(const f32x4*)(gate + (size_t)cnd * NMOD + col0 + bj * HALF + n * 16) * scale;
; #pragma unroll
;         for (int ai = 0; ai < 2; ++ai)
; #pragma unroll
;             for (int m = 0; m < 4; ++m) { const size_t off = (size_t)(rl0 + ai * HALF + m * 16) * DM + col0;
; #pragma unroll
;                 for (int bj = 0; bj < 2; ++bj)
; #pragma unroll
;                     for (int n = 0; n < 2; ++n) { const f32x4 bs = ldb(bp + off + bj * HALF + n * 16); st4_bf(op + off + bj * HALF + n * 16, bs + gv[bj][n] * acc[ai][bj][m][n]); }
;                 asm volatile("" ::: "memory"); }
;     }
	v_pk_fma_f32 v[42:43], v[42:43], v[138:139], v[228:229]
	v_pk_fma_f32 v[44:45], v[44:45], v[140:141], v[230:231]
	v_cvt_pk_bf16_f32 v42, v42, v43
	s_nop 0
	v_cvt_pk_bf16_f32 v43, v44, v45
	global_store_dwordx2 v[54:55], v[42:43], off offset:32
	global_load_dwordx4 v[228:231], v[158:159], off offset:64
	s_waitcnt vmcnt(14)
	v_pk_fma_f32 v[38:39], v[38:39], v[134:135], v[232:233]
	v_pk_fma_f32 v[40:41], v[40:41], v[136:137], v[234:235]
	v_cvt_pk_bf16_f32 v38, v38, v39
	v_lshl_add_u64 v[42:43], v[180:181], 0, v[148:149]
	v_cvt_pk_bf16_f32 v39, v40, v41
	global_store_dwordx2 v[54:55], v[38:39], off offset:256
	global_load_dwordx4 v[232:235], v[158:159], off offset:512
	v_lshl_add_u64 v[44:45], v[42:43], 2, v[146:147]
	s_waitcnt vmcnt(14)
	v_pk_fma_f32 v[30:31], v[30:31], v[130:131], v[236:237]
	v_pk_fma_f32 v[32:33], v[32:33], v[132:133], v[238:239]
	v_cvt_pk_bf16_f32 v30, v30, v31
	v_lshl_add_u64 v[38:39], v[42:43], 1, s[26:27]
	v_cvt_pk_bf16_f32 v31, v32, v33
	global_store_dwordx2 v[54:55], v[30:31], off offset:288
	global_load_dwordx4 v[236:239], v[158:159], off offset:576
	s_waitcnt vmcnt(14)
	v_pk_fma_f32 v[30:31], v[34:35], v[142:143], v[208:209]
	v_pk_fma_f32 v[32:33], v[36:37], v[144:145], v[210:211]
	v_cvt_pk_bf16_f32 v30, v30, v31
	s_nop 0
	v_cvt_pk_bf16_f32 v31, v32, v33
	global_store_dwordx2 v[38:39], v[30:31], off
	s_waitcnt vmcnt(13)
	v_pk_fma_f32 v[26:27], v[26:27], v[138:139], v[212:213]
	v_pk_fma_f32 v[28:29], v[28:29], v[140:141], v[214:215]
	v_cvt_pk_bf16_f32 v26, v26, v27
	s_nop 0
	v_cvt_pk_bf16_f32 v27, v28, v29
	global_store_dwordx2 v[38:39], v[26:27], off offset:32
	s_waitcnt vmcnt(12)
	v_pk_fma_f32 v[22:23], v[22:23], v[134:135], v[216:217]
	v_pk_fma_f32 v[24:25], v[24:25], v[136:137], v[218:219]
	v_cvt_pk_bf16_f32 v22, v22, v23
	v_lshl_add_u64 v[26:27], v[182:183], 0, v[148:149]
	v_cvt_pk_bf16_f32 v23, v24, v25
	global_store_dwordx2 v[38:39], v[22:23], off offset:256
	v_lshl_add_u64 v[28:29], v[26:27], 2, v[146:147]
	s_waitcnt vmcnt(11)
	v_pk_fma_f32 v[14:15], v[14:15], v[130:131], v[220:221]
	v_pk_fma_f32 v[16:17], v[16:17], v[132:133], v[222:223]
	v_cvt_pk_bf16_f32 v14, v14, v15
	v_lshl_add_u64 v[22:23], v[26:27], 1, s[26:27]
	v_cvt_pk_bf16_f32 v15, v16, v17
	global_store_dwordx2 v[38:39], v[14:15], off offset:288
	s_waitcnt vmcnt(10)
	v_pk_fma_f32 v[14:15], v[18:19], v[142:143], v[224:225]
	v_pk_fma_f32 v[16:17], v[20:21], v[144:145], v[226:227]
	v_cvt_pk_bf16_f32 v14, v14, v15
	s_nop 0
	v_cvt_pk_bf16_f32 v15, v16, v17
	global_store_dwordx2 v[22:23], v[14:15], off
	s_waitcnt vmcnt(9)
	v_pk_fma_f32 v[10:11], v[10:11], v[138:139], v[228:229]
	v_pk_fma_f32 v[12:13], v[12:13], v[140:141], v[230:231]
	v_cvt_pk_bf16_f32 v10, v10, v11
	s_nop 0
	v_cvt_pk_bf16_f32 v11, v12, v13
	global_store_dwordx2 v[22:23], v[10:11], off offset:32
	s_waitcnt vmcnt(8)
	v_pk_fma_f32 v[6:7], v[6:7], v[134:135], v[232:233]
	v_pk_fma_f32 v[8:9], v[8:9], v[136:137], v[234:235]
	v_cvt_pk_bf16_f32 v6, v6, v7
	s_nop 0
	v_cvt_pk_bf16_f32 v7, v8, v9
	global_store_dwordx2 v[22:23], v[6:7], off offset:256
	s_waitcnt vmcnt(7)
	v_pk_fma_f32 v[2:3], v[2:3], v[130:131], v[236:237]
	v_pk_fma_f32 v[4:5], v[4:5], v[132:133], v[238:239]
	v_cvt_pk_bf16_f32 v2, v2, v3
	s_nop 0
	v_cvt_pk_bf16_f32 v3, v4, v5
	global_store_dwordx2 v[22:23], v[2:3], off offset:288
	s_cbranch_vccnz .LBB0_1191
	s_andn2_b64 vcc, exec, s[2:3]
	s_cbranch_vccnz .LBB0_1190
	s_barrier
	s_branch .LBB0_1190

; __device__ __forceinline__ unsigned cvt4_fp8(float a, float b, float c, float d) { int w = 0; w = __builtin_amdgcn_cvt_pk_fp8_f32(clamp448(a), clamp448(b), w, false); w = __builtin_amdgcn_cvt_pk_fp8_f32(clamp448(c), clamp448(d), w, true); return (unsigned)w; }
; __device__ __forceinline__ float siluf_(float x) { return x * sigmoidf_(x); }
; __device__ __forceinline__ u32x4 pack8(const f32x4 a, const f32x4 b) { u32x4 w; w.x = cvt_pk_bf16(a[0], a[1]); w.y = cvt_pk_bf16(a[2], a[3]); w.z = cvt_pk_bf16(b[0], b[1]); w.w = cvt_pk_bf16(b[2], b[3]); return w; }
;     __device__ __forceinline__ void operator()(const AccT& acc, const Unit& u, int wr, int wc, int fr, int fq) const {
;         const int row0 = u.orow0 + wr * 64 + fr, cb = u.pn * 128 + wc * 32 + 8 * fq, nb = u.pn * 256 + wc * 32 + 8 * fq;
;         f32x4 cg0 = *(const f32x4*)(cmax + nb) * (1.0f / 127.0f), cg1 = *(const f32x4*)(cmax + nb + 4) * (1.0f / 127.0f), cu0 = *(const f32x4*)(cmax + nb + 128) * (1.0f / 127.0f), cu1 = *(const f32x4*)(cmax + nb + 132) * (1.0f / 127.0f);
; #pragma unroll
;         for (int ai = 0; ai < 2; ++ai)
; #pragma unroll
;             for (int m = 0; m < 4; ++m) { const int row = row0 + ai * HALF + m * 16; const float rs = rsc[row]; f32x4 z0, z1;
;                 const i32x4v g0 = __builtin_bit_cast(i32x4v, acc[ai][0][m][0]), g1 = __builtin_bit_cast(i32x4v, acc[ai][0][m][1]), u0 = __builtin_bit_cast(i32x4v, acc[ai][1][m][0]), u1 = __builtin_bit_cast(i32x4v, acc[ai][1][m][1]);
; #pragma unroll
;                 for (int j = 0; j < 4; ++j) { z0[j] = siluf_((float)g0[j] * (rs * cg0[j])) * ((float)u0[j] * (rs * cu0[j])); z1[j] = siluf_((float)g1[j] * (rs * cg1[j])) * ((float)u1[j] * (rs * cu1[j])); }
;                 if (sout8 > 0.f) { u32x2 w; w.x = cvt4_fp8(z0[0] * sout8, z0[1] * sout8, z0[2] * sout8, z0[3] * sout8); w.y = cvt4_fp8(z1[0] * sout8, z1[1] * sout8, z1[2] * sout8, z1[3] * sout8); *(u32x2*)((unsigned char*)O + (size_t)row * ldo + cb) = w; }
;                 else *(u32x4*)(O + (size_t)row * ldo + cb) = pack8(z0, z1);
;                 __builtin_amdgcn_sched_barrier(0); }
.LBB0_1420:
	v_lshl_or_b32 v130, s63, 8, v177
	v_ashrrev_i32_e32 v131, 31, v130
	v_lshl_add_u64 v[130:131], v[130:131], 2, s[16:17]
	v_add_u32_e32 v132, s62, v175
	global_load_dwordx4 v[136:139], v[130:131], off offset:512
	global_load_dwordx4 v[140:143], v[130:131], off
	global_load_dwordx4 v[144:147], v[130:131], off offset:528
	global_load_dwordx4 v[148:151], v[130:131], off offset:16
	v_ashrrev_i32_e32 v133, 31, v132
	v_lshl_add_u64 v[134:135], v[132:133], 2, s[14:15]
	global_load_dword v152, v[134:135], off
	global_load_dword v211, v[134:135], off offset:64
	global_load_dword v212, v[134:135], off offset:128
	global_load_dword v213, v[134:135], off offset:192
	global_load_dword v214, v[134:135], off offset:512
	global_load_dword v215, v[134:135], off offset:576
	global_load_dword v216, v[134:135], off offset:640
	global_load_dword v217, v[134:135], off offset:704
	v_cvt_f32_i32_e32 v155, v126
	v_cvt_f32_i32_e32 v154, v118
	v_cvt_f32_i32_e32 v157, v122
	v_cvt_f32_i32_e32 v156, v114
	v_cvt_f32_i32_e32 v159, v127
	v_cvt_f32_i32_e32 v158, v119
	v_cvt_f32_i32_e32 v161, v123
	v_cvt_f32_i32_e32 v160, v115
	v_cvt_f32_i32_e32 v183, v128
	v_cvt_f32_i32_e32 v182, v120
	v_cvt_f32_i32_e32 v184, v116
	v_cvt_f32_i32_e32 v188, v117
	v_cvt_f32_i32_e32 v186, v121
	v_cvt_f32_i32_e32 v185, v124
	v_cvt_f32_i32_e32 v189, v125
	v_cvt_f32_i32_e32 v187, v129
	v_lshl_or_b32 v130, s63, 7, v177
	v_ashrrev_i32_e32 v131, 31, v130
	s_waitcnt vmcnt(0)
	v_mov_b32_e32 v114, v136
	v_mov_b32_e32 v115, v140
	v_mov_b32_e32 v116, v144
	v_mov_b32_e32 v117, v148
	v_mov_b32_e32 v140, v137
	v_mov_b32_e32 v148, v145
	v_mov_b32_e32 v122, v138
	v_mov_b32_e32 v123, v142
	v_pk_mul_f32 v[114:115], v[114:115], s[24:25] op_sel_hi:[1,0]
	v_pk_mul_f32 v[116:117], v[116:117], s[24:25] op_sel_hi:[1,0]
	v_mov_b32_e32 v142, v139
	v_pk_mul_f32 v[118:119], v[140:141], s[24:25] op_sel_hi:[1,0]
	v_pk_mul_f32 v[120:121], v[148:149], s[24:25] op_sel_hi:[1,0]
	v_pk_mul_f32 v[122:123], v[122:123], s[24:25] op_sel_hi:[1,0]
	v_pk_mul_f32 v[136:137], v[114:115], v[152:153] op_sel_hi:[1,0]
	v_pk_mul_f32 v[138:139], v[152:153], v[116:117] op_sel_hi:[0,1]
	v_mov_b32_e32 v124, v146
	v_mov_b32_e32 v125, v150
	v_mov_b32_e32 v150, v147
	v_pk_mul_f32 v[126:127], v[142:143], s[24:25] op_sel_hi:[1,0]
	v_pk_mul_f32 v[140:141], v[118:119], v[152:153] op_sel_hi:[1,0]
	v_pk_mul_f32 v[142:143], v[152:153], v[120:121] op_sel_hi:[0,1]
	v_pk_mul_f32 v[144:145], v[122:123], v[152:153] op_sel_hi:[1,0]
	v_pk_mul_f32 v[136:137], v[136:137], v[154:155]
	v_pk_mul_f32 v[138:139], v[138:139], v[156:157]
	v_pk_mul_f32 v[124:125], v[124:125], s[24:25] op_sel_hi:[1,0]
	v_pk_mul_f32 v[128:129], v[150:151], s[24:25] op_sel_hi:[1,0]
	v_pk_mul_f32 v[140:141], v[140:141], v[158:159]
	v_pk_mul_f32 v[142:143], v[142:143], v[160:161]
	v_pk_mul_f32 v[144:145], v[144:145], v[182:183]
	v_mul_f32_e32 v133, 0xbfb8aa3b, v137
	v_mul_f32_e32 v150, 0xbfb8aa3b, v139
	v_pk_mul_f32 v[146:147], v[152:153], v[124:125] op_sel_hi:[0,1]
	v_pk_mul_f32 v[148:149], v[126:127], v[152:153] op_sel_hi:[1,0]
	v_mul_f32_e32 v151, 0xbfb8aa3b, v141
	v_mul_f32_e32 v153, 0xbfb8aa3b, v143
	v_mul_f32_e32 v154, 0xbfb8aa3b, v145
	v_exp_f32_e32 v133, v133
	v_exp_f32_e32 v150, v150
	v_exp_f32_e32 v151, v151
	v_exp_f32_e32 v153, v153
	v_exp_f32_e32 v154, v154
	v_add_f32_e32 v133, 1.0, v133
	v_add_f32_e32 v150, 1.0, v150
	v_add_f32_e32 v151, 1.0, v151
	v_add_f32_e32 v153, 1.0, v153
	v_add_f32_e32 v154, 1.0, v154
	v_rcp_f32_e32 v133, v133
	v_rcp_f32_e32 v150, v150
	v_rcp_f32_e32 v151, v151
	v_rcp_f32_e32 v153, v153
	v_rcp_f32_e32 v154, v154
	v_mul_f32_e32 v133, v137, v133
	v_mul_f32_e32 v137, v139, v150
	v_mul_f32_e32 v139, v141, v151
	v_mul_f32_e32 v141, v143, v153
	v_mul_f32_e32 v143, v145, v154
	v_mul_f32_e32 v133, v136, v133
	v_mul_f32_e32 v145, v138, v137
	v_pk_mul_f32 v[136:137], v[152:153], v[128:129] op_sel_hi:[0,1]
	v_pk_mul_f32 v[136:137], v[136:137], v[188:189]
	v_mul_f32_e32 v138, v140, v139
	v_mul_f32_e32 v139, v142, v141
	v_mul_f32_e32 v141, 0xbfb8aa3b, v137
	v_exp_f32_e32 v141, v141
	v_pk_mul_f32 v[148:149], v[148:149], v[186:187]
	v_pk_mul_f32 v[146:147], v[146:147], v[184:185]
	v_mul_f32_e32 v156, 0xbfb8aa3b, v149
	v_exp_f32_e32 v156, v156
	v_add_f32_e32 v141, 1.0, v141
	v_rcp_f32_e32 v141, v141
	v_mul_f32_e32 v140, v144, v143
	v_add_f32_e32 v143, 1.0, v156
	v_mul_f32_e32 v155, 0xbfb8aa3b, v147
	v_rcp_f32_e32 v143, v143
	v_exp_f32_e32 v155, v155
	v_mul_f32_e32 v137, v137, v141
	v_mul_f32_e32 v136, v136, v137
	v_mul_f32_e32 v133, 4.0, v133
	v_mul_f32_e32 v137, 4.0, v138
	v_med3_f32 v133, v133, s58, v181
	v_med3_f32 v137, v137, s58, v181
	v_mov_b32_e32 v138, v163
	v_mul_f32_e32 v143, v149, v143
	v_cvt_pk_fp8_f32 v138, v133, v137
	v_add_f32_e32 v155, 1.0, v155
	v_mul_f32_e32 v143, v148, v143
	v_rcp_f32_e32 v155, v155
	v_mul_f32_e32 v140, 4.0, v140
	v_mul_f32_e32 v133, 4.0, v143
	v_med3_f32 v137, v140, s58, v181
	v_med3_f32 v133, v133, s58, v181
	v_cvt_pk_fp8_f32 v138, v137, v133 op_sel:[0,0,1]
	v_mul_f32_e32 v133, 4.0, v145
	v_mul_f32_e32 v137, 4.0, v139
	v_med3_f32 v133, v133, s58, v181
	v_med3_f32 v137, v137, s58, v181
	v_mov_b32_e32 v139, v163
	v_mul_f32_e32 v142, v147, v155
	v_cvt_pk_fp8_f32 v139, v133, v137
	v_mul_f32_e32 v142, v146, v142
	v_mul_f32_e32 v140, 4.0, v142
	v_mul_f32_e32 v133, 4.0, v136
	v_med3_f32 v136, v140, s58, v181
	v_med3_f32 v133, v133, s58, v181
	v_cvt_pk_fp8_f32 v139, v136, v133 op_sel:[0,0,1]
	v_mov_b64_e32 v[136:137], s[6:7]
	v_mad_i64_i32 v[140:141], s[34:35], v132, s59, v[136:137]
	v_lshl_add_u64 v[140:141], v[140:141], 0, v[130:131]
	global_store_dwordx2 v[140:141], v[138:139], off
	v_mov_b32_e32 v138, v211
	v_cvt_f32_i32_e32 v141, v110
; __device__ __forceinline__ unsigned cvt4_fp8(float a, float b, float c, float d) { int w = 0; w = __builtin_amdgcn_cvt_pk_fp8_f32(clamp448(a), clamp448(b), w, false); w = __builtin_amdgcn_cvt_pk_fp8_f32(clamp448(c), clamp448(d), w, true); return (unsigned)w; }
; __device__ __forceinline__ float siluf_(float x) { return x * sigmoidf_(x); }
; __device__ __forceinline__ u32x4 pack8(const f32x4 a, const f32x4 b) { u32x4 w; w.x = cvt_pk_bf16(a[0], a[1]); w.y = cvt_pk_bf16(a[2], a[3]); w.z = cvt_pk_bf16(b[0], b[1]); w.w = cvt_pk_bf16(b[2], b[3]); return w; }
;     __device__ __forceinline__ void operator()(const AccT& acc, const Unit& u, int wr, int wc, int fr, int fq) const {
;         const int row0 = u.orow0 + wr * 64 + fr, cb = u.pn * 128 + wc * 32 + 8 * fq, nb = u.pn * 256 + wc * 32 + 8 * fq;
;         f32x4 cg0 = *(const f32x4*)(cmax + nb) * (1.0f / 127.0f), cg1 = *(const f32x4*)(cmax + nb + 4) * (1.0f / 127.0f), cu0 = *(const f32x4*)(cmax + nb + 128) * (1.0f / 127.0f), cu1 = *(const f32x4*)(cmax + nb + 132) * (1.0f / 127.0f);
; #pragma unroll
;         for (int ai = 0; ai < 2; ++ai)
; #pragma unroll
;             for (int m = 0; m < 4; ++m) { const int row = row0 + ai * HALF + m * 16; const float rs = rsc[row]; f32x4 z0, z1;
;                 const i32x4v g0 = __builtin_bit_cast(i32x4v, acc[ai][0][m][0]), g1 = __builtin_bit_cast(i32x4v, acc[ai][0][m][1]), u0 = __builtin_bit_cast(i32x4v, acc[ai][1][m][0]), u1 = __builtin_bit_cast(i32x4v, acc[ai][1][m][1]);
; #pragma unroll
;                 for (int j = 0; j < 4; ++j) { z0[j] = siluf_((float)g0[j] * (rs * cg0[j])) * ((float)u0[j] * (rs * cu0[j])); z1[j] = siluf_((float)g1[j] * (rs * cg1[j])) * ((float)u1[j] * (rs * cu1[j])); }
;                 if (sout8 > 0.f) { u32x2 w; w.x = cvt4_fp8(z0[0] * sout8, z0[1] * sout8, z0[2] * sout8, z0[3] * sout8); w.y = cvt4_fp8(z1[0] * sout8, z1[1] * sout8, z1[2] * sout8, z1[3] * sout8); *(u32x2*)((unsigned char*)O + (size_t)row * ldo + cb) = w; }
;                 else *(u32x4*)(O + (size_t)row * ldo + cb) = pack8(z0, z1);
;                 __builtin_amdgcn_sched_barrier(0); }
	v_cvt_f32_i32_e32 v140, v102
	v_cvt_f32_i32_e32 v111, v111
	v_cvt_f32_i32_e32 v110, v103
	v_cvt_f32_i32_e32 v143, v106
	v_cvt_f32_i32_e32 v142, v98
	v_cvt_f32_i32_e32 v103, v107
	v_cvt_f32_i32_e32 v102, v99
	v_cvt_f32_i32_e32 v99, v112
	v_cvt_f32_i32_e32 v98, v104
	v_cvt_f32_i32_e32 v107, v108
	v_cvt_f32_i32_e32 v106, v100
	v_cvt_f32_i32_e32 v112, v105
	v_cvt_f32_i32_e32 v105, v109
	v_cvt_f32_i32_e32 v104, v101
	v_cvt_f32_i32_e32 v113, v113
	v_mov_b32_e32 v100, v163
	v_mov_b32_e32 v101, v163
	v_add_u32_e32 v133, 16, v132
	v_pk_mul_f32 v[108:109], v[114:115], v[138:139] op_sel_hi:[1,0]
	v_pk_mul_f32 v[146:147], v[118:119], v[138:139] op_sel_hi:[1,0]
	v_pk_mul_f32 v[144:145], v[116:117], v[138:139] op_sel_hi:[1,0]
	v_pk_mul_f32 v[148:149], v[120:121], v[138:139] op_sel_hi:[1,0]
	v_pk_mul_f32 v[150:151], v[122:123], v[138:139] op_sel_hi:[1,0]
	v_pk_mul_f32 v[152:153], v[124:125], v[138:139] op_sel_hi:[1,0]
	v_pk_mul_f32 v[154:155], v[126:127], v[138:139] op_sel_hi:[1,0]
	v_pk_mul_f32 v[138:139], v[128:129], v[138:139] op_sel_hi:[1,0]
	v_pk_mul_f32 v[108:109], v[108:109], v[140:141]
	v_pk_mul_f32 v[110:111], v[146:147], v[110:111]
	v_pk_mul_f32 v[140:141], v[144:145], v[142:143]
	v_pk_mul_f32 v[102:103], v[148:149], v[102:103]
	v_pk_mul_f32 v[98:99], v[150:151], v[98:99]
	v_pk_mul_f32 v[106:107], v[152:153], v[106:107]
	v_pk_mul_f32 v[104:105], v[138:139], v[104:105]
	v_mul_f32_e32 v138, 0xbfb8aa3b, v109
	v_mul_f32_e32 v142, 0xbfb8aa3b, v111
	v_mul_f32_e32 v139, 0xbfb8aa3b, v141
	v_mul_f32_e32 v143, 0xbfb8aa3b, v103
	v_mul_f32_e32 v144, 0xbfb8aa3b, v99
	v_mul_f32_e32 v145, 0xbfb8aa3b, v107
	v_mul_f32_e32 v147, 0xbfb8aa3b, v105
	v_exp_f32_e32 v138, v138
	v_exp_f32_e32 v142, v142
	v_exp_f32_e32 v139, v139
	v_exp_f32_e32 v143, v143
	v_exp_f32_e32 v144, v144
	v_exp_f32_e32 v145, v145
	v_exp_f32_e32 v147, v147
	v_pk_mul_f32 v[112:113], v[154:155], v[112:113]
	v_add_f32_e32 v138, 1.0, v138
	v_mul_f32_e32 v146, 0xbfb8aa3b, v113
	v_exp_f32_e32 v146, v146
	v_add_f32_e32 v142, 1.0, v142
	v_add_f32_e32 v139, 1.0, v139
	v_add_f32_e32 v143, 1.0, v143
	v_add_f32_e32 v144, 1.0, v144
	v_add_f32_e32 v145, 1.0, v145
	v_add_f32_e32 v147, 1.0, v147
	v_rcp_f32_e32 v138, v138
	v_rcp_f32_e32 v142, v142
	v_rcp_f32_e32 v139, v139
	v_rcp_f32_e32 v143, v143
	v_rcp_f32_e32 v144, v144
	v_rcp_f32_e32 v145, v145
	v_rcp_f32_e32 v147, v147
	v_add_f32_e32 v146, 1.0, v146
	v_rcp_f32_e32 v146, v146
	v_mul_f32_e32 v109, v109, v138
	v_mul_f32_e32 v111, v111, v142
	v_mul_f32_e32 v138, v141, v139
	v_mul_f32_e32 v103, v103, v143
	v_mul_f32_e32 v99, v99, v144
	v_mul_f32_e32 v107, v107, v145
	v_mul_f32_e32 v105, v105, v147
	v_mul_f32_e32 v108, v108, v109
	v_mul_f32_e32 v110, v110, v111
	v_mul_f32_e32 v109, v140, v138
	v_mul_f32_e32 v102, v102, v103
	v_mul_f32_e32 v98, v98, v99
	v_mul_f32_e32 v99, v106, v107
	v_mul_f32_e32 v104, v104, v105
	v_mul_f32_e32 v105, 4.0, v108
	v_mul_f32_e32 v106, 4.0, v110
	v_mul_f32_e32 v107, 4.0, v109
	v_mul_f32_e32 v102, 4.0, v102
	v_med3_f32 v105, v105, s58, v181
	v_med3_f32 v106, v106, s58, v181
	v_mul_f32_e32 v113, v113, v146
	v_cvt_pk_fp8_f32 v100, v105, v106
	v_med3_f32 v105, v107, s58, v181
	v_med3_f32 v102, v102, s58, v181
	v_mul_f32_e32 v103, v112, v113
	v_cvt_pk_fp8_f32 v101, v105, v102
	v_mul_f32_e32 v98, 4.0, v98
	v_mul_f32_e32 v103, 4.0, v103
	v_mul_f32_e32 v99, 4.0, v99
	v_mul_f32_e32 v104, 4.0, v104
	v_med3_f32 v98, v98, s58, v181
	v_med3_f32 v103, v103, s58, v181
	v_cvt_pk_fp8_f32 v100, v98, v103 op_sel:[0,0,1]
	v_med3_f32 v98, v99, s58, v181
	v_med3_f32 v99, v104, s58, v181
	v_cvt_pk_fp8_f32 v101, v98, v99 op_sel:[0,0,1]
	v_mad_i64_i32 v[98:99], s[34:35], v133, s59, v[136:137]
	v_lshl_add_u64 v[98:99], v[98:99], 0, v[130:131]
	global_store_dwordx2 v[98:99], v[100:101], off
	v_mov_b32_e32 v98, v212
	v_cvt_f32_i32_e32 v101, v94
	v_cvt_f32_i32_e32 v100, v86
	v_cvt_f32_i32_e32 v95, v95
	v_cvt_f32_i32_e32 v94, v87
	v_cvt_f32_i32_e32 v103, v90
	v_cvt_f32_i32_e32 v102, v82
	v_cvt_f32_i32_e32 v87, v91
	v_cvt_f32_i32_e32 v86, v83
	v_cvt_f32_i32_e32 v83, v96
	v_cvt_f32_i32_e32 v82, v88
	v_cvt_f32_i32_e32 v91, v92
	v_cvt_f32_i32_e32 v90, v84
	v_cvt_f32_i32_e32 v96, v89
	v_cvt_f32_i32_e32 v89, v93
	v_cvt_f32_i32_e32 v88, v85
	v_cvt_f32_i32_e32 v97, v97
	v_mov_b32_e32 v84, v163
	v_mov_b32_e32 v85, v163
	v_add_u32_e32 v133, 32, v132
	v_pk_mul_f32 v[92:93], v[114:115], v[98:99] op_sel_hi:[1,0]
	v_pk_mul_f32 v[106:107], v[118:119], v[98:99] op_sel_hi:[1,0]
	v_pk_mul_f32 v[104:105], v[116:117], v[98:99] op_sel_hi:[1,0]
	v_pk_mul_f32 v[108:109], v[120:121], v[98:99] op_sel_hi:[1,0]
	v_pk_mul_f32 v[110:111], v[122:123], v[98:99] op_sel_hi:[1,0]
	v_pk_mul_f32 v[112:113], v[124:125], v[98:99] op_sel_hi:[1,0]
	v_pk_mul_f32 v[138:139], v[126:127], v[98:99] op_sel_hi:[1,0]
	v_pk_mul_f32 v[98:99], v[128:129], v[98:99] op_sel_hi:[1,0]
	v_pk_mul_f32 v[92:93], v[92:93], v[100:101]
	v_pk_mul_f32 v[94:95], v[106:107], v[94:95]
	v_pk_mul_f32 v[100:101], v[104:105], v[102:103]
	v_pk_mul_f32 v[86:87], v[108:109], v[86:87]
	v_pk_mul_f32 v[82:83], v[110:111], v[82:83]
	v_pk_mul_f32 v[90:91], v[112:113], v[90:91]
	v_pk_mul_f32 v[88:89], v[98:99], v[88:89]
	v_mul_f32_e32 v98, 0xbfb8aa3b, v93
	v_mul_f32_e32 v102, 0xbfb8aa3b, v95
	v_mul_f32_e32 v99, 0xbfb8aa3b, v101
	v_mul_f32_e32 v103, 0xbfb8aa3b, v87
	v_mul_f32_e32 v104, 0xbfb8aa3b, v83
	v_mul_f32_e32 v105, 0xbfb8aa3b, v91
	v_mul_f32_e32 v107, 0xbfb8aa3b, v89
	v_exp_f32_e32 v98, v98
	v_exp_f32_e32 v102, v102
	v_exp_f32_e32 v99, v99
	v_exp_f32_e32 v103, v103
	v_exp_f32_e32 v104, v104
	v_exp_f32_e32 v105, v105
	v_exp_f32_e32 v107, v107
	v_pk_mul_f32 v[96:97], v[138:139], v[96:97]
	v_add_f32_e32 v98, 1.0, v98
; __device__ __forceinline__ unsigned cvt4_fp8(float a, float b, float c, float d) { int w = 0; w = __builtin_amdgcn_cvt_pk_fp8_f32(clamp448(a), clamp448(b), w, false); w = __builtin_amdgcn_cvt_pk_fp8_f32(clamp448(c), clamp448(d), w, true); return (unsigned)w; }
; __device__ __forceinline__ float siluf_(float x) { return x * sigmoidf_(x); }
; __device__ __forceinline__ u32x4 pack8(const f32x4 a, const f32x4 b) { u32x4 w; w.x = cvt_pk_bf16(a[0], a[1]); w.y = cvt_pk_bf16(a[2], a[3]); w.z = cvt_pk_bf16(b[0], b[1]); w.w = cvt_pk_bf16(b[2], b[3]); return w; }
;     __device__ __forceinline__ void operator()(const AccT& acc, const Unit& u, int wr, int wc, int fr, int fq) const {
;         const int row0 = u.orow0 + wr * 64 + fr, cb = u.pn * 128 + wc * 32 + 8 * fq, nb = u.pn * 256 + wc * 32 + 8 * fq;
;         f32x4 cg0 = *(const f32x4*)(cmax + nb) * (1.0f / 127.0f), cg1 = *(const f32x4*)(cmax + nb + 4) * (1.0f / 127.0f), cu0 = *(const f32x4*)(cmax + nb + 128) * (1.0f / 127.0f), cu1 = *(const f32x4*)(cmax + nb + 132) * (1.0f / 127.0f);
; #pragma unroll
;         for (int ai = 0; ai < 2; ++ai)
; #pragma unroll
;             for (int m = 0; m < 4; ++m) { const int row = row0 + ai * HALF + m * 16; const float rs = rsc[row]; f32x4 z0, z1;
;                 const i32x4v g0 = __builtin_bit_cast(i32x4v, acc[ai][0][m][0]), g1 = __builtin_bit_cast(i32x4v, acc[ai][0][m][1]), u0 = __builtin_bit_cast(i32x4v, acc[ai][1][m][0]), u1 = __builtin_bit_cast(i32x4v, acc[ai][1][m][1]);
; #pragma unroll
;                 for (int j = 0; j < 4; ++j) { z0[j] = siluf_((float)g0[j] * (rs * cg0[j])) * ((float)u0[j] * (rs * cu0[j])); z1[j] = siluf_((float)g1[j] * (rs * cg1[j])) * ((float)u1[j] * (rs * cu1[j])); }
;                 if (sout8 > 0.f) { u32x2 w; w.x = cvt4_fp8(z0[0] * sout8, z0[1] * sout8, z0[2] * sout8, z0[3] * sout8); w.y = cvt4_fp8(z1[0] * sout8, z1[1] * sout8, z1[2] * sout8, z1[3] * sout8); *(u32x2*)((unsigned char*)O + (size_t)row * ldo + cb) = w; }
;                 else *(u32x4*)(O + (size_t)row * ldo + cb) = pack8(z0, z1);
;                 __builtin_amdgcn_sched_barrier(0); }
	v_mul_f32_e32 v106, 0xbfb8aa3b, v97
	v_exp_f32_e32 v106, v106
	v_add_f32_e32 v102, 1.0, v102
	v_add_f32_e32 v99, 1.0, v99
	v_add_f32_e32 v103, 1.0, v103
	v_add_f32_e32 v104, 1.0, v104
	v_add_f32_e32 v105, 1.0, v105
	v_add_f32_e32 v107, 1.0, v107
	v_rcp_f32_e32 v98, v98
	v_rcp_f32_e32 v102, v102
	v_rcp_f32_e32 v99, v99
	v_rcp_f32_e32 v103, v103
	v_rcp_f32_e32 v104, v104
	v_rcp_f32_e32 v105, v105
	v_rcp_f32_e32 v107, v107
	v_add_f32_e32 v106, 1.0, v106
	v_rcp_f32_e32 v106, v106
	v_mul_f32_e32 v93, v93, v98
	v_mul_f32_e32 v95, v95, v102
	v_mul_f32_e32 v98, v101, v99
	v_mul_f32_e32 v87, v87, v103
	v_mul_f32_e32 v83, v83, v104
	v_mul_f32_e32 v91, v91, v105
	v_mul_f32_e32 v89, v89, v107
	v_mul_f32_e32 v92, v92, v93
	v_mul_f32_e32 v94, v94, v95
	v_mul_f32_e32 v93, v100, v98
	v_mul_f32_e32 v86, v86, v87
	v_mul_f32_e32 v82, v82, v83
	v_mul_f32_e32 v83, v90, v91
	v_mul_f32_e32 v88, v88, v89
	v_mul_f32_e32 v89, 4.0, v92
	v_mul_f32_e32 v90, 4.0, v94
	v_mul_f32_e32 v91, 4.0, v93
	v_mul_f32_e32 v86, 4.0, v86
	v_med3_f32 v89, v89, s58, v181
	v_med3_f32 v90, v90, s58, v181
	v_mul_f32_e32 v97, v97, v106
	v_cvt_pk_fp8_f32 v84, v89, v90
	v_med3_f32 v89, v91, s58, v181
	v_med3_f32 v86, v86, s58, v181
	v_mul_f32_e32 v87, v96, v97
	v_cvt_pk_fp8_f32 v85, v89, v86
	v_mul_f32_e32 v82, 4.0, v82
	v_mul_f32_e32 v87, 4.0, v87
	v_mul_f32_e32 v83, 4.0, v83
	v_mul_f32_e32 v88, 4.0, v88
	v_med3_f32 v82, v82, s58, v181
	v_med3_f32 v87, v87, s58, v181
	v_cvt_pk_fp8_f32 v84, v82, v87 op_sel:[0,0,1]
	v_med3_f32 v82, v83, s58, v181
	v_med3_f32 v83, v88, s58, v181
	v_cvt_pk_fp8_f32 v85, v82, v83 op_sel:[0,0,1]
	v_mad_i64_i32 v[82:83], s[34:35], v133, s59, v[136:137]
	v_lshl_add_u64 v[82:83], v[82:83], 0, v[130:131]
	global_store_dwordx2 v[82:83], v[84:85], off
	v_mov_b32_e32 v82, v213
	v_cvt_f32_i32_e32 v85, v78
	v_cvt_f32_i32_e32 v84, v70
	v_cvt_f32_i32_e32 v79, v79
	v_cvt_f32_i32_e32 v78, v71
	v_cvt_f32_i32_e32 v87, v74
	v_cvt_f32_i32_e32 v86, v66
	v_cvt_f32_i32_e32 v71, v75
	v_cvt_f32_i32_e32 v70, v67
	v_cvt_f32_i32_e32 v67, v80
	v_cvt_f32_i32_e32 v66, v72
	v_cvt_f32_i32_e32 v75, v76
	v_cvt_f32_i32_e32 v74, v68
	v_cvt_f32_i32_e32 v80, v73
	v_cvt_f32_i32_e32 v73, v77
	v_cvt_f32_i32_e32 v72, v69
	v_cvt_f32_i32_e32 v81, v81
	v_mov_b32_e32 v68, v163
	v_mov_b32_e32 v69, v163
	v_add_u32_e32 v100, 48, v132
	v_pk_mul_f32 v[76:77], v[114:115], v[82:83] op_sel_hi:[1,0]
	v_pk_mul_f32 v[90:91], v[118:119], v[82:83] op_sel_hi:[1,0]
	v_pk_mul_f32 v[88:89], v[116:117], v[82:83] op_sel_hi:[1,0]
	v_pk_mul_f32 v[92:93], v[120:121], v[82:83] op_sel_hi:[1,0]
	v_pk_mul_f32 v[94:95], v[122:123], v[82:83] op_sel_hi:[1,0]
	v_pk_mul_f32 v[96:97], v[124:125], v[82:83] op_sel_hi:[1,0]
	v_pk_mul_f32 v[98:99], v[126:127], v[82:83] op_sel_hi:[1,0]
	v_pk_mul_f32 v[82:83], v[128:129], v[82:83] op_sel_hi:[1,0]
	v_pk_mul_f32 v[76:77], v[76:77], v[84:85]
	v_pk_mul_f32 v[78:79], v[90:91], v[78:79]
	v_pk_mul_f32 v[84:85], v[88:89], v[86:87]
	v_pk_mul_f32 v[70:71], v[92:93], v[70:71]
	v_pk_mul_f32 v[66:67], v[94:95], v[66:67]
	v_pk_mul_f32 v[74:75], v[96:97], v[74:75]
	v_pk_mul_f32 v[72:73], v[82:83], v[72:73]
	v_mul_f32_e32 v82, 0xbfb8aa3b, v77
	v_mul_f32_e32 v86, 0xbfb8aa3b, v79
	v_mul_f32_e32 v83, 0xbfb8aa3b, v85
	v_mul_f32_e32 v87, 0xbfb8aa3b, v71
	v_mul_f32_e32 v88, 0xbfb8aa3b, v67
	v_mul_f32_e32 v89, 0xbfb8aa3b, v75
	v_mul_f32_e32 v91, 0xbfb8aa3b, v73
	v_exp_f32_e32 v82, v82
	v_exp_f32_e32 v86, v86
	v_exp_f32_e32 v83, v83
	v_exp_f32_e32 v87, v87
	v_exp_f32_e32 v88, v88
	v_exp_f32_e32 v89, v89
	v_exp_f32_e32 v91, v91
	v_pk_mul_f32 v[80:81], v[98:99], v[80:81]
	v_add_f32_e32 v82, 1.0, v82
	v_mul_f32_e32 v90, 0xbfb8aa3b, v81
	v_exp_f32_e32 v90, v90
	v_add_f32_e32 v86, 1.0, v86
	v_add_f32_e32 v83, 1.0, v83
	v_add_f32_e32 v87, 1.0, v87
	v_add_f32_e32 v88, 1.0, v88
	v_add_f32_e32 v89, 1.0, v89
	v_add_f32_e32 v91, 1.0, v91
	v_rcp_f32_e32 v82, v82
	v_rcp_f32_e32 v86, v86
	v_rcp_f32_e32 v83, v83
	v_rcp_f32_e32 v87, v87
	v_rcp_f32_e32 v88, v88
	v_rcp_f32_e32 v89, v89
	v_rcp_f32_e32 v91, v91
	v_add_f32_e32 v90, 1.0, v90
	v_rcp_f32_e32 v90, v90
	v_mul_f32_e32 v77, v77, v82
	v_mul_f32_e32 v79, v79, v86
	v_mul_f32_e32 v82, v85, v83
	v_mul_f32_e32 v71, v71, v87
	v_mul_f32_e32 v67, v67, v88
	v_mul_f32_e32 v75, v75, v89
	v_mul_f32_e32 v73, v73, v91
	v_mul_f32_e32 v76, v76, v77
	v_mul_f32_e32 v78, v78, v79
	v_mul_f32_e32 v77, v84, v82
	v_mul_f32_e32 v70, v70, v71
	v_mul_f32_e32 v66, v66, v67
	v_mul_f32_e32 v67, v74, v75
	v_mul_f32_e32 v72, v72, v73
	v_mul_f32_e32 v73, 4.0, v76
	v_mul_f32_e32 v74, 4.0, v78
	v_mul_f32_e32 v75, 4.0, v77
	v_mul_f32_e32 v70, 4.0, v70
	v_med3_f32 v73, v73, s58, v181
	v_med3_f32 v74, v74, s58, v181
	v_mul_f32_e32 v81, v81, v90
	v_cvt_pk_fp8_f32 v68, v73, v74
	v_med3_f32 v73, v75, s58, v181
	v_med3_f32 v70, v70, s58, v181
	v_mul_f32_e32 v71, v80, v81
	v_cvt_pk_fp8_f32 v69, v73, v70
	v_mul_f32_e32 v66, 4.0, v66
	v_mul_f32_e32 v71, 4.0, v71
	v_mul_f32_e32 v67, 4.0, v67
	v_mul_f32_e32 v72, 4.0, v72
	v_med3_f32 v66, v66, s58, v181
	v_med3_f32 v71, v71, s58, v181
	v_cvt_pk_fp8_f32 v68, v66, v71 op_sel:[0,0,1]
	v_med3_f32 v66, v67, s58, v181
	v_med3_f32 v67, v72, s58, v181
	v_cvt_pk_fp8_f32 v69, v66, v67 op_sel:[0,0,1]
	v_mad_i64_i32 v[66:67], s[34:35], v100, s59, v[136:137]
	v_lshl_add_u64 v[66:67], v[66:67], 0, v[130:131]
	global_store_dwordx2 v[66:67], v[68:69], off
	v_mov_b32_e32 v66, v214
	v_cvt_f32_i32_e32 v69, v62
	v_cvt_f32_i32_e32 v68, v54
	v_cvt_f32_i32_e32 v63, v63
	v_cvt_f32_i32_e32 v62, v55
	v_cvt_f32_i32_e32 v71, v58
	v_cvt_f32_i32_e32 v70, v50
	v_cvt_f32_i32_e32 v55, v59
	v_cvt_f32_i32_e32 v54, v51
	v_cvt_f32_i32_e32 v51, v64
	v_cvt_f32_i32_e32 v50, v56
	v_cvt_f32_i32_e32 v59, v60
; __device__ __forceinline__ unsigned cvt4_fp8(float a, float b, float c, float d) { int w = 0; w = __builtin_amdgcn_cvt_pk_fp8_f32(clamp448(a), clamp448(b), w, false); w = __builtin_amdgcn_cvt_pk_fp8_f32(clamp448(c), clamp448(d), w, true); return (unsigned)w; }
; __device__ __forceinline__ float siluf_(float x) { return x * sigmoidf_(x); }
; __device__ __forceinline__ u32x4 pack8(const f32x4 a, const f32x4 b) { u32x4 w; w.x = cvt_pk_bf16(a[0], a[1]); w.y = cvt_pk_bf16(a[2], a[3]); w.z = cvt_pk_bf16(b[0], b[1]); w.w = cvt_pk_bf16(b[2], b[3]); return w; }
;     __device__ __forceinline__ void operator()(const AccT& acc, const Unit& u, int wr, int wc, int fr, int fq) const {
;         const int row0 = u.orow0 + wr * 64 + fr, cb = u.pn * 128 + wc * 32 + 8 * fq, nb = u.pn * 256 + wc * 32 + 8 * fq;
;         f32x4 cg0 = *(const f32x4*)(cmax + nb) * (1.0f / 127.0f), cg1 = *(const f32x4*)(cmax + nb + 4) * (1.0f / 127.0f), cu0 = *(const f32x4*)(cmax + nb + 128) * (1.0f / 127.0f), cu1 = *(const f32x4*)(cmax + nb + 132) * (1.0f / 127.0f);
; #pragma unroll
;         for (int ai = 0; ai < 2; ++ai)
; #pragma unroll
;             for (int m = 0; m < 4; ++m) { const int row = row0 + ai * HALF + m * 16; const float rs = rsc[row]; f32x4 z0, z1;
;                 const i32x4v g0 = __builtin_bit_cast(i32x4v, acc[ai][0][m][0]), g1 = __builtin_bit_cast(i32x4v, acc[ai][0][m][1]), u0 = __builtin_bit_cast(i32x4v, acc[ai][1][m][0]), u1 = __builtin_bit_cast(i32x4v, acc[ai][1][m][1]);
; #pragma unroll
;                 for (int j = 0; j < 4; ++j) { z0[j] = siluf_((float)g0[j] * (rs * cg0[j])) * ((float)u0[j] * (rs * cu0[j])); z1[j] = siluf_((float)g1[j] * (rs * cg1[j])) * ((float)u1[j] * (rs * cu1[j])); }
;                 if (sout8 > 0.f) { u32x2 w; w.x = cvt4_fp8(z0[0] * sout8, z0[1] * sout8, z0[2] * sout8, z0[3] * sout8); w.y = cvt4_fp8(z1[0] * sout8, z1[1] * sout8, z1[2] * sout8, z1[3] * sout8); *(u32x2*)((unsigned char*)O + (size_t)row * ldo + cb) = w; }
;                 else *(u32x4*)(O + (size_t)row * ldo + cb) = pack8(z0, z1);
;                 __builtin_amdgcn_sched_barrier(0); }
	v_cvt_f32_i32_e32 v58, v52
	v_cvt_f32_i32_e32 v64, v57
	v_cvt_f32_i32_e32 v57, v61
	v_cvt_f32_i32_e32 v56, v53
	v_cvt_f32_i32_e32 v65, v65
	v_mov_b32_e32 v52, v163
	v_mov_b32_e32 v53, v163
	v_add_u32_e32 v84, 0x80, v132
	v_pk_mul_f32 v[60:61], v[114:115], v[66:67] op_sel_hi:[1,0]
	v_pk_mul_f32 v[74:75], v[118:119], v[66:67] op_sel_hi:[1,0]
	v_pk_mul_f32 v[72:73], v[116:117], v[66:67] op_sel_hi:[1,0]
	v_pk_mul_f32 v[76:77], v[120:121], v[66:67] op_sel_hi:[1,0]
	v_pk_mul_f32 v[78:79], v[122:123], v[66:67] op_sel_hi:[1,0]
	v_pk_mul_f32 v[80:81], v[124:125], v[66:67] op_sel_hi:[1,0]
	v_pk_mul_f32 v[82:83], v[126:127], v[66:67] op_sel_hi:[1,0]
	v_pk_mul_f32 v[66:67], v[128:129], v[66:67] op_sel_hi:[1,0]
	v_pk_mul_f32 v[60:61], v[60:61], v[68:69]
	v_pk_mul_f32 v[62:63], v[74:75], v[62:63]
	v_pk_mul_f32 v[68:69], v[72:73], v[70:71]
	v_pk_mul_f32 v[54:55], v[76:77], v[54:55]
	v_pk_mul_f32 v[50:51], v[78:79], v[50:51]
	v_pk_mul_f32 v[58:59], v[80:81], v[58:59]
	v_pk_mul_f32 v[56:57], v[66:67], v[56:57]
	v_mul_f32_e32 v66, 0xbfb8aa3b, v61
	v_mul_f32_e32 v70, 0xbfb8aa3b, v63
	v_mul_f32_e32 v67, 0xbfb8aa3b, v69
	v_mul_f32_e32 v71, 0xbfb8aa3b, v55
	v_mul_f32_e32 v72, 0xbfb8aa3b, v51
	v_mul_f32_e32 v73, 0xbfb8aa3b, v59
	v_mul_f32_e32 v75, 0xbfb8aa3b, v57
	v_exp_f32_e32 v66, v66
	v_exp_f32_e32 v70, v70
	v_exp_f32_e32 v67, v67
	v_exp_f32_e32 v71, v71
	v_exp_f32_e32 v72, v72
	v_exp_f32_e32 v73, v73
	v_exp_f32_e32 v75, v75
	v_pk_mul_f32 v[64:65], v[82:83], v[64:65]
	v_add_f32_e32 v66, 1.0, v66
	v_mul_f32_e32 v74, 0xbfb8aa3b, v65
	v_exp_f32_e32 v74, v74
	v_add_f32_e32 v70, 1.0, v70
	v_add_f32_e32 v67, 1.0, v67
	v_add_f32_e32 v71, 1.0, v71
	v_add_f32_e32 v72, 1.0, v72
	v_add_f32_e32 v73, 1.0, v73
	v_add_f32_e32 v75, 1.0, v75
	v_rcp_f32_e32 v66, v66
	v_rcp_f32_e32 v70, v70
	v_rcp_f32_e32 v67, v67
	v_rcp_f32_e32 v71, v71
	v_rcp_f32_e32 v72, v72
	v_rcp_f32_e32 v73, v73
	v_rcp_f32_e32 v75, v75
	v_add_f32_e32 v74, 1.0, v74
	v_rcp_f32_e32 v74, v74
	v_mul_f32_e32 v61, v61, v66
	v_mul_f32_e32 v63, v63, v70
	v_mul_f32_e32 v66, v69, v67
	v_mul_f32_e32 v55, v55, v71
	v_mul_f32_e32 v51, v51, v72
	v_mul_f32_e32 v59, v59, v73
	v_mul_f32_e32 v57, v57, v75
	v_mul_f32_e32 v60, v60, v61
	v_mul_f32_e32 v62, v62, v63
	v_mul_f32_e32 v61, v68, v66
	v_mul_f32_e32 v54, v54, v55
	v_mul_f32_e32 v50, v50, v51
	v_mul_f32_e32 v51, v58, v59
	v_mul_f32_e32 v56, v56, v57
	v_mul_f32_e32 v57, 4.0, v60
	v_mul_f32_e32 v58, 4.0, v62
	v_mul_f32_e32 v59, 4.0, v61
	v_mul_f32_e32 v54, 4.0, v54
	v_med3_f32 v57, v57, s58, v181
	v_med3_f32 v58, v58, s58, v181
	v_mul_f32_e32 v65, v65, v74
	v_cvt_pk_fp8_f32 v52, v57, v58
	v_med3_f32 v57, v59, s58, v181
	v_med3_f32 v54, v54, s58, v181
	v_mul_f32_e32 v55, v64, v65
	v_cvt_pk_fp8_f32 v53, v57, v54
	v_mul_f32_e32 v50, 4.0, v50
	v_mul_f32_e32 v55, 4.0, v55
	v_mul_f32_e32 v51, 4.0, v51
	v_mul_f32_e32 v56, 4.0, v56
	v_med3_f32 v50, v50, s58, v181
	v_med3_f32 v55, v55, s58, v181
	v_cvt_pk_fp8_f32 v52, v50, v55 op_sel:[0,0,1]
	v_med3_f32 v50, v51, s58, v181
	v_med3_f32 v51, v56, s58, v181
	v_cvt_pk_fp8_f32 v53, v50, v51 op_sel:[0,0,1]
	v_mad_i64_i32 v[50:51], s[34:35], v84, s59, v[136:137]
	v_lshl_add_u64 v[50:51], v[50:51], 0, v[130:131]
	global_store_dwordx2 v[50:51], v[52:53], off
	v_mov_b32_e32 v50, v215
	v_cvt_f32_i32_e32 v53, v46
	v_cvt_f32_i32_e32 v52, v38
	v_cvt_f32_i32_e32 v47, v47
	v_cvt_f32_i32_e32 v46, v39
	v_cvt_f32_i32_e32 v55, v42
	v_cvt_f32_i32_e32 v54, v34
	v_cvt_f32_i32_e32 v39, v43
	v_cvt_f32_i32_e32 v38, v35
	v_cvt_f32_i32_e32 v35, v48
	v_cvt_f32_i32_e32 v34, v40
	v_cvt_f32_i32_e32 v43, v44
	v_cvt_f32_i32_e32 v42, v36
	v_cvt_f32_i32_e32 v48, v41
	v_cvt_f32_i32_e32 v41, v45
	v_cvt_f32_i32_e32 v40, v37
	v_cvt_f32_i32_e32 v49, v49
	v_mov_b32_e32 v36, v163
	v_mov_b32_e32 v37, v163
	v_add_u32_e32 v68, 0x90, v132
	v_pk_mul_f32 v[44:45], v[114:115], v[50:51] op_sel_hi:[1,0]
	v_pk_mul_f32 v[58:59], v[118:119], v[50:51] op_sel_hi:[1,0]
	v_pk_mul_f32 v[56:57], v[116:117], v[50:51] op_sel_hi:[1,0]
	v_pk_mul_f32 v[60:61], v[120:121], v[50:51] op_sel_hi:[1,0]
	v_pk_mul_f32 v[62:63], v[122:123], v[50:51] op_sel_hi:[1,0]
	v_pk_mul_f32 v[64:65], v[124:125], v[50:51] op_sel_hi:[1,0]
	v_pk_mul_f32 v[66:67], v[126:127], v[50:51] op_sel_hi:[1,0]
	v_pk_mul_f32 v[50:51], v[128:129], v[50:51] op_sel_hi:[1,0]
	v_pk_mul_f32 v[44:45], v[44:45], v[52:53]
	v_pk_mul_f32 v[46:47], v[58:59], v[46:47]
	v_pk_mul_f32 v[52:53], v[56:57], v[54:55]
	v_pk_mul_f32 v[38:39], v[60:61], v[38:39]
	v_pk_mul_f32 v[34:35], v[62:63], v[34:35]
	v_pk_mul_f32 v[42:43], v[64:65], v[42:43]
	v_pk_mul_f32 v[40:41], v[50:51], v[40:41]
	v_mul_f32_e32 v50, 0xbfb8aa3b, v45
	v_mul_f32_e32 v54, 0xbfb8aa3b, v47
	v_mul_f32_e32 v51, 0xbfb8aa3b, v53
	v_mul_f32_e32 v55, 0xbfb8aa3b, v39
	v_mul_f32_e32 v56, 0xbfb8aa3b, v35
	v_mul_f32_e32 v57, 0xbfb8aa3b, v43
	v_mul_f32_e32 v59, 0xbfb8aa3b, v41
	v_exp_f32_e32 v50, v50
	v_exp_f32_e32 v54, v54
	v_exp_f32_e32 v51, v51
	v_exp_f32_e32 v55, v55
	v_exp_f32_e32 v56, v56
	v_exp_f32_e32 v57, v57
	v_exp_f32_e32 v59, v59
	v_pk_mul_f32 v[48:49], v[66:67], v[48:49]
	v_add_f32_e32 v50, 1.0, v50
	v_mul_f32_e32 v58, 0xbfb8aa3b, v49
	v_exp_f32_e32 v58, v58
	v_add_f32_e32 v54, 1.0, v54
	v_add_f32_e32 v51, 1.0, v51
	v_add_f32_e32 v55, 1.0, v55
	v_add_f32_e32 v56, 1.0, v56
	v_add_f32_e32 v57, 1.0, v57
	v_add_f32_e32 v59, 1.0, v59
	v_rcp_f32_e32 v50, v50
	v_rcp_f32_e32 v54, v54
	v_rcp_f32_e32 v51, v51
	v_rcp_f32_e32 v55, v55
	v_rcp_f32_e32 v56, v56
	v_rcp_f32_e32 v57, v57
	v_rcp_f32_e32 v59, v59
	v_add_f32_e32 v58, 1.0, v58
	v_rcp_f32_e32 v58, v58
	v_mul_f32_e32 v45, v45, v50
	v_mul_f32_e32 v47, v47, v54
	v_mul_f32_e32 v50, v53, v51
	v_mul_f32_e32 v39, v39, v55
	v_mul_f32_e32 v35, v35, v56
; __device__ __forceinline__ unsigned cvt4_fp8(float a, float b, float c, float d) { int w = 0; w = __builtin_amdgcn_cvt_pk_fp8_f32(clamp448(a), clamp448(b), w, false); w = __builtin_amdgcn_cvt_pk_fp8_f32(clamp448(c), clamp448(d), w, true); return (unsigned)w; }
; __device__ __forceinline__ float siluf_(float x) { return x * sigmoidf_(x); }
; __device__ __forceinline__ u32x4 pack8(const f32x4 a, const f32x4 b) { u32x4 w; w.x = cvt_pk_bf16(a[0], a[1]); w.y = cvt_pk_bf16(a[2], a[3]); w.z = cvt_pk_bf16(b[0], b[1]); w.w = cvt_pk_bf16(b[2], b[3]); return w; }
;     __device__ __forceinline__ void operator()(const AccT& acc, const Unit& u, int wr, int wc, int fr, int fq) const {
;         const int row0 = u.orow0 + wr * 64 + fr, cb = u.pn * 128 + wc * 32 + 8 * fq, nb = u.pn * 256 + wc * 32 + 8 * fq;
;         f32x4 cg0 = *(const f32x4*)(cmax + nb) * (1.0f / 127.0f), cg1 = *(const f32x4*)(cmax + nb + 4) * (1.0f / 127.0f), cu0 = *(const f32x4*)(cmax + nb + 128) * (1.0f / 127.0f), cu1 = *(const f32x4*)(cmax + nb + 132) * (1.0f / 127.0f);
; #pragma unroll
;         for (int ai = 0; ai < 2; ++ai)
; #pragma unroll
;             for (int m = 0; m < 4; ++m) { const int row = row0 + ai * HALF + m * 16; const float rs = rsc[row]; f32x4 z0, z1;
;                 const i32x4v g0 = __builtin_bit_cast(i32x4v, acc[ai][0][m][0]), g1 = __builtin_bit_cast(i32x4v, acc[ai][0][m][1]), u0 = __builtin_bit_cast(i32x4v, acc[ai][1][m][0]), u1 = __builtin_bit_cast(i32x4v, acc[ai][1][m][1]);
; #pragma unroll
;                 for (int j = 0; j < 4; ++j) { z0[j] = siluf_((float)g0[j] * (rs * cg0[j])) * ((float)u0[j] * (rs * cu0[j])); z1[j] = siluf_((float)g1[j] * (rs * cg1[j])) * ((float)u1[j] * (rs * cu1[j])); }
;                 if (sout8 > 0.f) { u32x2 w; w.x = cvt4_fp8(z0[0] * sout8, z0[1] * sout8, z0[2] * sout8, z0[3] * sout8); w.y = cvt4_fp8(z1[0] * sout8, z1[1] * sout8, z1[2] * sout8, z1[3] * sout8); *(u32x2*)((unsigned char*)O + (size_t)row * ldo + cb) = w; }
;                 else *(u32x4*)(O + (size_t)row * ldo + cb) = pack8(z0, z1);
;                 __builtin_amdgcn_sched_barrier(0); }
	v_mul_f32_e32 v43, v43, v57
	v_mul_f32_e32 v41, v41, v59
	v_mul_f32_e32 v44, v44, v45
	v_mul_f32_e32 v46, v46, v47
	v_mul_f32_e32 v45, v52, v50
	v_mul_f32_e32 v38, v38, v39
	v_mul_f32_e32 v34, v34, v35
	v_mul_f32_e32 v35, v42, v43
	v_mul_f32_e32 v40, v40, v41
	v_mul_f32_e32 v41, 4.0, v44
	v_mul_f32_e32 v42, 4.0, v46
	v_mul_f32_e32 v43, 4.0, v45
	v_mul_f32_e32 v38, 4.0, v38
	v_med3_f32 v41, v41, s58, v181
	v_med3_f32 v42, v42, s58, v181
	v_mul_f32_e32 v49, v49, v58
	v_cvt_pk_fp8_f32 v36, v41, v42
	v_med3_f32 v41, v43, s58, v181
	v_med3_f32 v38, v38, s58, v181
	v_mul_f32_e32 v39, v48, v49
	v_cvt_pk_fp8_f32 v37, v41, v38
	v_mul_f32_e32 v34, 4.0, v34
	v_mul_f32_e32 v39, 4.0, v39
	v_mul_f32_e32 v35, 4.0, v35
	v_mul_f32_e32 v40, 4.0, v40
	v_med3_f32 v34, v34, s58, v181
	v_med3_f32 v39, v39, s58, v181
	v_cvt_pk_fp8_f32 v36, v34, v39 op_sel:[0,0,1]
	v_med3_f32 v34, v35, s58, v181
	v_med3_f32 v35, v40, s58, v181
	v_cvt_pk_fp8_f32 v37, v34, v35 op_sel:[0,0,1]
	v_mad_i64_i32 v[34:35], s[34:35], v68, s59, v[136:137]
	v_lshl_add_u64 v[34:35], v[34:35], 0, v[130:131]
	global_store_dwordx2 v[34:35], v[36:37], off
	v_mov_b32_e32 v34, v216
	v_cvt_f32_i32_e32 v37, v30
	v_cvt_f32_i32_e32 v36, v22
	v_cvt_f32_i32_e32 v31, v31
	v_cvt_f32_i32_e32 v30, v23
	v_cvt_f32_i32_e32 v39, v26
	v_cvt_f32_i32_e32 v38, v18
	v_cvt_f32_i32_e32 v23, v27
	v_cvt_f32_i32_e32 v22, v19
	v_cvt_f32_i32_e32 v19, v32
	v_cvt_f32_i32_e32 v18, v24
	v_cvt_f32_i32_e32 v27, v28
	v_cvt_f32_i32_e32 v26, v20
	v_cvt_f32_i32_e32 v32, v25
	v_cvt_f32_i32_e32 v25, v29
	v_cvt_f32_i32_e32 v24, v21
	v_cvt_f32_i32_e32 v33, v33
	v_mov_b32_e32 v20, v163
	v_mov_b32_e32 v21, v163
	v_add_u32_e32 v52, 0xa0, v132
	v_pk_mul_f32 v[28:29], v[114:115], v[34:35] op_sel_hi:[1,0]
	v_pk_mul_f32 v[42:43], v[118:119], v[34:35] op_sel_hi:[1,0]
	v_pk_mul_f32 v[40:41], v[116:117], v[34:35] op_sel_hi:[1,0]
	v_pk_mul_f32 v[44:45], v[120:121], v[34:35] op_sel_hi:[1,0]
	v_pk_mul_f32 v[46:47], v[122:123], v[34:35] op_sel_hi:[1,0]
	v_pk_mul_f32 v[48:49], v[124:125], v[34:35] op_sel_hi:[1,0]
	v_pk_mul_f32 v[50:51], v[126:127], v[34:35] op_sel_hi:[1,0]
	v_pk_mul_f32 v[34:35], v[128:129], v[34:35] op_sel_hi:[1,0]
	v_pk_mul_f32 v[28:29], v[28:29], v[36:37]
	v_pk_mul_f32 v[30:31], v[42:43], v[30:31]
	v_pk_mul_f32 v[36:37], v[40:41], v[38:39]
	v_pk_mul_f32 v[22:23], v[44:45], v[22:23]
	v_pk_mul_f32 v[18:19], v[46:47], v[18:19]
	v_pk_mul_f32 v[26:27], v[48:49], v[26:27]
	v_pk_mul_f32 v[24:25], v[34:35], v[24:25]
	v_mul_f32_e32 v34, 0xbfb8aa3b, v29
	v_mul_f32_e32 v38, 0xbfb8aa3b, v31
	v_mul_f32_e32 v35, 0xbfb8aa3b, v37
	v_mul_f32_e32 v39, 0xbfb8aa3b, v23
	v_mul_f32_e32 v40, 0xbfb8aa3b, v19
	v_mul_f32_e32 v41, 0xbfb8aa3b, v27
	v_mul_f32_e32 v43, 0xbfb8aa3b, v25
	v_exp_f32_e32 v34, v34
	v_exp_f32_e32 v38, v38
	v_exp_f32_e32 v35, v35
	v_exp_f32_e32 v39, v39
	v_exp_f32_e32 v40, v40
	v_exp_f32_e32 v41, v41
	v_exp_f32_e32 v43, v43
	v_pk_mul_f32 v[32:33], v[50:51], v[32:33]
	v_add_f32_e32 v34, 1.0, v34
	v_mul_f32_e32 v42, 0xbfb8aa3b, v33
	v_exp_f32_e32 v42, v42
	v_add_f32_e32 v38, 1.0, v38
	v_add_f32_e32 v35, 1.0, v35
	v_add_f32_e32 v39, 1.0, v39
	v_add_f32_e32 v40, 1.0, v40
	v_add_f32_e32 v41, 1.0, v41
	v_add_f32_e32 v43, 1.0, v43
	v_rcp_f32_e32 v34, v34
	v_rcp_f32_e32 v38, v38
	v_rcp_f32_e32 v35, v35
	v_rcp_f32_e32 v39, v39
	v_rcp_f32_e32 v40, v40
	v_rcp_f32_e32 v41, v41
	v_rcp_f32_e32 v43, v43
	v_add_f32_e32 v42, 1.0, v42
	v_rcp_f32_e32 v42, v42
	v_mul_f32_e32 v29, v29, v34
	v_mul_f32_e32 v31, v31, v38
	v_mul_f32_e32 v34, v37, v35
	v_mul_f32_e32 v23, v23, v39
	v_mul_f32_e32 v19, v19, v40
	v_mul_f32_e32 v27, v27, v41
	v_mul_f32_e32 v25, v25, v43
	v_mul_f32_e32 v28, v28, v29
	v_mul_f32_e32 v30, v30, v31
	v_mul_f32_e32 v29, v36, v34
	v_mul_f32_e32 v22, v22, v23
	v_mul_f32_e32 v18, v18, v19
	v_mul_f32_e32 v19, v26, v27
	v_mul_f32_e32 v24, v24, v25
	v_mul_f32_e32 v25, 4.0, v28
	v_mul_f32_e32 v26, 4.0, v30
	v_mul_f32_e32 v27, 4.0, v29
	v_mul_f32_e32 v22, 4.0, v22
	v_med3_f32 v25, v25, s58, v181
	v_med3_f32 v26, v26, s58, v181
	v_mul_f32_e32 v33, v33, v42
	v_cvt_pk_fp8_f32 v20, v25, v26
	v_med3_f32 v25, v27, s58, v181
	v_med3_f32 v22, v22, s58, v181
	v_mul_f32_e32 v23, v32, v33
; __device__ __forceinline__ unsigned cvt4_fp8(float a, float b, float c, float d) { int w = 0; w = __builtin_amdgcn_cvt_pk_fp8_f32(clamp448(a), clamp448(b), w, false); w = __builtin_amdgcn_cvt_pk_fp8_f32(clamp448(c), clamp448(d), w, true); return (unsigned)w; }
; __device__ __forceinline__ float siluf_(float x) { return x * sigmoidf_(x); }
; __device__ __forceinline__ u32x4 pack8(const f32x4 a, const f32x4 b) { u32x4 w; w.x = cvt_pk_bf16(a[0], a[1]); w.y = cvt_pk_bf16(a[2], a[3]); w.z = cvt_pk_bf16(b[0], b[1]); w.w = cvt_pk_bf16(b[2], b[3]); return w; }
;     __device__ __forceinline__ void operator()(const AccT& acc, const Unit& u, int wr, int wc, int fr, int fq) const {
;         const int row0 = u.orow0 + wr * 64 + fr, cb = u.pn * 128 + wc * 32 + 8 * fq, nb = u.pn * 256 + wc * 32 + 8 * fq;
;         f32x4 cg0 = *(const f32x4*)(cmax + nb) * (1.0f / 127.0f), cg1 = *(const f32x4*)(cmax + nb + 4) * (1.0f / 127.0f), cu0 = *(const f32x4*)(cmax + nb + 128) * (1.0f / 127.0f), cu1 = *(const f32x4*)(cmax + nb + 132) * (1.0f / 127.0f);
; #pragma unroll
;         for (int ai = 0; ai < 2; ++ai)
; #pragma unroll
;             for (int m = 0; m < 4; ++m) { const int row = row0 + ai * HALF + m * 16; const float rs = rsc[row]; f32x4 z0, z1;
;                 const i32x4v g0 = __builtin_bit_cast(i32x4v, acc[ai][0][m][0]), g1 = __builtin_bit_cast(i32x4v, acc[ai][0][m][1]), u0 = __builtin_bit_cast(i32x4v, acc[ai][1][m][0]), u1 = __builtin_bit_cast(i32x4v, acc[ai][1][m][1]);
; #pragma unroll
;                 for (int j = 0; j < 4; ++j) { z0[j] = siluf_((float)g0[j] * (rs * cg0[j])) * ((float)u0[j] * (rs * cu0[j])); z1[j] = siluf_((float)g1[j] * (rs * cg1[j])) * ((float)u1[j] * (rs * cu1[j])); }
;                 if (sout8 > 0.f) { u32x2 w; w.x = cvt4_fp8(z0[0] * sout8, z0[1] * sout8, z0[2] * sout8, z0[3] * sout8); w.y = cvt4_fp8(z1[0] * sout8, z1[1] * sout8, z1[2] * sout8, z1[3] * sout8); *(u32x2*)((unsigned char*)O + (size_t)row * ldo + cb) = w; }
;                 else *(u32x4*)(O + (size_t)row * ldo + cb) = pack8(z0, z1);
;                 __builtin_amdgcn_sched_barrier(0); }
	v_cvt_pk_fp8_f32 v21, v25, v22
	v_mul_f32_e32 v18, 4.0, v18
	v_mul_f32_e32 v23, 4.0, v23
	v_mul_f32_e32 v19, 4.0, v19
	v_mul_f32_e32 v24, 4.0, v24
	v_med3_f32 v18, v18, s58, v181
	v_med3_f32 v23, v23, s58, v181
	v_cvt_pk_fp8_f32 v20, v18, v23 op_sel:[0,0,1]
	v_med3_f32 v18, v19, s58, v181
	v_med3_f32 v19, v24, s58, v181
	v_cvt_pk_fp8_f32 v21, v18, v19 op_sel:[0,0,1]
	v_mad_i64_i32 v[18:19], s[34:35], v52, s59, v[136:137]
	v_lshl_add_u64 v[18:19], v[18:19], 0, v[130:131]
	global_store_dwordx2 v[18:19], v[20:21], off
	v_mov_b32_e32 v18, v217
	v_cvt_f32_i32_e32 v21, v14
	v_cvt_f32_i32_e32 v20, v6
	v_cvt_f32_i32_e32 v15, v15
	v_cvt_f32_i32_e32 v14, v7
	v_cvt_f32_i32_e32 v23, v10
	v_cvt_f32_i32_e32 v22, v2
	v_cvt_f32_i32_e32 v7, v11
	v_cvt_f32_i32_e32 v6, v3
	v_cvt_f32_i32_e32 v3, v16
	v_cvt_f32_i32_e32 v2, v8
	v_cvt_f32_i32_e32 v11, v12
	v_cvt_f32_i32_e32 v10, v4
	v_cvt_f32_i32_e32 v16, v9
	v_cvt_f32_i32_e32 v9, v13
	v_cvt_f32_i32_e32 v8, v5
	v_cvt_f32_i32_e32 v17, v17
	v_mov_b32_e32 v4, v163
	v_mov_b32_e32 v5, v163
	v_add_u32_e32 v36, 0xb0, v132
	v_pk_mul_f32 v[12:13], v[114:115], v[18:19] op_sel_hi:[1,0]
	v_pk_mul_f32 v[26:27], v[118:119], v[18:19] op_sel_hi:[1,0]
	v_pk_mul_f32 v[24:25], v[116:117], v[18:19] op_sel_hi:[1,0]
	v_pk_mul_f32 v[28:29], v[120:121], v[18:19] op_sel_hi:[1,0]
	v_pk_mul_f32 v[30:31], v[122:123], v[18:19] op_sel_hi:[1,0]
	v_pk_mul_f32 v[32:33], v[124:125], v[18:19] op_sel_hi:[1,0]
	v_pk_mul_f32 v[34:35], v[126:127], v[18:19] op_sel_hi:[1,0]
	v_pk_mul_f32 v[18:19], v[128:129], v[18:19] op_sel_hi:[1,0]
	v_pk_mul_f32 v[12:13], v[12:13], v[20:21]
	v_pk_mul_f32 v[14:15], v[26:27], v[14:15]
	v_pk_mul_f32 v[20:21], v[24:25], v[22:23]
	v_pk_mul_f32 v[6:7], v[28:29], v[6:7]
	v_pk_mul_f32 v[2:3], v[30:31], v[2:3]
	v_pk_mul_f32 v[10:11], v[32:33], v[10:11]
	v_pk_mul_f32 v[8:9], v[18:19], v[8:9]
	v_mul_f32_e32 v18, 0xbfb8aa3b, v13
	v_mul_f32_e32 v22, 0xbfb8aa3b, v15
	v_mul_f32_e32 v19, 0xbfb8aa3b, v21
	v_mul_f32_e32 v23, 0xbfb8aa3b, v7
	v_mul_f32_e32 v24, 0xbfb8aa3b, v3
	v_mul_f32_e32 v25, 0xbfb8aa3b, v11
	v_mul_f32_e32 v27, 0xbfb8aa3b, v9
	v_exp_f32_e32 v18, v18
	v_exp_f32_e32 v22, v22
	v_exp_f32_e32 v19, v19
	v_exp_f32_e32 v23, v23
	v_exp_f32_e32 v24, v24
	v_exp_f32_e32 v25, v25
	v_exp_f32_e32 v27, v27
	v_pk_mul_f32 v[16:17], v[34:35], v[16:17]
	v_add_f32_e32 v18, 1.0, v18
	v_mul_f32_e32 v26, 0xbfb8aa3b, v17
	v_exp_f32_e32 v26, v26
	v_add_f32_e32 v22, 1.0, v22
	v_add_f32_e32 v19, 1.0, v19
	v_add_f32_e32 v23, 1.0, v23
	v_add_f32_e32 v24, 1.0, v24
	v_add_f32_e32 v25, 1.0, v25
	v_add_f32_e32 v27, 1.0, v27
	v_rcp_f32_e32 v18, v18
	v_rcp_f32_e32 v22, v22
	v_rcp_f32_e32 v19, v19
	v_rcp_f32_e32 v23, v23
	v_rcp_f32_e32 v24, v24
	v_rcp_f32_e32 v25, v25
	v_rcp_f32_e32 v27, v27
	v_add_f32_e32 v26, 1.0, v26
	v_rcp_f32_e32 v26, v26
	v_mul_f32_e32 v13, v13, v18
	v_mul_f32_e32 v15, v15, v22
	v_mul_f32_e32 v18, v21, v19
	v_mul_f32_e32 v7, v7, v23
	v_mul_f32_e32 v3, v3, v24
	v_mul_f32_e32 v11, v11, v25
	v_mul_f32_e32 v9, v9, v27
	v_mul_f32_e32 v12, v12, v13
	v_mul_f32_e32 v14, v14, v15
	v_mul_f32_e32 v13, v20, v18
	v_mul_f32_e32 v6, v6, v7
	v_mul_f32_e32 v2, v2, v3
	v_mul_f32_e32 v3, v10, v11
	v_mul_f32_e32 v8, v8, v9
	v_mul_f32_e32 v9, 4.0, v12
	v_mul_f32_e32 v10, 4.0, v14
	v_mul_f32_e32 v11, 4.0, v13
	v_mul_f32_e32 v6, 4.0, v6
	v_med3_f32 v9, v9, s58, v181
	v_med3_f32 v10, v10, s58, v181
	v_mul_f32_e32 v17, v17, v26
	v_cvt_pk_fp8_f32 v4, v9, v10
	v_med3_f32 v9, v11, s58, v181
	v_med3_f32 v6, v6, s58, v181
	v_mul_f32_e32 v7, v16, v17
	v_cvt_pk_fp8_f32 v5, v9, v6
	v_mul_f32_e32 v2, 4.0, v2
	v_mul_f32_e32 v7, 4.0, v7
	v_mul_f32_e32 v3, 4.0, v3
	v_mul_f32_e32 v8, 4.0, v8
	v_med3_f32 v2, v2, s58, v181
	v_med3_f32 v7, v7, s58, v181
	v_cvt_pk_fp8_f32 v4, v2, v7 op_sel:[0,0,1]
	v_med3_f32 v2, v3, s58, v181
	v_med3_f32 v3, v8, s58, v181
	v_cvt_pk_fp8_f32 v5, v2, v3 op_sel:[0,0,1]
	v_mad_i64_i32 v[2:3], s[34:35], v36, s59, v[136:137]
	v_lshl_add_u64 v[2:3], v[2:3], 0, v[130:131]
	global_store_dwordx2 v[2:3], v[4:5], off
	s_andn2_b64 vcc, exec, s[28:29]
	s_mov_b64 s[28:29], -1
	s_cbranch_vccnz .LBB0_1408
	s_andn2_b64 vcc, exec, s[4:5]
	s_cbranch_vccnz .LBB0_1407
	s_barrier
	s_branch .LBB0_1407

; __device__ __forceinline__ void st4_bf(bf16_t* p, const f32x4 v) { u32x2 w; w.x = cvt_pk_bf16(v[0], v[1]); w.y = cvt_pk_bf16(v[2], v[3]); *(u32x2*)p = w; }
;     static __device__ __forceinline__ f32x4 ldb(const bf16_t* p) { return ld4_bf(p); }
;     __device__ __forceinline__ void operator()(const AccT& acc, const Unit& u, int wr, int wc, int fr, int fq) const { if (u.g == 0) q(acc, u, wr, wc, fr, fq); else kv(acc, u, wr, wc, fr, fq); }
; __device__ __forceinline__ float bf_lo(unsigned w) { return __uint_as_float(w << 16); }
; __device__ __forceinline__ float bf_hi(unsigned w) { return __uint_as_float(w & 0xffff0000u); }
; __device__ __forceinline__ f32x4 ld4_bf(const bf16_t* p) { const u32x2 w = *(const u32x2*)p; return (f32x4){bf_lo(w.x), bf_hi(w.x), bf_lo(w.y), bf_hi(w.y)}; }
;     __device__ __forceinline__ void operator()(const AccT& acc, const Unit& u, int wr, int wc, int fr, int fq) const {
;         const int cnd = cond_of(u.orow0);
;         const BT* bp = (u.orow0 < ML) ? bl + (size_t)u.orow0 * DM : bc + (size_t)(u.orow0 - ML) * DM;
;         bf16_t* op = out + (size_t)u.orow0 * DM;
;         const int rl0 = wr * 64 + fr, col0 = u.pn * BM + wc * 32 + 4 * fq;
;         f32x4 gv[2][2];
; #pragma unroll
;         for (int bj = 0; bj < 2; ++bj)
; #pragma unroll
;             for (int n = 0; n < 2; ++n) gv[bj][n] = *(const f32x4*)(gate + (size_t)cnd * NMOD + col0 + bj * HALF + n * 16) * scale;
; #pragma unroll
;         for (int ai = 0; ai < 2; ++ai)
; #pragma unroll
;             for (int m = 0; m < 4; ++m) { const size_t off = (size_t)(rl0 + ai * HALF + m * 16) * DM + col0;
; #pragma unroll
;                 for (int bj = 0; bj < 2; ++bj)
; #pragma unroll
;                     for (int n = 0; n < 2; ++n) { const f32x4 bs = ldb(bp + off + bj * HALF + n * 16); st4_bf(op + off + bj * HALF + n * 16, bs + gv[bj][n] * acc[ai][bj][m][n]); }
;                 asm volatile("" ::: "memory"); }
;     }
.LBB0_1541:
	s_min_i32 s14, s26, 0x4000
	s_ashr_i32 s14, s14, 12
	v_lshl_or_b32 v2, s66, 8, v227
	s_mul_hi_i32 s27, s14, 0xc000
	s_mul_i32 s14, s14, 0xc000
	v_ashrrev_i32_e32 v3, 31, v2
	v_lshl_add_u64 v[4:5], v[196:197], 0, v[2:3]
	s_add_u32 s26, s57, s14
	v_lshlrev_b64 v[8:9], 1, v[4:5]
	s_addc_u32 s27, s58, s27
	v_lshl_add_u64 v[26:27], s[28:29], 0, v[8:9]
	v_lshl_add_u64 v[12:13], v[2:3], 2, s[26:27]
	global_load_dwordx2 v[32:33], v[26:27], off
	global_load_dwordx4 v[4:7], v[12:13], off
	s_add_u32 s26, s53, s30
	s_addc_u32 s27, s54, s31
	global_load_dwordx4 v[14:17], v[12:13], off offset:64
	global_load_dwordx4 v[18:21], v[12:13], off offset:512
	global_load_dwordx4 v[22:25], v[12:13], off offset:576
	v_lshl_add_u64 v[28:29], s[26:27], 0, v[8:9]
	s_and_b64 vcc, exec, s[2:3]
	s_mov_b64 s[2:3], -1
	global_load_dwordx2 v[34:35], v[26:27], off offset:32
	global_load_dwordx2 v[36:37], v[26:27], off offset:256
	global_load_dwordx2 v[38:39], v[26:27], off offset:288
	v_lshl_add_u64 v[64:65], v[198:199], 0, v[2:3]
	v_lshlrev_b64 v[64:65], 1, v[64:65]
	v_lshl_add_u64 v[64:65], s[28:29], 0, v[64:65]
	global_load_dwordx2 v[40:41], v[64:65], off
	global_load_dwordx2 v[42:43], v[64:65], off offset:32
	global_load_dwordx2 v[44:45], v[64:65], off offset:256
	global_load_dwordx2 v[46:47], v[64:65], off offset:288
	v_lshl_add_u64 v[64:65], v[200:201], 0, v[2:3]
	v_lshlrev_b64 v[64:65], 1, v[64:65]
	v_lshl_add_u64 v[64:65], s[28:29], 0, v[64:65]
	global_load_dwordx2 v[48:49], v[64:65], off
	global_load_dwordx2 v[50:51], v[64:65], off offset:32
	global_load_dwordx2 v[52:53], v[64:65], off offset:256
	global_load_dwordx2 v[54:55], v[64:65], off offset:288
	v_lshl_add_u64 v[64:65], v[202:203], 0, v[2:3]
	v_lshlrev_b64 v[64:65], 1, v[64:65]
	v_lshl_add_u64 v[64:65], s[28:29], 0, v[64:65]
	global_load_dwordx2 v[56:57], v[64:65], off
	global_load_dwordx2 v[58:59], v[64:65], off offset:32
	global_load_dwordx2 v[60:61], v[64:65], off offset:256
	global_load_dwordx2 v[62:63], v[64:65], off offset:288
	s_waitcnt vmcnt(15)
	v_lshlrev_b32_e32 v8, 16, v32
	v_and_b32_e32 v9, 0xffff0000, v32
	v_pk_mul_f32 v[12:13], v[6:7], s[22:23] op_sel_hi:[1, 0]
	v_pk_mul_f32 v[6:7], v[4:5], s[22:23] op_sel_hi:[1, 0]
	v_lshlrev_b32_e32 v10, 16, v33
	v_and_b32_e32 v11, 0xffff0000, v33
	v_pk_fma_f32 v[8:9], v[190:191], v[6:7], v[8:9]
	v_pk_fma_f32 v[4:5], v[192:193], v[12:13], v[10:11]
	v_cvt_pk_bf16_f32 v8, v8, v9
	s_nop 0
	v_cvt_pk_bf16_f32 v9, v4, v5
	global_store_dwordx2 v[28:29], v[8:9], off
	v_lshl_add_u64 v[64:65], v[204:205], 0, v[2:3]
	v_lshlrev_b64 v[64:65], 1, v[64:65]
	v_lshl_add_u64 v[64:65], s[28:29], 0, v[64:65]
	global_load_dwordx2 v[32:33], v[64:65], off
	v_pk_mul_f32 v[4:5], v[14:15], s[22:23] op_sel_hi:[1,0]
	v_pk_mul_f32 v[8:9], v[16:17], s[22:23] op_sel_hi:[1,0]
	s_waitcnt vmcnt(16)
	v_lshlrev_b32_e32 v14, 16, v34
	v_and_b32_e32 v15, 0xffff0000, v34
	v_lshlrev_b32_e32 v10, 16, v35
	v_and_b32_e32 v11, 0xffff0000, v35
	v_pk_fma_f32 v[14:15], v[186:187], v[4:5], v[14:15]
	v_pk_fma_f32 v[10:11], v[188:189], v[8:9], v[10:11]
	v_cvt_pk_bf16_f32 v14, v14, v15
	s_nop 0
	v_cvt_pk_bf16_f32 v15, v10, v11
	global_store_dwordx2 v[28:29], v[14:15], off offset:32
	global_load_dwordx2 v[34:35], v[64:65], off offset:32
	v_pk_mul_f32 v[10:11], v[18:19], s[22:23] op_sel_hi:[1,0]
	v_pk_mul_f32 v[14:15], v[20:21], s[22:23] op_sel_hi:[1,0]
	s_waitcnt vmcnt(17)
	v_lshlrev_b32_e32 v18, 16, v36
	v_and_b32_e32 v19, 0xffff0000, v36
	v_lshlrev_b32_e32 v16, 16, v37
	v_and_b32_e32 v17, 0xffff0000, v37
	v_pk_fma_f32 v[18:19], v[182:183], v[10:11], v[18:19]
	v_pk_fma_f32 v[16:17], v[184:185], v[14:15], v[16:17]
	v_cvt_pk_bf16_f32 v18, v18, v19
	s_nop 0
	v_cvt_pk_bf16_f32 v19, v16, v17
	global_store_dwordx2 v[28:29], v[18:19], off offset:256
	global_load_dwordx2 v[36:37], v[64:65], off offset:256
	v_lshl_add_u64 v[16:17], v[198:199], 0, v[2:3]
	v_lshlrev_b64 v[26:27], 1, v[16:17]
	v_pk_mul_f32 v[16:17], v[22:23], s[22:23] op_sel_hi:[1,0]
	v_pk_mul_f32 v[18:19], v[24:25], s[22:23] op_sel_hi:[1,0]
	v_lshl_add_u64 v[30:31], s[28:29], 0, v[26:27]
	s_waitcnt vmcnt(18)
	v_lshlrev_b32_e32 v22, 16, v38
	v_and_b32_e32 v23, 0xffff0000, v38
	v_lshlrev_b32_e32 v20, 16, v39
	v_and_b32_e32 v21, 0xffff0000, v39
	v_pk_fma_f32 v[22:23], v[178:179], v[16:17], v[22:23]
	v_pk_fma_f32 v[20:21], v[180:181], v[18:19], v[20:21]
	v_cvt_pk_bf16_f32 v22, v22, v23
	s_nop 0
	v_cvt_pk_bf16_f32 v23, v20, v21
	global_store_dwordx2 v[28:29], v[22:23], off offset:288
	global_load_dwordx2 v[38:39], v[64:65], off offset:288
	v_lshl_add_u64 v[22:23], s[26:27], 0, v[26:27]
	s_waitcnt vmcnt(19)
	v_lshlrev_b32_e32 v24, 16, v40
	v_and_b32_e32 v25, 0xffff0000, v40
	v_lshlrev_b32_e32 v20, 16, v41
	v_and_b32_e32 v21, 0xffff0000, v41
	v_pk_fma_f32 v[24:25], v[174:175], v[6:7], v[24:25]
	v_pk_fma_f32 v[20:21], v[176:177], v[12:13], v[20:21]
	v_cvt_pk_bf16_f32 v24, v24, v25
	s_nop 0
	v_cvt_pk_bf16_f32 v25, v20, v21
	global_store_dwordx2 v[22:23], v[24:25], off
	v_lshl_add_u64 v[64:65], v[206:207], 0, v[2:3]
	v_lshlrev_b64 v[64:65], 1, v[64:65]
	v_lshl_add_u64 v[64:65], s[28:29], 0, v[64:65]
	global_load_dwordx2 v[40:41], v[64:65], off
	s_waitcnt vmcnt(20)
	v_lshlrev_b32_e32 v24, 16, v42
	v_and_b32_e32 v25, 0xffff0000, v42
	v_lshlrev_b32_e32 v20, 16, v43
	v_and_b32_e32 v21, 0xffff0000, v43
	v_pk_fma_f32 v[24:25], v[170:171], v[4:5], v[24:25]
	v_pk_fma_f32 v[20:21], v[172:173], v[8:9], v[20:21]
	v_cvt_pk_bf16_f32 v24, v24, v25
	s_nop 0
	v_cvt_pk_bf16_f32 v25, v20, v21
	global_store_dwordx2 v[22:23], v[24:25], off offset:32
	global_load_dwordx2 v[42:43], v[64:65], off offset:32
	s_waitcnt vmcnt(21)
; __device__ __forceinline__ void st4_bf(bf16_t* p, const f32x4 v) { u32x2 w; w.x = cvt_pk_bf16(v[0], v[1]); w.y = cvt_pk_bf16(v[2], v[3]); *(u32x2*)p = w; }
;     static __device__ __forceinline__ f32x4 ldb(const bf16_t* p) { return ld4_bf(p); }
;     __device__ __forceinline__ void operator()(const AccT& acc, const Unit& u, int wr, int wc, int fr, int fq) const { if (u.g == 0) q(acc, u, wr, wc, fr, fq); else kv(acc, u, wr, wc, fr, fq); }
; __device__ __forceinline__ float bf_lo(unsigned w) { return __uint_as_float(w << 16); }
; __device__ __forceinline__ float bf_hi(unsigned w) { return __uint_as_float(w & 0xffff0000u); }
; __device__ __forceinline__ f32x4 ld4_bf(const bf16_t* p) { const u32x2 w = *(const u32x2*)p; return (f32x4){bf_lo(w.x), bf_hi(w.x), bf_lo(w.y), bf_hi(w.y)}; }
;     __device__ __forceinline__ void operator()(const AccT& acc, const Unit& u, int wr, int wc, int fr, int fq) const {
;         const int cnd = cond_of(u.orow0);
;         const BT* bp = (u.orow0 < ML) ? bl + (size_t)u.orow0 * DM : bc + (size_t)(u.orow0 - ML) * DM;
;         bf16_t* op = out + (size_t)u.orow0 * DM;
;         const int rl0 = wr * 64 + fr, col0 = u.pn * BM + wc * 32 + 4 * fq;
;         f32x4 gv[2][2];
; #pragma unroll
;         for (int bj = 0; bj < 2; ++bj)
; #pragma unroll
;             for (int n = 0; n < 2; ++n) gv[bj][n] = *(const f32x4*)(gate + (size_t)cnd * NMOD + col0 + bj * HALF + n * 16) * scale;
; #pragma unroll
;         for (int ai = 0; ai < 2; ++ai)
; #pragma unroll
;             for (int m = 0; m < 4; ++m) { const size_t off = (size_t)(rl0 + ai * HALF + m * 16) * DM + col0;
; #pragma unroll
;                 for (int bj = 0; bj < 2; ++bj)
; #pragma unroll
;                     for (int n = 0; n < 2; ++n) { const f32x4 bs = ldb(bp + off + bj * HALF + n * 16); st4_bf(op + off + bj * HALF + n * 16, bs + gv[bj][n] * acc[ai][bj][m][n]); }
;                 asm volatile("" ::: "memory"); }
;     }
	v_lshlrev_b32_e32 v24, 16, v44
	v_and_b32_e32 v25, 0xffff0000, v44
	v_lshlrev_b32_e32 v20, 16, v45
	v_and_b32_e32 v21, 0xffff0000, v45
	v_pk_fma_f32 v[24:25], v[166:167], v[10:11], v[24:25]
	v_pk_fma_f32 v[20:21], v[168:169], v[14:15], v[20:21]
	v_cvt_pk_bf16_f32 v24, v24, v25
	s_nop 0
	v_cvt_pk_bf16_f32 v25, v20, v21
	global_store_dwordx2 v[22:23], v[24:25], off offset:256
	global_load_dwordx2 v[44:45], v[64:65], off offset:256
	v_lshl_add_u64 v[24:25], v[200:201], 0, v[2:3]
	v_lshlrev_b64 v[24:25], 1, v[24:25]
	v_lshl_add_u64 v[26:27], s[28:29], 0, v[24:25]
	s_waitcnt vmcnt(22)
	v_lshlrev_b32_e32 v28, 16, v46
	v_and_b32_e32 v29, 0xffff0000, v46
	v_lshlrev_b32_e32 v20, 16, v47
	v_and_b32_e32 v21, 0xffff0000, v47
	v_pk_fma_f32 v[28:29], v[162:163], v[16:17], v[28:29]
	v_pk_fma_f32 v[20:21], v[164:165], v[18:19], v[20:21]
	v_cvt_pk_bf16_f32 v28, v28, v29
	s_nop 0
	v_cvt_pk_bf16_f32 v29, v20, v21
	global_store_dwordx2 v[22:23], v[28:29], off offset:288
	global_load_dwordx2 v[46:47], v[64:65], off offset:288
	v_lshl_add_u64 v[22:23], s[26:27], 0, v[24:25]
	s_waitcnt vmcnt(23)
	v_lshlrev_b32_e32 v24, 16, v48
	v_and_b32_e32 v25, 0xffff0000, v48
	v_lshlrev_b32_e32 v20, 16, v49
	v_and_b32_e32 v21, 0xffff0000, v49
	v_pk_fma_f32 v[24:25], v[158:159], v[6:7], v[24:25]
	v_pk_fma_f32 v[20:21], v[160:161], v[12:13], v[20:21]
	v_cvt_pk_bf16_f32 v24, v24, v25
	s_nop 0
	v_cvt_pk_bf16_f32 v25, v20, v21
	global_store_dwordx2 v[22:23], v[24:25], off
	v_lshl_add_u64 v[64:65], v[208:209], 0, v[2:3]
	v_lshlrev_b64 v[64:65], 1, v[64:65]
	v_lshl_add_u64 v[64:65], s[28:29], 0, v[64:65]
	global_load_dwordx2 v[48:49], v[64:65], off
	s_waitcnt vmcnt(24)
	v_lshlrev_b32_e32 v24, 16, v50
	v_and_b32_e32 v25, 0xffff0000, v50
	v_lshlrev_b32_e32 v20, 16, v51
	v_and_b32_e32 v21, 0xffff0000, v51
	v_pk_fma_f32 v[24:25], v[154:155], v[4:5], v[24:25]
	v_pk_fma_f32 v[20:21], v[156:157], v[8:9], v[20:21]
	v_cvt_pk_bf16_f32 v24, v24, v25
	s_nop 0
	v_cvt_pk_bf16_f32 v25, v20, v21
	global_store_dwordx2 v[22:23], v[24:25], off offset:32
	global_load_dwordx2 v[50:51], v[64:65], off offset:32
	s_waitcnt vmcnt(25)
	v_lshlrev_b32_e32 v24, 16, v52
	v_and_b32_e32 v25, 0xffff0000, v52
	v_lshlrev_b32_e32 v20, 16, v53
	v_and_b32_e32 v21, 0xffff0000, v53
	v_pk_fma_f32 v[24:25], v[150:151], v[10:11], v[24:25]
	v_pk_fma_f32 v[20:21], v[152:153], v[14:15], v[20:21]
	v_cvt_pk_bf16_f32 v24, v24, v25
	s_nop 0
	v_cvt_pk_bf16_f32 v25, v20, v21
	global_store_dwordx2 v[22:23], v[24:25], off offset:256
	global_load_dwordx2 v[52:53], v[64:65], off offset:256
	v_lshl_add_u64 v[24:25], v[202:203], 0, v[2:3]
	v_lshlrev_b64 v[24:25], 1, v[24:25]
	v_lshl_add_u64 v[26:27], s[28:29], 0, v[24:25]
	s_waitcnt vmcnt(26)
	v_lshlrev_b32_e32 v28, 16, v54
	v_and_b32_e32 v29, 0xffff0000, v54
	v_lshlrev_b32_e32 v20, 16, v55
	v_and_b32_e32 v21, 0xffff0000, v55
	v_pk_fma_f32 v[28:29], v[146:147], v[16:17], v[28:29]
	v_pk_fma_f32 v[20:21], v[148:149], v[18:19], v[20:21]
	v_cvt_pk_bf16_f32 v28, v28, v29
	s_nop 0
	v_cvt_pk_bf16_f32 v29, v20, v21
	global_store_dwordx2 v[22:23], v[28:29], off offset:288
	global_load_dwordx2 v[54:55], v[64:65], off offset:288
	v_lshl_add_u64 v[22:23], s[26:27], 0, v[24:25]
	s_waitcnt vmcnt(27)
	v_lshlrev_b32_e32 v24, 16, v56
	v_and_b32_e32 v25, 0xffff0000, v56
	v_lshlrev_b32_e32 v20, 16, v57
	v_and_b32_e32 v21, 0xffff0000, v57
	v_pk_fma_f32 v[24:25], v[142:143], v[6:7], v[24:25]
	v_pk_fma_f32 v[20:21], v[144:145], v[12:13], v[20:21]
	v_cvt_pk_bf16_f32 v24, v24, v25
	s_nop 0
	v_cvt_pk_bf16_f32 v25, v20, v21
	global_store_dwordx2 v[22:23], v[24:25], off
	v_lshl_add_u64 v[64:65], v[210:211], 0, v[2:3]
	v_lshlrev_b64 v[64:65], 1, v[64:65]
	v_lshl_add_u64 v[64:65], s[28:29], 0, v[64:65]
	global_load_dwordx2 v[56:57], v[64:65], off
	s_waitcnt vmcnt(28)
	v_lshlrev_b32_e32 v24, 16, v58
	v_and_b32_e32 v25, 0xffff0000, v58
	v_lshlrev_b32_e32 v20, 16, v59
	v_and_b32_e32 v21, 0xffff0000, v59
	v_pk_fma_f32 v[24:25], v[138:139], v[4:5], v[24:25]
	v_pk_fma_f32 v[20:21], v[140:141], v[8:9], v[20:21]
	v_cvt_pk_bf16_f32 v24, v24, v25
	s_nop 0
	v_cvt_pk_bf16_f32 v25, v20, v21
	global_store_dwordx2 v[22:23], v[24:25], off offset:32
	global_load_dwordx2 v[58:59], v[64:65], off offset:32
	s_waitcnt vmcnt(29)
	v_lshlrev_b32_e32 v24, 16, v60
	v_and_b32_e32 v25, 0xffff0000, v60
	v_lshlrev_b32_e32 v20, 16, v61
	v_and_b32_e32 v21, 0xffff0000, v61
	v_pk_fma_f32 v[24:25], v[134:135], v[10:11], v[24:25]
	v_pk_fma_f32 v[20:21], v[136:137], v[14:15], v[20:21]
	v_cvt_pk_bf16_f32 v24, v24, v25
	s_nop 0
	v_cvt_pk_bf16_f32 v25, v20, v21
	global_store_dwordx2 v[22:23], v[24:25], off offset:256
	global_load_dwordx2 v[60:61], v[64:65], off offset:256
	v_lshl_add_u64 v[24:25], v[204:205], 0, v[2:3]
	v_lshlrev_b64 v[24:25], 1, v[24:25]
	v_lshl_add_u64 v[26:27], s[28:29], 0, v[24:25]
	s_waitcnt vmcnt(30)
	v_lshlrev_b32_e32 v28, 16, v62
	v_and_b32_e32 v29, 0xffff0000, v62
	v_lshlrev_b32_e32 v20, 16, v63
	v_and_b32_e32 v21, 0xffff0000, v63
	v_pk_fma_f32 v[28:29], v[130:131], v[16:17], v[28:29]
	v_pk_fma_f32 v[20:21], v[132:133], v[18:19], v[20:21]
	v_cvt_pk_bf16_f32 v28, v28, v29
	s_nop 0
	v_cvt_pk_bf16_f32 v29, v20, v21
	global_store_dwordx2 v[22:23], v[28:29], off offset:288
	global_load_dwordx2 v[62:63], v[64:65], off offset:288
	v_lshl_add_u64 v[22:23], s[26:27], 0, v[24:25]
	s_waitcnt vmcnt(30)
	v_lshlrev_b32_e32 v24, 16, v32
	v_and_b32_e32 v25, 0xffff0000, v32
	v_lshlrev_b32_e32 v20, 16, v33
	v_and_b32_e32 v21, 0xffff0000, v33
	v_pk_fma_f32 v[24:25], v[126:127], v[6:7], v[24:25]
	v_pk_fma_f32 v[20:21], v[128:129], v[12:13], v[20:21]
	v_cvt_pk_bf16_f32 v24, v24, v25
	s_nop 0
	v_cvt_pk_bf16_f32 v25, v20, v21
	global_store_dwordx2 v[22:23], v[24:25], off
	s_waitcnt vmcnt(29)
; __device__ __forceinline__ void st4_bf(bf16_t* p, const f32x4 v) { u32x2 w; w.x = cvt_pk_bf16(v[0], v[1]); w.y = cvt_pk_bf16(v[2], v[3]); *(u32x2*)p = w; }
;     static __device__ __forceinline__ f32x4 ldb(const bf16_t* p) { return ld4_bf(p); }
;     __device__ __forceinline__ void operator()(const AccT& acc, const Unit& u, int wr, int wc, int fr, int fq) const { if (u.g == 0) q(acc, u, wr, wc, fr, fq); else kv(acc, u, wr, wc, fr, fq); }
; __device__ __forceinline__ float bf_lo(unsigned w) { return __uint_as_float(w << 16); }
; __device__ __forceinline__ float bf_hi(unsigned w) { return __uint_as_float(w & 0xffff0000u); }
; __device__ __forceinline__ f32x4 ld4_bf(const bf16_t* p) { const u32x2 w = *(const u32x2*)p; return (f32x4){bf_lo(w.x), bf_hi(w.x), bf_lo(w.y), bf_hi(w.y)}; }
;     __device__ __forceinline__ void operator()(const AccT& acc, const Unit& u, int wr, int wc, int fr, int fq) const {
;         const int cnd = cond_of(u.orow0);
;         const BT* bp = (u.orow0 < ML) ? bl + (size_t)u.orow0 * DM : bc + (size_t)(u.orow0 - ML) * DM;
;         bf16_t* op = out + (size_t)u.orow0 * DM;
;         const int rl0 = wr * 64 + fr, col0 = u.pn * BM + wc * 32 + 4 * fq;
;         f32x4 gv[2][2];
; #pragma unroll
;         for (int bj = 0; bj < 2; ++bj)
; #pragma unroll
;             for (int n = 0; n < 2; ++n) gv[bj][n] = *(const f32x4*)(gate + (size_t)cnd * NMOD + col0 + bj * HALF + n * 16) * scale;
; #pragma unroll
;         for (int ai = 0; ai < 2; ++ai)
; #pragma unroll
;             for (int m = 0; m < 4; ++m) { const size_t off = (size_t)(rl0 + ai * HALF + m * 16) * DM + col0;
; #pragma unroll
;                 for (int bj = 0; bj < 2; ++bj)
; #pragma unroll
;                     for (int n = 0; n < 2; ++n) { const f32x4 bs = ldb(bp + off + bj * HALF + n * 16); st4_bf(op + off + bj * HALF + n * 16, bs + gv[bj][n] * acc[ai][bj][m][n]); }
;                 asm volatile("" ::: "memory"); }
;     }
	v_lshlrev_b32_e32 v24, 16, v34
	v_and_b32_e32 v25, 0xffff0000, v34
	v_lshlrev_b32_e32 v20, 16, v35
	v_and_b32_e32 v21, 0xffff0000, v35
	v_pk_fma_f32 v[24:25], v[122:123], v[4:5], v[24:25]
	v_pk_fma_f32 v[20:21], v[124:125], v[8:9], v[20:21]
	v_cvt_pk_bf16_f32 v24, v24, v25
	s_nop 0
	v_cvt_pk_bf16_f32 v25, v20, v21
	global_store_dwordx2 v[22:23], v[24:25], off offset:32
	s_waitcnt vmcnt(28)
	v_lshlrev_b32_e32 v24, 16, v36
	v_and_b32_e32 v25, 0xffff0000, v36
	v_lshlrev_b32_e32 v20, 16, v37
	v_and_b32_e32 v21, 0xffff0000, v37
	v_pk_fma_f32 v[24:25], v[118:119], v[10:11], v[24:25]
	v_pk_fma_f32 v[20:21], v[120:121], v[14:15], v[20:21]
	v_cvt_pk_bf16_f32 v24, v24, v25
	s_nop 0
	v_cvt_pk_bf16_f32 v25, v20, v21
	global_store_dwordx2 v[22:23], v[24:25], off offset:256
	v_lshl_add_u64 v[24:25], v[206:207], 0, v[2:3]
	v_lshlrev_b64 v[24:25], 1, v[24:25]
	v_lshl_add_u64 v[26:27], s[28:29], 0, v[24:25]
	s_waitcnt vmcnt(27)
	v_lshlrev_b32_e32 v28, 16, v38
	v_and_b32_e32 v29, 0xffff0000, v38
	v_lshlrev_b32_e32 v20, 16, v39
	v_and_b32_e32 v21, 0xffff0000, v39
	v_pk_fma_f32 v[28:29], v[110:111], v[16:17], v[28:29]
	v_pk_fma_f32 v[20:21], v[112:113], v[18:19], v[20:21]
	v_cvt_pk_bf16_f32 v28, v28, v29
	s_nop 0
	v_cvt_pk_bf16_f32 v29, v20, v21
	global_store_dwordx2 v[22:23], v[28:29], off offset:288
	v_lshl_add_u64 v[22:23], s[26:27], 0, v[24:25]
	s_waitcnt vmcnt(26)
	v_lshlrev_b32_e32 v24, 16, v40
	v_and_b32_e32 v25, 0xffff0000, v40
	v_lshlrev_b32_e32 v20, 16, v41
	v_and_b32_e32 v21, 0xffff0000, v41
	v_pk_fma_f32 v[24:25], v[114:115], v[6:7], v[24:25]
	v_pk_fma_f32 v[20:21], v[116:117], v[12:13], v[20:21]
	v_cvt_pk_bf16_f32 v24, v24, v25
	s_nop 0
	v_cvt_pk_bf16_f32 v25, v20, v21
	global_store_dwordx2 v[22:23], v[24:25], off
	s_waitcnt vmcnt(25)
	v_lshlrev_b32_e32 v24, 16, v42
	v_and_b32_e32 v25, 0xffff0000, v42
	v_lshlrev_b32_e32 v20, 16, v43
	v_and_b32_e32 v21, 0xffff0000, v43
	v_pk_fma_f32 v[24:25], v[106:107], v[4:5], v[24:25]
	v_pk_fma_f32 v[20:21], v[108:109], v[8:9], v[20:21]
	v_cvt_pk_bf16_f32 v24, v24, v25
	s_nop 0
	v_cvt_pk_bf16_f32 v25, v20, v21
	global_store_dwordx2 v[22:23], v[24:25], off offset:32
	s_waitcnt vmcnt(24)
	v_lshlrev_b32_e32 v24, 16, v44
	v_and_b32_e32 v25, 0xffff0000, v44
	v_lshlrev_b32_e32 v20, 16, v45
	v_and_b32_e32 v21, 0xffff0000, v45
	v_pk_fma_f32 v[24:25], v[102:103], v[10:11], v[24:25]
	v_pk_fma_f32 v[20:21], v[104:105], v[14:15], v[20:21]
	v_cvt_pk_bf16_f32 v24, v24, v25
	s_nop 0
	v_cvt_pk_bf16_f32 v25, v20, v21
	global_store_dwordx2 v[22:23], v[24:25], off offset:256
	v_lshl_add_u64 v[24:25], v[208:209], 0, v[2:3]
	v_lshlrev_b64 v[24:25], 1, v[24:25]
	v_lshl_add_u64 v[26:27], s[28:29], 0, v[24:25]
	v_lshl_add_u64 v[2:3], v[210:211], 0, v[2:3]
	v_lshlrev_b64 v[2:3], 1, v[2:3]
	s_waitcnt vmcnt(23)
	v_lshlrev_b32_e32 v28, 16, v46
	v_and_b32_e32 v29, 0xffff0000, v46
	v_lshlrev_b32_e32 v20, 16, v47
	v_and_b32_e32 v21, 0xffff0000, v47
	v_pk_fma_f32 v[28:29], v[94:95], v[16:17], v[28:29]
	v_pk_fma_f32 v[20:21], v[96:97], v[18:19], v[20:21]
	v_cvt_pk_bf16_f32 v28, v28, v29
	s_nop 0
	v_cvt_pk_bf16_f32 v29, v20, v21
	global_store_dwordx2 v[22:23], v[28:29], off offset:288
	v_lshl_add_u64 v[22:23], s[26:27], 0, v[24:25]
	s_waitcnt vmcnt(22)
	v_lshlrev_b32_e32 v24, 16, v48
	v_and_b32_e32 v25, 0xffff0000, v48
	v_lshlrev_b32_e32 v20, 16, v49
	v_and_b32_e32 v21, 0xffff0000, v49
	v_pk_fma_f32 v[24:25], v[98:99], v[6:7], v[24:25]
	v_pk_fma_f32 v[20:21], v[100:101], v[12:13], v[20:21]
	v_cvt_pk_bf16_f32 v24, v24, v25
	s_nop 0
	v_cvt_pk_bf16_f32 v25, v20, v21
	global_store_dwordx2 v[22:23], v[24:25], off
	s_waitcnt vmcnt(21)
	v_lshlrev_b32_e32 v24, 16, v50
	v_and_b32_e32 v25, 0xffff0000, v50
	v_lshlrev_b32_e32 v20, 16, v51
	v_and_b32_e32 v21, 0xffff0000, v51
	v_pk_fma_f32 v[24:25], v[90:91], v[4:5], v[24:25]
	v_pk_fma_f32 v[20:21], v[92:93], v[8:9], v[20:21]
	v_cvt_pk_bf16_f32 v24, v24, v25
	s_nop 0
	v_cvt_pk_bf16_f32 v25, v20, v21
	global_store_dwordx2 v[22:23], v[24:25], off offset:32
	s_waitcnt vmcnt(20)
	v_lshlrev_b32_e32 v24, 16, v52
	v_and_b32_e32 v25, 0xffff0000, v52
	v_lshlrev_b32_e32 v20, 16, v53
	v_and_b32_e32 v21, 0xffff0000, v53
	v_pk_fma_f32 v[24:25], v[86:87], v[10:11], v[24:25]
	v_pk_fma_f32 v[20:21], v[88:89], v[14:15], v[20:21]
	v_cvt_pk_bf16_f32 v24, v24, v25
	s_nop 0
	v_cvt_pk_bf16_f32 v25, v20, v21
	global_store_dwordx2 v[22:23], v[24:25], off offset:256
	v_lshl_add_u64 v[24:25], s[28:29], 0, v[2:3]
	v_lshl_add_u64 v[2:3], s[26:27], 0, v[2:3]
	s_waitcnt vmcnt(19)
	v_lshlrev_b32_e32 v26, 16, v54
	v_and_b32_e32 v27, 0xffff0000, v54
	v_lshlrev_b32_e32 v20, 16, v55
	v_and_b32_e32 v21, 0xffff0000, v55
	v_pk_fma_f32 v[26:27], v[78:79], v[16:17], v[26:27]
	v_pk_fma_f32 v[20:21], v[80:81], v[18:19], v[20:21]
	v_cvt_pk_bf16_f32 v26, v26, v27
	s_nop 0
	v_cvt_pk_bf16_f32 v27, v20, v21
	global_store_dwordx2 v[22:23], v[26:27], off offset:288
	s_waitcnt vmcnt(18)
	v_lshlrev_b32_e32 v22, 16, v56
	v_and_b32_e32 v23, 0xffff0000, v56
	v_lshlrev_b32_e32 v20, 16, v57
	v_and_b32_e32 v21, 0xffff0000, v57
	v_pk_fma_f32 v[6:7], v[82:83], v[6:7], v[22:23]
	v_pk_fma_f32 v[12:13], v[84:85], v[12:13], v[20:21]
	v_cvt_pk_bf16_f32 v6, v6, v7
	s_nop 0
	v_cvt_pk_bf16_f32 v7, v12, v13
	global_store_dwordx2 v[2:3], v[6:7], off
	s_waitcnt vmcnt(17)
	v_lshlrev_b32_e32 v12, 16, v58
	v_and_b32_e32 v13, 0xffff0000, v58
	v_lshlrev_b32_e32 v6, 16, v59
	v_and_b32_e32 v7, 0xffff0000, v59
	v_pk_fma_f32 v[4:5], v[74:75], v[4:5], v[12:13]
	v_pk_fma_f32 v[6:7], v[76:77], v[8:9], v[6:7]
	v_cvt_pk_bf16_f32 v4, v4, v5
	s_nop 0
	v_cvt_pk_bf16_f32 v5, v6, v7
	global_store_dwordx2 v[2:3], v[4:5], off offset:32
	s_waitcnt vmcnt(16)
	v_lshlrev_b32_e32 v6, 16, v60
	v_and_b32_e32 v7, 0xffff0000, v60
	v_lshlrev_b32_e32 v4, 16, v61
	v_and_b32_e32 v5, 0xffff0000, v61
	v_pk_fma_f32 v[6:7], v[70:71], v[10:11], v[6:7]
	v_pk_fma_f32 v[4:5], v[72:73], v[14:15], v[4:5]
	v_cvt_pk_bf16_f32 v6, v6, v7
	s_nop 0
	v_cvt_pk_bf16_f32 v7, v4, v5
	global_store_dwordx2 v[2:3], v[6:7], off offset:256
	s_waitcnt vmcnt(15)
	v_lshlrev_b32_e32 v6, 16, v62
	v_and_b32_e32 v7, 0xffff0000, v62
	v_lshlrev_b32_e32 v4, 16, v63
	v_and_b32_e32 v5, 0xffff0000, v63
	v_pk_fma_f32 v[6:7], v[66:67], v[16:17], v[6:7]
	v_pk_fma_f32 v[4:5], v[68:69], v[18:19], v[4:5]
	v_cvt_pk_bf16_f32 v6, v6, v7
	s_nop 0
	v_cvt_pk_bf16_f32 v7, v4, v5
	global_store_dwordx2 v[2:3], v[6:7], off offset:288
	s_cbranch_vccnz .LBB0_1521
	s_andn2_b64 vcc, exec, s[6:7]
	s_cbranch_vccnz .LBB0_1520
	s_barrier
	s_branch .LBB0_1520

; __device__ __forceinline__ unsigned cvt_pk_bf16(float lo, float hi) { unsigned r; asm("v_cvt_pk_bf16_f32 %0, %1, %2" : "=v"(r) : "v"(lo), "v"(hi)); return r; }
; __device__ __forceinline__ float bf_lo(unsigned w) { return __uint_as_float(w << 16); }
; __device__ __forceinline__ float bf_hi(unsigned w) { return __uint_as_float(w & 0xffff0000u); }
;     static __device__ __forceinline__ f32x4 ldb(const bf16_t* p) { return ld4_bf(p); }
; __device__ __forceinline__ f32x4 ld4_bf(const bf16_t* p) { const u32x2 w = *(const u32x2*)p; return (f32x4){bf_lo(w.x), bf_hi(w.x), bf_lo(w.y), bf_hi(w.y)}; }
; __device__ __forceinline__ void st4_bf(bf16_t* p, const f32x4 v) { u32x2 w; w.x = cvt_pk_bf16(v[0], v[1]); w.y = cvt_pk_bf16(v[2], v[3]); *(u32x2*)p = w; }
;     __device__ __forceinline__ void operator()(const AccT& acc, const Unit& u, int wr, int wc, int fr, int fq) const {
;         const int cnd = cond_of(u.orow0);
;         const BT* bp = (u.orow0 < ML) ? bl + (size_t)u.orow0 * DM : bc + (size_t)(u.orow0 - ML) * DM;
;         bf16_t* op = out + (size_t)u.orow0 * DM;
;         const int rl0 = wr * 64 + fr, col0 = u.pn * BM + wc * 32 + 4 * fq;
;         f32x4 gv[2][2];
; #pragma unroll
;         for (int bj = 0; bj < 2; ++bj)
; #pragma unroll
;             for (int n = 0; n < 2; ++n) gv[bj][n] = *(const f32x4*)(gate + (size_t)cnd * NMOD + col0 + bj * HALF + n * 16) * scale;
; #pragma unroll
;         for (int ai = 0; ai < 2; ++ai)
; #pragma unroll
;             for (int m = 0; m < 4; ++m) { const size_t off = (size_t)(rl0 + ai * HALF + m * 16) * DM + col0;
; #pragma unroll
;                 for (int bj = 0; bj < 2; ++bj)
; #pragma unroll
;                     for (int n = 0; n < 2; ++n) { const f32x4 bs = ldb(bp + off + bj * HALF + n * 16); st4_bf(op + off + bj * HALF + n * 16, bs + gv[bj][n] * acc[ai][bj][m][n]); }
;                 asm volatile("" ::: "memory"); }
.LBB0_2269:
	s_min_i32 s10, s24, 0x4000
	v_lshl_or_b32 v146, s60, 8, v197
	s_ashr_i32 s10, s10, 12
	v_ashrrev_i32_e32 v147, 31, v146
	s_mul_hi_i32 s19, s10, 0xc000
	s_mul_i32 s10, s10, 0xc000
	v_lshl_add_u64 v[122:123], v[172:173], 0, v[146:147]
	v_lshlrev_b64 v[148:149], 1, v[122:123]
	s_add_u32 s24, s53, s10
	v_lshl_add_u64 v[150:151], s[26:27], 0, v[148:149]
	s_addc_u32 s25, s54, s19
	global_load_dwordx2 v[206:207], v[150:151], off
	v_lshl_add_u64 v[122:123], v[146:147], 2, s[24:25]
	global_load_dwordx4 v[138:141], v[122:123], off
	s_add_u32 s24, s49, s28
	s_addc_u32 s25, s50, s29
	v_lshl_add_u64 v[148:149], s[24:25], 0, v[148:149]
	global_load_dwordx4 v[134:137], v[122:123], off offset:64
	global_load_dwordx4 v[126:129], v[122:123], off offset:512
	s_nop 0
	global_load_dwordx4 v[122:125], v[122:123], off offset:576
	s_andn2_b64 vcc, exec, s[20:21]
	s_mov_b64 s[20:21], -1
	global_load_dwordx2 v[208:209], v[150:151], off offset:32
	global_load_dwordx2 v[210:211], v[150:151], off offset:256
	global_load_dwordx2 v[212:213], v[150:151], off offset:288
	v_lshl_add_u64 v[156:157], v[174:175], 0, v[146:147]
	v_lshlrev_b64 v[156:157], 1, v[156:157]
	v_lshl_add_u64 v[156:157], s[26:27], 0, v[156:157]
	global_load_dwordx2 v[214:215], v[156:157], off
	global_load_dwordx2 v[216:217], v[156:157], off offset:32
	global_load_dwordx2 v[218:219], v[156:157], off offset:256
	global_load_dwordx2 v[220:221], v[156:157], off offset:288
	v_lshl_add_u64 v[156:157], v[176:177], 0, v[146:147]
	v_lshlrev_b64 v[156:157], 1, v[156:157]
	v_lshl_add_u64 v[156:157], s[26:27], 0, v[156:157]
	global_load_dwordx2 v[222:223], v[156:157], off
	global_load_dwordx2 v[224:225], v[156:157], off offset:32
	global_load_dwordx2 v[226:227], v[156:157], off offset:256
	global_load_dwordx2 v[228:229], v[156:157], off offset:288
	v_lshl_add_u64 v[156:157], v[178:179], 0, v[146:147]
	v_lshlrev_b64 v[156:157], 1, v[156:157]
	v_lshl_add_u64 v[156:157], s[26:27], 0, v[156:157]
	global_load_dwordx2 v[230:231], v[156:157], off
	global_load_dwordx2 v[232:233], v[156:157], off offset:32
	global_load_dwordx2 v[234:235], v[156:157], off offset:256
	global_load_dwordx2 v[236:237], v[156:157], off offset:288
	s_waitcnt vmcnt(15)
	v_lshlrev_b32_e32 v154, 16, v206
	v_and_b32_e32 v155, 0xffff0000, v206
	v_lshlrev_b32_e32 v152, 16, v207
	v_and_b32_e32 v153, 0xffff0000, v207
	v_pk_fma_f32 v[142:143], v[142:143], v[138:139], v[154:155]
	v_pk_fma_f32 v[144:145], v[144:145], v[140:141], v[152:153]
	v_cvt_pk_bf16_f32 v142, v142, v143
	s_nop 0
	v_cvt_pk_bf16_f32 v143, v144, v145
	global_store_dwordx2 v[148:149], v[142:143], off
	v_lshl_add_u64 v[156:157], v[180:181], 0, v[146:147]
	v_lshlrev_b64 v[156:157], 1, v[156:157]
	v_lshl_add_u64 v[156:157], s[26:27], 0, v[156:157]
	global_load_dwordx2 v[206:207], v[156:157], off
	s_waitcnt vmcnt(16)
	v_lshlrev_b32_e32 v144, 16, v208
	v_and_b32_e32 v145, 0xffff0000, v208
	v_lshlrev_b32_e32 v142, 16, v209
	v_and_b32_e32 v143, 0xffff0000, v209
	v_pk_fma_f32 v[130:131], v[130:131], v[134:135], v[144:145]
	v_pk_fma_f32 v[132:133], v[132:133], v[136:137], v[142:143]
	v_cvt_pk_bf16_f32 v130, v130, v131
	s_nop 0
	v_cvt_pk_bf16_f32 v131, v132, v133
	global_store_dwordx2 v[148:149], v[130:131], off offset:32
	global_load_dwordx2 v[208:209], v[156:157], off offset:32
	s_waitcnt vmcnt(17)
	v_lshlrev_b32_e32 v132, 16, v210
	v_and_b32_e32 v133, 0xffff0000, v210
	v_lshlrev_b32_e32 v130, 16, v211
	v_and_b32_e32 v131, 0xffff0000, v211
	v_pk_fma_f32 v[118:119], v[118:119], v[126:127], v[132:133]
	v_pk_fma_f32 v[120:121], v[120:121], v[128:129], v[130:131]
	v_cvt_pk_bf16_f32 v118, v118, v119
	s_nop 0
	v_cvt_pk_bf16_f32 v119, v120, v121
	global_store_dwordx2 v[148:149], v[118:119], off offset:256
	global_load_dwordx2 v[210:211], v[156:157], off offset:256
	v_lshl_add_u64 v[120:121], v[174:175], 0, v[146:147]
	v_lshlrev_b64 v[120:121], 1, v[120:121]
	v_lshl_add_u64 v[130:131], s[26:27], 0, v[120:121]
	s_waitcnt vmcnt(18)
	v_lshlrev_b32_e32 v132, 16, v212
	v_and_b32_e32 v133, 0xffff0000, v212
	v_lshlrev_b32_e32 v118, 16, v213
	v_and_b32_e32 v119, 0xffff0000, v213
	v_pk_fma_f32 v[110:111], v[110:111], v[122:123], v[132:133]
	v_pk_fma_f32 v[112:113], v[112:113], v[124:125], v[118:119]
	v_cvt_pk_bf16_f32 v110, v110, v111
	s_nop 0
	v_cvt_pk_bf16_f32 v111, v112, v113
	global_store_dwordx2 v[148:149], v[110:111], off offset:288
	global_load_dwordx2 v[212:213], v[156:157], off offset:288
	v_lshl_add_u64 v[112:113], s[24:25], 0, v[120:121]
	s_waitcnt vmcnt(19)
	v_lshlrev_b32_e32 v118, 16, v214
	v_and_b32_e32 v119, 0xffff0000, v214
	v_lshlrev_b32_e32 v110, 16, v215
	v_and_b32_e32 v111, 0xffff0000, v215
	v_pk_fma_f32 v[114:115], v[114:115], v[138:139], v[118:119]
	v_pk_fma_f32 v[110:111], v[116:117], v[140:141], v[110:111]
	v_cvt_pk_bf16_f32 v114, v114, v115
	s_nop 0
	v_cvt_pk_bf16_f32 v115, v110, v111
	global_store_dwordx2 v[112:113], v[114:115], off
	v_lshl_add_u64 v[156:157], v[182:183], 0, v[146:147]
	v_lshlrev_b64 v[156:157], 1, v[156:157]
	v_lshl_add_u64 v[156:157], s[26:27], 0, v[156:157]
	global_load_dwordx2 v[214:215], v[156:157], off
	s_waitcnt vmcnt(20)
	v_lshlrev_b32_e32 v114, 16, v216
	v_and_b32_e32 v115, 0xffff0000, v216
	v_lshlrev_b32_e32 v110, 16, v217
	v_and_b32_e32 v111, 0xffff0000, v217
	v_pk_fma_f32 v[106:107], v[106:107], v[134:135], v[114:115]
	v_pk_fma_f32 v[108:109], v[108:109], v[136:137], v[110:111]
	v_cvt_pk_bf16_f32 v106, v106, v107
	s_nop 0
	v_cvt_pk_bf16_f32 v107, v108, v109
	global_store_dwordx2 v[112:113], v[106:107], off offset:32
	global_load_dwordx2 v[216:217], v[156:157], off offset:32
	s_waitcnt vmcnt(21)
; __device__ __forceinline__ unsigned cvt_pk_bf16(float lo, float hi) { unsigned r; asm("v_cvt_pk_bf16_f32 %0, %1, %2" : "=v"(r) : "v"(lo), "v"(hi)); return r; }
; __device__ __forceinline__ float bf_lo(unsigned w) { return __uint_as_float(w << 16); }
; __device__ __forceinline__ float bf_hi(unsigned w) { return __uint_as_float(w & 0xffff0000u); }
;     static __device__ __forceinline__ f32x4 ldb(const bf16_t* p) { return ld4_bf(p); }
; __device__ __forceinline__ f32x4 ld4_bf(const bf16_t* p) { const u32x2 w = *(const u32x2*)p; return (f32x4){bf_lo(w.x), bf_hi(w.x), bf_lo(w.y), bf_hi(w.y)}; }
; __device__ __forceinline__ void st4_bf(bf16_t* p, const f32x4 v) { u32x2 w; w.x = cvt_pk_bf16(v[0], v[1]); w.y = cvt_pk_bf16(v[2], v[3]); *(u32x2*)p = w; }
;     __device__ __forceinline__ void operator()(const AccT& acc, const Unit& u, int wr, int wc, int fr, int fq) const {
;     ...
;         for (int ai = 0; ai < 2; ++ai)
; #pragma unroll
;             for (int m = 0; m < 4; ++m) { const size_t off = (size_t)(rl0 + ai * HALF + m * 16) * DM + col0;
; #pragma unroll
;                 for (int bj = 0; bj < 2; ++bj)
; #pragma unroll
;                     for (int n = 0; n < 2; ++n) { const f32x4 bs = ldb(bp + off + bj * HALF + n * 16); st4_bf(op + off + bj * HALF + n * 16, bs + gv[bj][n] * acc[ai][bj][m][n]); }
;                 asm volatile("" ::: "memory"); }
	v_lshlrev_b32_e32 v108, 16, v218
	v_and_b32_e32 v109, 0xffff0000, v218
	v_lshlrev_b32_e32 v106, 16, v219
	v_and_b32_e32 v107, 0xffff0000, v219
	v_pk_fma_f32 v[102:103], v[102:103], v[126:127], v[108:109]
	v_pk_fma_f32 v[104:105], v[104:105], v[128:129], v[106:107]
	v_cvt_pk_bf16_f32 v102, v102, v103
	s_nop 0
	v_cvt_pk_bf16_f32 v103, v104, v105
	global_store_dwordx2 v[112:113], v[102:103], off offset:256
	global_load_dwordx2 v[218:219], v[156:157], off offset:256
	v_lshl_add_u64 v[104:105], v[176:177], 0, v[146:147]
	v_lshlrev_b64 v[104:105], 1, v[104:105]
	v_lshl_add_u64 v[106:107], s[26:27], 0, v[104:105]
	s_waitcnt vmcnt(22)
	v_lshlrev_b32_e32 v108, 16, v220
	v_and_b32_e32 v109, 0xffff0000, v220
	v_lshlrev_b32_e32 v102, 16, v221
	v_and_b32_e32 v103, 0xffff0000, v221
	v_pk_fma_f32 v[94:95], v[94:95], v[122:123], v[108:109]
	v_pk_fma_f32 v[96:97], v[96:97], v[124:125], v[102:103]
	v_cvt_pk_bf16_f32 v94, v94, v95
	s_nop 0
	v_cvt_pk_bf16_f32 v95, v96, v97
	global_store_dwordx2 v[112:113], v[94:95], off offset:288
	global_load_dwordx2 v[220:221], v[156:157], off offset:288
	v_lshl_add_u64 v[96:97], s[24:25], 0, v[104:105]
	s_waitcnt vmcnt(23)
	v_lshlrev_b32_e32 v102, 16, v222
	v_and_b32_e32 v103, 0xffff0000, v222
	v_lshlrev_b32_e32 v94, 16, v223
	v_and_b32_e32 v95, 0xffff0000, v223
	v_pk_fma_f32 v[98:99], v[98:99], v[138:139], v[102:103]
	v_pk_fma_f32 v[94:95], v[100:101], v[140:141], v[94:95]
	v_cvt_pk_bf16_f32 v98, v98, v99
	s_nop 0
	v_cvt_pk_bf16_f32 v99, v94, v95
	global_store_dwordx2 v[96:97], v[98:99], off
	v_lshl_add_u64 v[156:157], v[184:185], 0, v[146:147]
	v_lshlrev_b64 v[156:157], 1, v[156:157]
	v_lshl_add_u64 v[156:157], s[26:27], 0, v[156:157]
	global_load_dwordx2 v[222:223], v[156:157], off
	s_waitcnt vmcnt(24)
	v_lshlrev_b32_e32 v98, 16, v224
	v_and_b32_e32 v99, 0xffff0000, v224
	v_lshlrev_b32_e32 v94, 16, v225
	v_and_b32_e32 v95, 0xffff0000, v225
	v_pk_fma_f32 v[90:91], v[90:91], v[134:135], v[98:99]
	v_pk_fma_f32 v[92:93], v[92:93], v[136:137], v[94:95]
	v_cvt_pk_bf16_f32 v90, v90, v91
	s_nop 0
	v_cvt_pk_bf16_f32 v91, v92, v93
	global_store_dwordx2 v[96:97], v[90:91], off offset:32
	global_load_dwordx2 v[224:225], v[156:157], off offset:32
	s_waitcnt vmcnt(25)
	v_lshlrev_b32_e32 v92, 16, v226
	v_and_b32_e32 v93, 0xffff0000, v226
	v_lshlrev_b32_e32 v90, 16, v227
	v_and_b32_e32 v91, 0xffff0000, v227
	v_pk_fma_f32 v[86:87], v[86:87], v[126:127], v[92:93]
	v_pk_fma_f32 v[88:89], v[88:89], v[128:129], v[90:91]
	v_cvt_pk_bf16_f32 v86, v86, v87
	s_nop 0
	v_cvt_pk_bf16_f32 v87, v88, v89
	global_store_dwordx2 v[96:97], v[86:87], off offset:256
	global_load_dwordx2 v[226:227], v[156:157], off offset:256
	v_lshl_add_u64 v[88:89], v[178:179], 0, v[146:147]
	v_lshlrev_b64 v[88:89], 1, v[88:89]
	v_lshl_add_u64 v[90:91], s[26:27], 0, v[88:89]
	s_waitcnt vmcnt(26)
	v_lshlrev_b32_e32 v92, 16, v228
	v_and_b32_e32 v93, 0xffff0000, v228
	v_lshlrev_b32_e32 v86, 16, v229
	v_and_b32_e32 v87, 0xffff0000, v229
	v_pk_fma_f32 v[78:79], v[78:79], v[122:123], v[92:93]
	v_pk_fma_f32 v[80:81], v[80:81], v[124:125], v[86:87]
	v_cvt_pk_bf16_f32 v78, v78, v79
	s_nop 0
	v_cvt_pk_bf16_f32 v79, v80, v81
	global_store_dwordx2 v[96:97], v[78:79], off offset:288
	global_load_dwordx2 v[228:229], v[156:157], off offset:288
	v_lshl_add_u64 v[80:81], s[24:25], 0, v[88:89]
	s_waitcnt vmcnt(27)
	v_lshlrev_b32_e32 v86, 16, v230
	v_and_b32_e32 v87, 0xffff0000, v230
	v_lshlrev_b32_e32 v78, 16, v231
	v_and_b32_e32 v79, 0xffff0000, v231
	v_pk_fma_f32 v[82:83], v[82:83], v[138:139], v[86:87]
	v_pk_fma_f32 v[78:79], v[84:85], v[140:141], v[78:79]
	v_cvt_pk_bf16_f32 v82, v82, v83
	s_nop 0
	v_cvt_pk_bf16_f32 v83, v78, v79
	global_store_dwordx2 v[80:81], v[82:83], off
	v_lshl_add_u64 v[156:157], v[186:187], 0, v[146:147]
	v_lshlrev_b64 v[156:157], 1, v[156:157]
	v_lshl_add_u64 v[156:157], s[26:27], 0, v[156:157]
	global_load_dwordx2 v[230:231], v[156:157], off
	s_waitcnt vmcnt(28)
	v_lshlrev_b32_e32 v82, 16, v232
	v_and_b32_e32 v83, 0xffff0000, v232
	v_lshlrev_b32_e32 v78, 16, v233
	v_and_b32_e32 v79, 0xffff0000, v233
	v_pk_fma_f32 v[74:75], v[74:75], v[134:135], v[82:83]
	v_pk_fma_f32 v[76:77], v[76:77], v[136:137], v[78:79]
	v_cvt_pk_bf16_f32 v74, v74, v75
	s_nop 0
	v_cvt_pk_bf16_f32 v75, v76, v77
	global_store_dwordx2 v[80:81], v[74:75], off offset:32
	global_load_dwordx2 v[232:233], v[156:157], off offset:32
	s_waitcnt vmcnt(29)
	v_lshlrev_b32_e32 v76, 16, v234
	v_and_b32_e32 v77, 0xffff0000, v234
	v_lshlrev_b32_e32 v74, 16, v235
	v_and_b32_e32 v75, 0xffff0000, v235
	v_pk_fma_f32 v[70:71], v[70:71], v[126:127], v[76:77]
	v_pk_fma_f32 v[72:73], v[72:73], v[128:129], v[74:75]
	v_cvt_pk_bf16_f32 v70, v70, v71
	s_nop 0
	v_cvt_pk_bf16_f32 v71, v72, v73
	global_store_dwordx2 v[80:81], v[70:71], off offset:256
	global_load_dwordx2 v[234:235], v[156:157], off offset:256
	v_lshl_add_u64 v[72:73], v[180:181], 0, v[146:147]
	v_lshlrev_b64 v[72:73], 1, v[72:73]
	v_lshl_add_u64 v[74:75], s[26:27], 0, v[72:73]
	s_waitcnt vmcnt(30)
	v_lshlrev_b32_e32 v76, 16, v236
	v_and_b32_e32 v77, 0xffff0000, v236
	v_lshlrev_b32_e32 v70, 16, v237
	v_and_b32_e32 v71, 0xffff0000, v237
	v_pk_fma_f32 v[66:67], v[66:67], v[122:123], v[76:77]
	v_pk_fma_f32 v[68:69], v[68:69], v[124:125], v[70:71]
	v_cvt_pk_bf16_f32 v66, v66, v67
	s_nop 0
	v_cvt_pk_bf16_f32 v67, v68, v69
	global_store_dwordx2 v[80:81], v[66:67], off offset:288
	global_load_dwordx2 v[236:237], v[156:157], off offset:288
	v_lshl_add_u64 v[68:69], s[24:25], 0, v[72:73]
	s_waitcnt vmcnt(30)
; __device__ __forceinline__ void st4_bf(bf16_t* p, const f32x4 v) { u32x2 w; w.x = cvt_pk_bf16(v[0], v[1]); w.y = cvt_pk_bf16(v[2], v[3]); *(u32x2*)p = w; }
;     static __device__ __forceinline__ f32x4 ldb(const bf16_t* p) { return ld4_bf(p); }
;     __device__ __forceinline__ void operator()(const AccT& acc, const Unit& u, int wr, int wc, int fr, int fq) const {
;     ...
;         for (int ai = 0; ai < 2; ++ai)
; #pragma unroll
;             for (int m = 0; m < 4; ++m) { const size_t off = (size_t)(rl0 + ai * HALF + m * 16) * DM + col0;
; #pragma unroll
;                 for (int bj = 0; bj < 2; ++bj)
; #pragma unroll
;                     for (int n = 0; n < 2; ++n) { const f32x4 bs = ldb(bp + off + bj * HALF + n * 16); st4_bf(op + off + bj * HALF + n * 16, bs + gv[bj][n] * acc[ai][bj][m][n]); }
;                 asm volatile("" ::: "memory"); }
;     }
	v_lshlrev_b32_e32 v70, 16, v206
	v_and_b32_e32 v71, 0xffff0000, v206
	v_lshlrev_b32_e32 v66, 16, v207
	v_and_b32_e32 v67, 0xffff0000, v207
	v_pk_fma_f32 v[62:63], v[62:63], v[138:139], v[70:71]
	v_pk_fma_f32 v[64:65], v[64:65], v[140:141], v[66:67]
	v_cvt_pk_bf16_f32 v62, v62, v63
	s_nop 0
	v_cvt_pk_bf16_f32 v63, v64, v65
	global_store_dwordx2 v[68:69], v[62:63], off
	s_waitcnt vmcnt(29)
	v_lshlrev_b32_e32 v64, 16, v208
	v_and_b32_e32 v65, 0xffff0000, v208
	v_lshlrev_b32_e32 v62, 16, v209
	v_and_b32_e32 v63, 0xffff0000, v209
	v_pk_fma_f32 v[58:59], v[58:59], v[134:135], v[64:65]
	v_pk_fma_f32 v[60:61], v[60:61], v[136:137], v[62:63]
	v_cvt_pk_bf16_f32 v58, v58, v59
	s_nop 0
	v_cvt_pk_bf16_f32 v59, v60, v61
	global_store_dwordx2 v[68:69], v[58:59], off offset:32
	s_waitcnt vmcnt(28)
	v_lshlrev_b32_e32 v60, 16, v210
	v_and_b32_e32 v61, 0xffff0000, v210
	v_lshlrev_b32_e32 v58, 16, v211
	v_and_b32_e32 v59, 0xffff0000, v211
	v_pk_fma_f32 v[54:55], v[54:55], v[126:127], v[60:61]
	v_pk_fma_f32 v[56:57], v[56:57], v[128:129], v[58:59]
	v_cvt_pk_bf16_f32 v54, v54, v55
	s_nop 0
	v_cvt_pk_bf16_f32 v55, v56, v57
	global_store_dwordx2 v[68:69], v[54:55], off offset:256
	v_lshl_add_u64 v[56:57], v[182:183], 0, v[146:147]
	v_lshlrev_b64 v[56:57], 1, v[56:57]
	v_lshl_add_u64 v[58:59], s[26:27], 0, v[56:57]
	s_waitcnt vmcnt(27)
	v_lshlrev_b32_e32 v60, 16, v212
	v_and_b32_e32 v61, 0xffff0000, v212
	v_lshlrev_b32_e32 v54, 16, v213
	v_and_b32_e32 v55, 0xffff0000, v213
	v_pk_fma_f32 v[46:47], v[46:47], v[122:123], v[60:61]
	v_pk_fma_f32 v[48:49], v[48:49], v[124:125], v[54:55]
	v_cvt_pk_bf16_f32 v46, v46, v47
	s_nop 0
	v_cvt_pk_bf16_f32 v47, v48, v49
	global_store_dwordx2 v[68:69], v[46:47], off offset:288
	v_lshl_add_u64 v[48:49], s[24:25], 0, v[56:57]
	s_waitcnt vmcnt(26)
	v_lshlrev_b32_e32 v54, 16, v214
	v_and_b32_e32 v55, 0xffff0000, v214
	v_lshlrev_b32_e32 v46, 16, v215
	v_and_b32_e32 v47, 0xffff0000, v215
	v_pk_fma_f32 v[50:51], v[50:51], v[138:139], v[54:55]
	v_pk_fma_f32 v[46:47], v[52:53], v[140:141], v[46:47]
	v_cvt_pk_bf16_f32 v50, v50, v51
	s_nop 0
	v_cvt_pk_bf16_f32 v51, v46, v47
	global_store_dwordx2 v[48:49], v[50:51], off
	s_waitcnt vmcnt(25)
	v_lshlrev_b32_e32 v50, 16, v216
	v_and_b32_e32 v51, 0xffff0000, v216
	v_lshlrev_b32_e32 v46, 16, v217
	v_and_b32_e32 v47, 0xffff0000, v217
	v_pk_fma_f32 v[42:43], v[42:43], v[134:135], v[50:51]
	v_pk_fma_f32 v[44:45], v[44:45], v[136:137], v[46:47]
	v_cvt_pk_bf16_f32 v42, v42, v43
	s_nop 0
	v_cvt_pk_bf16_f32 v43, v44, v45
	global_store_dwordx2 v[48:49], v[42:43], off offset:32
	s_waitcnt vmcnt(24)
	v_lshlrev_b32_e32 v44, 16, v218
	v_and_b32_e32 v45, 0xffff0000, v218
	v_lshlrev_b32_e32 v42, 16, v219
	v_and_b32_e32 v43, 0xffff0000, v219
	v_pk_fma_f32 v[38:39], v[38:39], v[126:127], v[44:45]
	v_pk_fma_f32 v[40:41], v[40:41], v[128:129], v[42:43]
	v_cvt_pk_bf16_f32 v38, v38, v39
	s_nop 0
	v_cvt_pk_bf16_f32 v39, v40, v41
	global_store_dwordx2 v[48:49], v[38:39], off offset:256
	v_lshl_add_u64 v[40:41], v[184:185], 0, v[146:147]
	v_lshlrev_b64 v[40:41], 1, v[40:41]
	v_lshl_add_u64 v[42:43], s[26:27], 0, v[40:41]
	s_waitcnt vmcnt(23)
	v_lshlrev_b32_e32 v44, 16, v220
	v_and_b32_e32 v45, 0xffff0000, v220
	v_lshlrev_b32_e32 v38, 16, v221
	v_and_b32_e32 v39, 0xffff0000, v221
	v_pk_fma_f32 v[30:31], v[30:31], v[122:123], v[44:45]
	v_pk_fma_f32 v[32:33], v[32:33], v[124:125], v[38:39]
	v_cvt_pk_bf16_f32 v30, v30, v31
	s_nop 0
	v_cvt_pk_bf16_f32 v31, v32, v33
	global_store_dwordx2 v[48:49], v[30:31], off offset:288
	v_lshl_add_u64 v[32:33], s[24:25], 0, v[40:41]
	s_waitcnt vmcnt(22)
	v_lshlrev_b32_e32 v38, 16, v222
	v_and_b32_e32 v39, 0xffff0000, v222
	v_lshlrev_b32_e32 v30, 16, v223
	v_and_b32_e32 v31, 0xffff0000, v223
	v_pk_fma_f32 v[34:35], v[34:35], v[138:139], v[38:39]
	v_pk_fma_f32 v[30:31], v[36:37], v[140:141], v[30:31]
	v_cvt_pk_bf16_f32 v34, v34, v35
	s_nop 0
	v_cvt_pk_bf16_f32 v35, v30, v31
	global_store_dwordx2 v[32:33], v[34:35], off
	s_waitcnt vmcnt(21)
	v_lshlrev_b32_e32 v34, 16, v224
	v_and_b32_e32 v35, 0xffff0000, v224
	v_lshlrev_b32_e32 v30, 16, v225
	v_and_b32_e32 v31, 0xffff0000, v225
	v_pk_fma_f32 v[26:27], v[26:27], v[134:135], v[34:35]
	v_pk_fma_f32 v[28:29], v[28:29], v[136:137], v[30:31]
	v_cvt_pk_bf16_f32 v26, v26, v27
	s_nop 0
	v_cvt_pk_bf16_f32 v27, v28, v29
	global_store_dwordx2 v[32:33], v[26:27], off offset:32
	s_waitcnt vmcnt(20)
	v_lshlrev_b32_e32 v28, 16, v226
	v_and_b32_e32 v29, 0xffff0000, v226
	v_lshlrev_b32_e32 v26, 16, v227
	v_and_b32_e32 v27, 0xffff0000, v227
	v_pk_fma_f32 v[22:23], v[22:23], v[126:127], v[28:29]
	v_pk_fma_f32 v[24:25], v[24:25], v[128:129], v[26:27]
	v_cvt_pk_bf16_f32 v22, v22, v23
	s_nop 0
	v_cvt_pk_bf16_f32 v23, v24, v25
	global_store_dwordx2 v[32:33], v[22:23], off offset:256
	v_lshl_add_u64 v[24:25], v[186:187], 0, v[146:147]
	v_lshlrev_b64 v[24:25], 1, v[24:25]
	v_lshl_add_u64 v[26:27], s[26:27], 0, v[24:25]
	s_waitcnt vmcnt(19)
	v_lshlrev_b32_e32 v28, 16, v228
	v_and_b32_e32 v29, 0xffff0000, v228
	v_lshlrev_b32_e32 v22, 16, v229
	v_and_b32_e32 v23, 0xffff0000, v229
	v_pk_fma_f32 v[14:15], v[14:15], v[122:123], v[28:29]
	v_pk_fma_f32 v[16:17], v[16:17], v[124:125], v[22:23]
	v_cvt_pk_bf16_f32 v14, v14, v15
	s_nop 0
	v_cvt_pk_bf16_f32 v15, v16, v17
	global_store_dwordx2 v[32:33], v[14:15], off offset:288
	v_lshl_add_u64 v[16:17], s[24:25], 0, v[24:25]
	s_waitcnt vmcnt(18)
	v_lshlrev_b32_e32 v22, 16, v230
	v_and_b32_e32 v23, 0xffff0000, v230
	v_lshlrev_b32_e32 v14, 16, v231
	v_and_b32_e32 v15, 0xffff0000, v231
	v_pk_fma_f32 v[18:19], v[18:19], v[138:139], v[22:23]
	v_pk_fma_f32 v[14:15], v[20:21], v[140:141], v[14:15]
	v_cvt_pk_bf16_f32 v18, v18, v19
	s_nop 0
	v_cvt_pk_bf16_f32 v19, v14, v15
	global_store_dwordx2 v[16:17], v[18:19], off
	s_waitcnt vmcnt(17)
	v_lshlrev_b32_e32 v18, 16, v232
	v_and_b32_e32 v19, 0xffff0000, v232
	v_lshlrev_b32_e32 v14, 16, v233
	v_and_b32_e32 v15, 0xffff0000, v233
	v_pk_fma_f32 v[10:11], v[10:11], v[134:135], v[18:19]
	v_pk_fma_f32 v[12:13], v[12:13], v[136:137], v[14:15]
	v_cvt_pk_bf16_f32 v10, v10, v11
	s_nop 0
	v_cvt_pk_bf16_f32 v11, v12, v13
	global_store_dwordx2 v[16:17], v[10:11], off offset:32
	s_waitcnt vmcnt(16)
	v_lshlrev_b32_e32 v12, 16, v234
	v_and_b32_e32 v13, 0xffff0000, v234
	v_lshlrev_b32_e32 v10, 16, v235
	v_and_b32_e32 v11, 0xffff0000, v235
	v_pk_fma_f32 v[6:7], v[6:7], v[126:127], v[12:13]
	v_pk_fma_f32 v[8:9], v[8:9], v[128:129], v[10:11]
	v_cvt_pk_bf16_f32 v6, v6, v7
	s_nop 0
	v_cvt_pk_bf16_f32 v7, v8, v9
	global_store_dwordx2 v[16:17], v[6:7], off offset:256
	s_waitcnt vmcnt(15)
	v_lshlrev_b32_e32 v8, 16, v236
	v_and_b32_e32 v9, 0xffff0000, v236
	v_lshlrev_b32_e32 v6, 16, v237
	v_and_b32_e32 v7, 0xffff0000, v237
	v_pk_fma_f32 v[2:3], v[2:3], v[122:123], v[8:9]
	v_pk_fma_f32 v[4:5], v[4:5], v[124:125], v[6:7]
	v_cvt_pk_bf16_f32 v2, v2, v3
	s_nop 0
	v_cvt_pk_bf16_f32 v3, v4, v5
	global_store_dwordx2 v[16:17], v[2:3], off offset:288
	s_cbranch_vccnz .LBB0_2249
	s_andn2_b64 vcc, exec, s[6:7]
	s_cbranch_vccnz .LBB0_2248
	s_barrier
	s_branch .LBB0_2248

; __device__ __forceinline__ unsigned cvt4_fp8(float a, float b, float c, float d) { int w = 0; w = __builtin_amdgcn_cvt_pk_fp8_f32(clamp448(a), clamp448(b), w, false); w = __builtin_amdgcn_cvt_pk_fp8_f32(clamp448(c), clamp448(d), w, true); return (unsigned)w; }
; __device__ __forceinline__ float sigmoidf_(float x) { return __builtin_amdgcn_rcpf(1.0f + __expf(-x)); }
; __device__ __forceinline__ float siluf_(float x) { return x * sigmoidf_(x); }
;     __device__ __forceinline__ void operator()(const AccT& acc, const Unit& u, int wr, int wc, int fr, int fq) const {
;         const int rl0 = wr * 64 + fr, cb = u.pn * 128 + wc * 32 + 8 * fq, nb = u.g * 14336 + u.pn * 256 + wc * 32 + 8 * fq;
;         const float* rs_p = rsc + (size_t)u.g * ML + u.pm * BM;
;         f32x4 cg0 = *(const f32x4*)(cmax + nb) * (1.0f / 127.0f), cg1 = *(const f32x4*)(cmax + nb + 4) * (1.0f / 127.0f), cu0 = *(const f32x4*)(cmax + nb + 128) * (1.0f / 127.0f), cu1 = *(const f32x4*)(cmax + nb + 132) * (1.0f / 127.0f);
; #pragma unroll
;         for (int ai = 0; ai < 2; ++ai)
; #pragma unroll
;             for (int m = 0; m < 4; ++m) { const int rl = rl0 + ai * HALF + m * 16; const float rs = rs_p[rl]; f32x4 z0, z1;
;                 const i32x4v g0 = __builtin_bit_cast(i32x4v, acc[ai][0][m][0]), g1 = __builtin_bit_cast(i32x4v, acc[ai][0][m][1]), u0 = __builtin_bit_cast(i32x4v, acc[ai][1][m][0]), u1 = __builtin_bit_cast(i32x4v, acc[ai][1][m][1]);
; #pragma unroll
;                 for (int j = 0; j < 4; ++j) { z0[j] = siluf_((float)g0[j] * (rs * cg0[j])) * ((float)u0[j] * (rs * cu0[j])); z1[j] = siluf_((float)g1[j] * (rs * cg1[j])) * ((float)u1[j] * (rs * cu1[j])); }
;                 u32x2 w; w.x = cvt4_fp8(z0[0] * sout8, z0[1] * sout8, z0[2] * sout8, z0[3] * sout8); w.y = cvt4_fp8(z1[0] * sout8, z1[1] * sout8, z1[2] * sout8, z1[3] * sout8);
;                 *(u32x2*)(O + (size_t)(u.orow0 + rl) * ldo + cb) = w;
;                 __builtin_amdgcn_sched_barrier(0); }
.LBB0_2553:
	v_mul_lo_u32 v130, v168, s70
	s_lshl_b32 s4, s44, 8
	v_add_u32_e32 v130, s4, v130
	v_or_b32_e32 v130, v130, v183
	v_ashrrev_i32_e32 v131, 31, v130
	v_lshl_add_u64 v[130:131], v[130:131], 2, s[24:25]
	v_ashrrev_i32_e32 v169, 31, v168
	s_lshl_b32 s4, s74, 8
	global_load_dwordx4 v[134:137], v[130:131], off offset:512
	global_load_dwordx4 v[138:141], v[130:131], off
	global_load_dwordx4 v[142:145], v[130:131], off offset:528
	global_load_dwordx4 v[146:149], v[130:131], off offset:16
	v_lshlrev_b64 v[130:131], 16, v[168:169]
	s_ashr_i32 s5, s4, 31
	v_lshl_add_u64 v[130:131], s[22:23], 0, v[130:131]
	s_lshl_b64 s[4:5], s[4:5], 2
	v_lshl_add_u64 v[132:133], v[130:131], 0, s[4:5]
	v_cvt_f32_i32_e32 v155, v118
	v_readfirstlane_b32 s4, v132
	v_readfirstlane_b32 s5, v133
	v_cvt_f32_i32_e32 v154, v114
	v_cvt_f32_i32_e32 v159, v119
	v_cvt_f32_i32_e32 v158, v115
	v_cvt_f32_i32_e32 v153, v126
	v_cvt_f32_i32_e32 v152, v122
	global_load_dword v150, v185, s[4:5]
	global_load_dword v219, v185, s[4:5] offset:64
	global_load_dword v220, v185, s[4:5] offset:128
	global_load_dword v221, v185, s[4:5] offset:192
	global_load_dword v222, v185, s[4:5] offset:512
	global_load_dword v223, v185, s[4:5] offset:576
	global_load_dword v224, v185, s[4:5] offset:640
	global_load_dword v225, v185, s[4:5] offset:704
	v_cvt_f32_i32_e32 v157, v127
	v_cvt_f32_i32_e32 v156, v123
	v_cvt_f32_i32_e32 v160, v124
	v_cvt_f32_i32_e32 v170, v125
	v_cvt_f32_i32_e32 v161, v128
	v_cvt_f32_i32_e32 v169, v120
	v_cvt_f32_i32_e32 v171, v129
	v_cvt_f32_i32_e32 v168, v116
	v_lshl_or_b32 v130, s44, 7, v183
	v_ashrrev_i32_e32 v131, 31, v130
	s_waitcnt vmcnt(0)
	v_mov_b32_e32 v114, v134
	v_mov_b32_e32 v115, v138
	v_mov_b32_e32 v118, v142
	v_mov_b32_e32 v119, v146
	v_mov_b32_e32 v146, v143
	v_mov_b32_e32 v138, v135
	v_pk_mul_f32 v[118:119], v[118:119], s[38:39] op_sel_hi:[1,0]
	v_pk_mul_f32 v[124:125], v[146:147], s[38:39] op_sel_hi:[1,0]
	v_mov_b32_e32 v127, v140
	v_mov_b32_e32 v140, v137
	v_pk_mul_f32 v[114:115], v[114:115], s[38:39] op_sel_hi:[1,0]
	v_pk_mul_f32 v[122:123], v[138:139], s[38:39] op_sel_hi:[1,0]
	v_mov_b32_e32 v126, v136
	v_pk_mul_f32 v[134:135], v[140:141], s[38:39] op_sel_hi:[1,0]
	v_mov_b32_e32 v129, v148
	v_pk_mul_f32 v[126:127], v[126:127], s[38:39] op_sel_hi:[1,0]
	v_mov_b32_e32 v128, v144
	v_pk_mul_f32 v[138:139], v[150:151], v[118:119] op_sel_hi:[0,1]
	v_pk_mul_f32 v[142:143], v[150:151], v[124:125] op_sel_hi:[0,1]
	v_pk_mul_f32 v[136:137], v[150:151], v[114:115] op_sel_hi:[0,1]
	v_pk_mul_f32 v[140:141], v[150:151], v[122:123] op_sel_hi:[0,1]
	v_pk_mul_f32 v[138:139], v[138:139], v[154:155]
	v_pk_mul_f32 v[142:143], v[142:143], v[158:159]
	v_pk_mul_f32 v[136:137], v[136:137], v[152:153]
	v_pk_mul_f32 v[140:141], v[140:141], v[156:157]
	v_mul_f32_e32 v120, 0xbfb8aa3b, v139
	v_mul_f32_e32 v148, 0xbfb8aa3b, v143
	v_pk_mul_f32 v[146:147], v[150:151], v[126:127] op_sel_hi:[0,1]
	v_mul_f32_e32 v116, 0xbfb8aa3b, v137
	v_mul_f32_e32 v144, 0xbfb8aa3b, v141
	v_exp_f32_e32 v120, v120
	v_exp_f32_e32 v148, v148
	v_pk_mul_f32 v[128:129], v[128:129], s[38:39] op_sel_hi:[1,0]
	v_pk_mul_f32 v[146:147], v[146:147], v[160:161]
	v_exp_f32_e32 v116, v116
	v_exp_f32_e32 v144, v144
	v_pk_mul_f32 v[192:193], v[150:151], v[128:129] op_sel_hi:[0,1]
	v_pk_mul_f32 v[194:195], v[150:151], v[134:135] op_sel_hi:[0,1]
	v_mul_f32_e32 v151, 0xbfb8aa3b, v147
	v_exp_f32_e32 v151, v151
	v_add_f32_e32 v120, 1.0, v120
	v_add_f32_e32 v148, 1.0, v148
	v_add_f32_e32 v116, 1.0, v116
	v_add_f32_e32 v144, 1.0, v144
	v_rcp_f32_e32 v120, v120
	v_rcp_f32_e32 v148, v148
	v_rcp_f32_e32 v116, v116
	v_rcp_f32_e32 v144, v144
	v_add_f32_e32 v151, 1.0, v151
	v_rcp_f32_e32 v151, v151
	v_mul_f32_e32 v120, v139, v120
	v_mul_f32_e32 v139, v143, v148
	v_mul_f32_e32 v116, v137, v116
	v_mul_f32_e32 v137, v141, v144
	v_mul_f32_e32 v144, v138, v120
	v_mul_f32_e32 v142, v142, v139
	v_cvt_f32_i32_e32 v139, v121
	v_cvt_f32_i32_e32 v138, v117
	v_mul_f32_e32 v143, v136, v116
	v_mul_f32_e32 v140, v140, v137
	v_pk_mul_f32 v[136:137], v[194:195], v[170:171]
	v_mov_b32_e32 v148, v145
	v_mul_f32_e32 v141, v147, v151
	v_mul_f32_e32 v116, 0xbfb8aa3b, v137
	v_pk_mul_f32 v[120:121], v[148:149], s[38:39] op_sel_hi:[1,0]
	v_mul_f32_e32 v141, v146, v141
	v_exp_f32_e32 v146, v116
	v_pk_mul_f32 v[116:117], v[150:151], v[120:121] op_sel_hi:[0,1]
	v_pk_mul_f32 v[116:117], v[116:117], v[138:139]
	v_pk_mul_f32 v[152:153], v[192:193], v[168:169]
	v_mul_f32_e32 v138, 0xbfb8aa3b, v117
	v_exp_f32_e32 v138, v138
	v_add_f32_e32 v145, 1.0, v146
	v_mul_f32_e32 v154, 0xbfb8aa3b, v153
	v_rcp_f32_e32 v145, v145
	v_add_f32_e32 v138, 1.0, v138
	v_rcp_f32_e32 v138, v138
	v_exp_f32_e32 v154, v154
	v_mul_f32_e32 v137, v137, v145
	v_mul_f32_e32 v136, v136, v137
	v_mul_f32_e32 v117, v117, v138
	v_add_f32_e32 v154, 1.0, v154
	v_mul_f32_e32 v116, v116, v117
	v_mul_f32_e32 v117, 4.0, v143
	v_mul_f32_e32 v137, 4.0, v140
	v_rcp_f32_e32 v154, v154
	v_med3_f32 v117, v117, s71, v187
	v_med3_f32 v137, v137, s71, v187
	v_mov_b32_e32 v138, v163
	v_cvt_pk_fp8_f32 v138, v117, v137
	v_mul_f32_e32 v140, 4.0, v141
	v_mul_f32_e32 v117, 4.0, v136
	v_mul_f32_e32 v139, v153, v154
	v_med3_f32 v136, v140, s71, v187
	v_med3_f32 v117, v117, s71, v187
	v_mul_f32_e32 v139, v152, v139
	v_cvt_pk_fp8_f32 v138, v136, v117 op_sel:[0,0,1]
	v_mul_f32_e32 v117, 4.0, v144
	v_mul_f32_e32 v136, 4.0, v142
	v_mul_f32_e32 v137, 4.0, v139
	v_med3_f32 v117, v117, s71, v187
	v_med3_f32 v136, v136, s71, v187
	v_mov_b32_e32 v139, v163
	v_cvt_pk_fp8_f32 v139, v117, v136
	v_mul_f32_e32 v116, 4.0, v116
	v_med3_f32 v117, v137, s71, v187
	v_med3_f32 v116, v116, s71, v187
	v_cvt_pk_fp8_f32 v139, v117, v116 op_sel:[0,0,1]
; __device__ __forceinline__ unsigned cvt4_fp8(float a, float b, float c, float d) { int w = 0; w = __builtin_amdgcn_cvt_pk_fp8_f32(clamp448(a), clamp448(b), w, false); w = __builtin_amdgcn_cvt_pk_fp8_f32(clamp448(c), clamp448(d), w, true); return (unsigned)w; }
; __device__ __forceinline__ float sigmoidf_(float x) { return __builtin_amdgcn_rcpf(1.0f + __expf(-x)); }
; __device__ __forceinline__ float siluf_(float x) { return x * sigmoidf_(x); }
;     __device__ __forceinline__ void operator()(const AccT& acc, const Unit& u, int wr, int wc, int fr, int fq) const {
;     ...
;             for (int m = 0; m < 4; ++m) { const int rl = rl0 + ai * HALF + m * 16; const float rs = rs_p[rl]; f32x4 z0, z1;
;                 const i32x4v g0 = __builtin_bit_cast(i32x4v, acc[ai][0][m][0]), g1 = __builtin_bit_cast(i32x4v, acc[ai][0][m][1]), u0 = __builtin_bit_cast(i32x4v, acc[ai][1][m][0]), u1 = __builtin_bit_cast(i32x4v, acc[ai][1][m][1]);
; #pragma unroll
;                 for (int j = 0; j < 4; ++j) { z0[j] = siluf_((float)g0[j] * (rs * cg0[j])) * ((float)u0[j] * (rs * cu0[j])); z1[j] = siluf_((float)g1[j] * (rs * cg1[j])) * ((float)u1[j] * (rs * cu1[j])); }
;                 u32x2 w; w.x = cvt4_fp8(z0[0] * sout8, z0[1] * sout8, z0[2] * sout8, z0[3] * sout8); w.y = cvt4_fp8(z1[0] * sout8, z1[1] * sout8, z1[2] * sout8, z1[3] * sout8);
;                 *(u32x2*)(O + (size_t)(u.orow0 + rl) * ldo + cb) = w;
;                 __builtin_amdgcn_sched_barrier(0); }
	v_add_u32_e32 v136, v190, v164
	v_mov_b64_e32 v[116:117], s[20:21]
	v_mad_i64_i32 v[140:141], s[6:7], v136, s72, v[116:117]
	v_lshl_add_u64 v[140:141], v[140:141], 0, v[130:131]
	global_store_dwordx2 v[140:141], v[138:139], off
	v_mov_b32_e32 v138, v219
	v_cvt_f32_i32_e32 v141, v110
	v_cvt_f32_i32_e32 v140, v102
	v_cvt_f32_i32_e32 v111, v111
	v_cvt_f32_i32_e32 v110, v103
	v_cvt_f32_i32_e32 v143, v106
	v_cvt_f32_i32_e32 v142, v98
	v_cvt_f32_i32_e32 v103, v107
	v_cvt_f32_i32_e32 v102, v99
	v_cvt_f32_i32_e32 v99, v112
	v_cvt_f32_i32_e32 v98, v104
	v_cvt_f32_i32_e32 v107, v108
	v_cvt_f32_i32_e32 v106, v100
	v_cvt_f32_i32_e32 v112, v105
	v_cvt_f32_i32_e32 v105, v109
	v_cvt_f32_i32_e32 v104, v101
	v_cvt_f32_i32_e32 v113, v113
	v_mov_b32_e32 v100, v163
	v_mov_b32_e32 v101, v163
	v_pk_mul_f32 v[108:109], v[114:115], v[138:139] op_sel_hi:[1,0]
	v_pk_mul_f32 v[146:147], v[122:123], v[138:139] op_sel_hi:[1,0]
	v_pk_mul_f32 v[144:145], v[118:119], v[138:139] op_sel_hi:[1,0]
	v_pk_mul_f32 v[148:149], v[124:125], v[138:139] op_sel_hi:[1,0]
	v_pk_mul_f32 v[150:151], v[126:127], v[138:139] op_sel_hi:[1,0]
	v_pk_mul_f32 v[152:153], v[128:129], v[138:139] op_sel_hi:[1,0]
	v_pk_mul_f32 v[154:155], v[134:135], v[138:139] op_sel_hi:[1,0]
	v_pk_mul_f32 v[138:139], v[120:121], v[138:139] op_sel_hi:[1,0]
	v_pk_mul_f32 v[108:109], v[108:109], v[140:141]
	v_pk_mul_f32 v[110:111], v[146:147], v[110:111]
	v_pk_mul_f32 v[140:141], v[144:145], v[142:143]
	v_pk_mul_f32 v[102:103], v[148:149], v[102:103]
	v_pk_mul_f32 v[98:99], v[150:151], v[98:99]
	v_pk_mul_f32 v[106:107], v[152:153], v[106:107]
	v_pk_mul_f32 v[104:105], v[138:139], v[104:105]
	v_mul_f32_e32 v137, 0xbfb8aa3b, v109
	v_mul_f32_e32 v139, 0xbfb8aa3b, v111
	v_mul_f32_e32 v138, 0xbfb8aa3b, v141
	v_mul_f32_e32 v142, 0xbfb8aa3b, v103
	v_mul_f32_e32 v143, 0xbfb8aa3b, v99
	v_mul_f32_e32 v144, 0xbfb8aa3b, v107
	v_mul_f32_e32 v146, 0xbfb8aa3b, v105
	v_exp_f32_e32 v137, v137
	v_exp_f32_e32 v139, v139
	v_exp_f32_e32 v138, v138
	v_exp_f32_e32 v142, v142
	v_exp_f32_e32 v143, v143
	v_exp_f32_e32 v144, v144
	v_exp_f32_e32 v146, v146
	v_pk_mul_f32 v[112:113], v[154:155], v[112:113]
	v_add_f32_e32 v137, 1.0, v137
	v_mul_f32_e32 v145, 0xbfb8aa3b, v113
	v_exp_f32_e32 v145, v145
	v_add_f32_e32 v139, 1.0, v139
	v_add_f32_e32 v138, 1.0, v138
	v_add_f32_e32 v142, 1.0, v142
	v_add_f32_e32 v143, 1.0, v143
	v_add_f32_e32 v144, 1.0, v144
	v_add_f32_e32 v146, 1.0, v146
	v_rcp_f32_e32 v137, v137
	v_rcp_f32_e32 v139, v139
	v_rcp_f32_e32 v138, v138
	v_rcp_f32_e32 v142, v142
	v_rcp_f32_e32 v143, v143
	v_rcp_f32_e32 v144, v144
	v_rcp_f32_e32 v146, v146
	v_add_f32_e32 v145, 1.0, v145
	v_rcp_f32_e32 v145, v145
	v_mul_f32_e32 v109, v109, v137
	v_mul_f32_e32 v111, v111, v139
	v_mul_f32_e32 v137, v141, v138
	v_mul_f32_e32 v103, v103, v142
	v_mul_f32_e32 v99, v99, v143
	v_mul_f32_e32 v107, v107, v144
	v_mul_f32_e32 v105, v105, v146
	v_mul_f32_e32 v108, v108, v109
	v_mul_f32_e32 v110, v110, v111
	v_mul_f32_e32 v109, v140, v137
	v_mul_f32_e32 v102, v102, v103
	v_mul_f32_e32 v98, v98, v99
	v_mul_f32_e32 v99, v106, v107
	v_mul_f32_e32 v104, v104, v105
	v_mul_f32_e32 v105, 4.0, v108
	v_mul_f32_e32 v106, 4.0, v110
	v_mul_f32_e32 v107, 4.0, v109
	v_mul_f32_e32 v102, 4.0, v102
	v_med3_f32 v105, v105, s71, v187
	v_med3_f32 v106, v106, s71, v187
	v_mul_f32_e32 v113, v113, v145
	v_med3_f32 v107, v107, s71, v187
	v_cvt_pk_fp8_f32 v100, v105, v106
	v_med3_f32 v102, v102, s71, v187
	v_mul_f32_e32 v103, v112, v113
	v_cvt_pk_fp8_f32 v101, v107, v102
	v_mul_f32_e32 v98, 4.0, v98
	v_mul_f32_e32 v103, 4.0, v103
	v_mul_f32_e32 v99, 4.0, v99
	v_mul_f32_e32 v104, 4.0, v104
	v_med3_f32 v98, v98, s71, v187
	v_med3_f32 v103, v103, s71, v187
	v_med3_f32 v99, v99, s71, v187
	v_cvt_pk_fp8_f32 v100, v98, v103 op_sel:[0,0,1]
	v_med3_f32 v98, v104, s71, v187
	v_cvt_pk_fp8_f32 v101, v99, v98 op_sel:[0,0,1]
	v_add_u32_e32 v98, v190, v180
	v_mad_i64_i32 v[98:99], s[6:7], v98, s72, v[116:117]
	v_lshl_add_u64 v[98:99], v[98:99], 0, v[130:131]
	global_store_dwordx2 v[98:99], v[100:101], off
	v_mov_b32_e32 v98, v220
	v_cvt_f32_i32_e32 v101, v94
	v_cvt_f32_i32_e32 v100, v86
	v_cvt_f32_i32_e32 v95, v95
	v_cvt_f32_i32_e32 v94, v87
	v_cvt_f32_i32_e32 v103, v90
	v_cvt_f32_i32_e32 v102, v82
	v_cvt_f32_i32_e32 v87, v91
	v_cvt_f32_i32_e32 v86, v83
	v_cvt_f32_i32_e32 v83, v96
	v_cvt_f32_i32_e32 v82, v88
	v_cvt_f32_i32_e32 v91, v92
	v_cvt_f32_i32_e32 v90, v84
	v_cvt_f32_i32_e32 v96, v89
	v_cvt_f32_i32_e32 v89, v93
	v_cvt_f32_i32_e32 v88, v85
	v_cvt_f32_i32_e32 v97, v97
	v_mov_b32_e32 v84, v163
	v_mov_b32_e32 v85, v163
	v_pk_mul_f32 v[92:93], v[114:115], v[98:99] op_sel_hi:[1,0]
	v_pk_mul_f32 v[106:107], v[122:123], v[98:99] op_sel_hi:[1,0]
	v_pk_mul_f32 v[104:105], v[118:119], v[98:99] op_sel_hi:[1,0]
	v_pk_mul_f32 v[108:109], v[124:125], v[98:99] op_sel_hi:[1,0]
	v_pk_mul_f32 v[110:111], v[126:127], v[98:99] op_sel_hi:[1,0]
	v_pk_mul_f32 v[112:113], v[128:129], v[98:99] op_sel_hi:[1,0]
	v_pk_mul_f32 v[138:139], v[134:135], v[98:99] op_sel_hi:[1,0]
	v_pk_mul_f32 v[98:99], v[120:121], v[98:99] op_sel_hi:[1,0]
	v_pk_mul_f32 v[92:93], v[92:93], v[100:101]
	v_pk_mul_f32 v[94:95], v[106:107], v[94:95]
	v_pk_mul_f32 v[100:101], v[104:105], v[102:103]
	v_pk_mul_f32 v[86:87], v[108:109], v[86:87]
	v_pk_mul_f32 v[82:83], v[110:111], v[82:83]
	v_pk_mul_f32 v[90:91], v[112:113], v[90:91]
	v_pk_mul_f32 v[88:89], v[98:99], v[88:89]
	v_mul_f32_e32 v98, 0xbfb8aa3b, v93
	v_mul_f32_e32 v102, 0xbfb8aa3b, v95
	v_mul_f32_e32 v99, 0xbfb8aa3b, v101
	v_mul_f32_e32 v103, 0xbfb8aa3b, v87
	v_mul_f32_e32 v104, 0xbfb8aa3b, v83
	v_mul_f32_e32 v105, 0xbfb8aa3b, v91
	v_mul_f32_e32 v107, 0xbfb8aa3b, v89
	v_exp_f32_e32 v98, v98
; __device__ __forceinline__ unsigned cvt4_fp8(float a, float b, float c, float d) { int w = 0; w = __builtin_amdgcn_cvt_pk_fp8_f32(clamp448(a), clamp448(b), w, false); w = __builtin_amdgcn_cvt_pk_fp8_f32(clamp448(c), clamp448(d), w, true); return (unsigned)w; }
; __device__ __forceinline__ float sigmoidf_(float x) { return __builtin_amdgcn_rcpf(1.0f + __expf(-x)); }
; __device__ __forceinline__ float siluf_(float x) { return x * sigmoidf_(x); }
;     __device__ __forceinline__ void operator()(const AccT& acc, const Unit& u, int wr, int wc, int fr, int fq) const {
;     ...
;             for (int m = 0; m < 4; ++m) { const int rl = rl0 + ai * HALF + m * 16; const float rs = rs_p[rl]; f32x4 z0, z1;
;                 const i32x4v g0 = __builtin_bit_cast(i32x4v, acc[ai][0][m][0]), g1 = __builtin_bit_cast(i32x4v, acc[ai][0][m][1]), u0 = __builtin_bit_cast(i32x4v, acc[ai][1][m][0]), u1 = __builtin_bit_cast(i32x4v, acc[ai][1][m][1]);
; #pragma unroll
;                 for (int j = 0; j < 4; ++j) { z0[j] = siluf_((float)g0[j] * (rs * cg0[j])) * ((float)u0[j] * (rs * cu0[j])); z1[j] = siluf_((float)g1[j] * (rs * cg1[j])) * ((float)u1[j] * (rs * cu1[j])); }
;                 u32x2 w; w.x = cvt4_fp8(z0[0] * sout8, z0[1] * sout8, z0[2] * sout8, z0[3] * sout8); w.y = cvt4_fp8(z1[0] * sout8, z1[1] * sout8, z1[2] * sout8, z1[3] * sout8);
;                 *(u32x2*)(O + (size_t)(u.orow0 + rl) * ldo + cb) = w;
;                 __builtin_amdgcn_sched_barrier(0); }
	v_exp_f32_e32 v102, v102
	v_exp_f32_e32 v99, v99
	v_exp_f32_e32 v103, v103
	v_exp_f32_e32 v104, v104
	v_exp_f32_e32 v105, v105
	v_exp_f32_e32 v107, v107
	v_pk_mul_f32 v[96:97], v[138:139], v[96:97]
	v_add_f32_e32 v98, 1.0, v98
	v_mul_f32_e32 v106, 0xbfb8aa3b, v97
	v_exp_f32_e32 v106, v106
	v_add_f32_e32 v102, 1.0, v102
	v_add_f32_e32 v99, 1.0, v99
	v_add_f32_e32 v103, 1.0, v103
	v_add_f32_e32 v104, 1.0, v104
	v_add_f32_e32 v105, 1.0, v105
	v_add_f32_e32 v107, 1.0, v107
	v_rcp_f32_e32 v98, v98
	v_rcp_f32_e32 v102, v102
	v_rcp_f32_e32 v99, v99
	v_rcp_f32_e32 v103, v103
	v_rcp_f32_e32 v104, v104
	v_rcp_f32_e32 v105, v105
	v_rcp_f32_e32 v107, v107
	v_add_f32_e32 v106, 1.0, v106
	v_rcp_f32_e32 v106, v106
	v_mul_f32_e32 v93, v93, v98
	v_mul_f32_e32 v95, v95, v102
	v_mul_f32_e32 v98, v101, v99
	v_mul_f32_e32 v87, v87, v103
	v_mul_f32_e32 v83, v83, v104
	v_mul_f32_e32 v91, v91, v105
	v_mul_f32_e32 v89, v89, v107
	v_mul_f32_e32 v92, v92, v93
	v_mul_f32_e32 v94, v94, v95
	v_mul_f32_e32 v93, v100, v98
	v_mul_f32_e32 v86, v86, v87
	v_mul_f32_e32 v82, v82, v83
	v_mul_f32_e32 v83, v90, v91
	v_mul_f32_e32 v88, v88, v89
	v_mul_f32_e32 v89, 4.0, v92
	v_mul_f32_e32 v90, 4.0, v94
	v_mul_f32_e32 v91, 4.0, v93
	v_mul_f32_e32 v86, 4.0, v86
	v_med3_f32 v89, v89, s71, v187
	v_med3_f32 v90, v90, s71, v187
	v_mul_f32_e32 v97, v97, v106
	v_med3_f32 v91, v91, s71, v187
	v_cvt_pk_fp8_f32 v84, v89, v90
	v_med3_f32 v86, v86, s71, v187
	v_mul_f32_e32 v87, v96, v97
	v_cvt_pk_fp8_f32 v85, v91, v86
	v_mul_f32_e32 v82, 4.0, v82
	v_mul_f32_e32 v87, 4.0, v87
	v_mul_f32_e32 v83, 4.0, v83
	v_mul_f32_e32 v88, 4.0, v88
	v_med3_f32 v82, v82, s71, v187
	v_med3_f32 v87, v87, s71, v187
	v_med3_f32 v83, v83, s71, v187
	v_cvt_pk_fp8_f32 v84, v82, v87 op_sel:[0,0,1]
	v_med3_f32 v82, v88, s71, v187
	v_cvt_pk_fp8_f32 v85, v83, v82 op_sel:[0,0,1]
	v_add_u32_e32 v82, v190, v181
	v_mad_i64_i32 v[82:83], s[6:7], v82, s72, v[116:117]
	v_lshl_add_u64 v[82:83], v[82:83], 0, v[130:131]
	global_store_dwordx2 v[82:83], v[84:85], off
	v_mov_b32_e32 v82, v221
	v_cvt_f32_i32_e32 v85, v78
	v_cvt_f32_i32_e32 v84, v70
	v_cvt_f32_i32_e32 v79, v79
	v_cvt_f32_i32_e32 v78, v71
	v_cvt_f32_i32_e32 v87, v74
	v_cvt_f32_i32_e32 v86, v66
	v_cvt_f32_i32_e32 v71, v75
	v_cvt_f32_i32_e32 v70, v67
	v_cvt_f32_i32_e32 v67, v80
	v_cvt_f32_i32_e32 v66, v72
	v_cvt_f32_i32_e32 v75, v76
	v_cvt_f32_i32_e32 v74, v68
	v_cvt_f32_i32_e32 v80, v73
	v_cvt_f32_i32_e32 v73, v77
	v_cvt_f32_i32_e32 v72, v69
	v_cvt_f32_i32_e32 v81, v81
	v_mov_b32_e32 v68, v163
	v_mov_b32_e32 v69, v163
	v_pk_mul_f32 v[76:77], v[114:115], v[82:83] op_sel_hi:[1,0]
	v_pk_mul_f32 v[90:91], v[122:123], v[82:83] op_sel_hi:[1,0]
	v_pk_mul_f32 v[88:89], v[118:119], v[82:83] op_sel_hi:[1,0]
	v_pk_mul_f32 v[92:93], v[124:125], v[82:83] op_sel_hi:[1,0]
	v_pk_mul_f32 v[94:95], v[126:127], v[82:83] op_sel_hi:[1,0]
	v_pk_mul_f32 v[96:97], v[128:129], v[82:83] op_sel_hi:[1,0]
	v_pk_mul_f32 v[98:99], v[134:135], v[82:83] op_sel_hi:[1,0]
	v_pk_mul_f32 v[82:83], v[120:121], v[82:83] op_sel_hi:[1,0]
	v_pk_mul_f32 v[76:77], v[76:77], v[84:85]
	v_pk_mul_f32 v[78:79], v[90:91], v[78:79]
	v_pk_mul_f32 v[84:85], v[88:89], v[86:87]
	v_pk_mul_f32 v[70:71], v[92:93], v[70:71]
	v_pk_mul_f32 v[66:67], v[94:95], v[66:67]
	v_pk_mul_f32 v[74:75], v[96:97], v[74:75]
	v_pk_mul_f32 v[72:73], v[82:83], v[72:73]
	v_mul_f32_e32 v82, 0xbfb8aa3b, v77
	v_mul_f32_e32 v86, 0xbfb8aa3b, v79
	v_mul_f32_e32 v83, 0xbfb8aa3b, v85
	v_mul_f32_e32 v87, 0xbfb8aa3b, v71
	v_mul_f32_e32 v88, 0xbfb8aa3b, v67
	v_mul_f32_e32 v89, 0xbfb8aa3b, v75
	v_mul_f32_e32 v91, 0xbfb8aa3b, v73
	v_exp_f32_e32 v82, v82
	v_exp_f32_e32 v86, v86
	v_exp_f32_e32 v83, v83
	v_exp_f32_e32 v87, v87
	v_exp_f32_e32 v88, v88
	v_exp_f32_e32 v89, v89
	v_exp_f32_e32 v91, v91
	v_pk_mul_f32 v[80:81], v[98:99], v[80:81]
	v_add_f32_e32 v82, 1.0, v82
	v_mul_f32_e32 v90, 0xbfb8aa3b, v81
	v_exp_f32_e32 v90, v90
	v_add_f32_e32 v86, 1.0, v86
	v_add_f32_e32 v83, 1.0, v83
	v_add_f32_e32 v87, 1.0, v87
	v_add_f32_e32 v88, 1.0, v88
	v_add_f32_e32 v89, 1.0, v89
	v_add_f32_e32 v91, 1.0, v91
	v_rcp_f32_e32 v82, v82
	v_rcp_f32_e32 v86, v86
	v_rcp_f32_e32 v83, v83
	v_rcp_f32_e32 v87, v87
	v_rcp_f32_e32 v88, v88
	v_rcp_f32_e32 v89, v89
	v_rcp_f32_e32 v91, v91
	v_add_f32_e32 v90, 1.0, v90
	v_rcp_f32_e32 v90, v90
	v_mul_f32_e32 v77, v77, v82
	v_mul_f32_e32 v79, v79, v86
	v_mul_f32_e32 v82, v85, v83
	v_mul_f32_e32 v71, v71, v87
	v_mul_f32_e32 v67, v67, v88
	v_mul_f32_e32 v75, v75, v89
	v_mul_f32_e32 v73, v73, v91
	v_mul_f32_e32 v76, v76, v77
	v_mul_f32_e32 v78, v78, v79
	v_mul_f32_e32 v77, v84, v82
	v_mul_f32_e32 v70, v70, v71
	v_mul_f32_e32 v66, v66, v67
	v_mul_f32_e32 v67, v74, v75
	v_mul_f32_e32 v72, v72, v73
	v_mul_f32_e32 v73, 4.0, v76
	v_mul_f32_e32 v74, 4.0, v78
	v_mul_f32_e32 v75, 4.0, v77
	v_mul_f32_e32 v70, 4.0, v70
	v_med3_f32 v73, v73, s71, v187
	v_med3_f32 v74, v74, s71, v187
	v_mul_f32_e32 v81, v81, v90
	v_med3_f32 v75, v75, s71, v187
	v_cvt_pk_fp8_f32 v68, v73, v74
	v_med3_f32 v70, v70, s71, v187
	v_mul_f32_e32 v71, v80, v81
	v_cvt_pk_fp8_f32 v69, v75, v70
	v_mul_f32_e32 v66, 4.0, v66
	v_mul_f32_e32 v71, 4.0, v71
	v_mul_f32_e32 v67, 4.0, v67
	v_mul_f32_e32 v72, 4.0, v72
	v_med3_f32 v66, v66, s71, v187
	v_med3_f32 v71, v71, s71, v187
	v_med3_f32 v67, v67, s71, v187
	v_cvt_pk_fp8_f32 v68, v66, v71 op_sel:[0,0,1]
	v_med3_f32 v66, v72, s71, v187
	v_cvt_pk_fp8_f32 v69, v67, v66 op_sel:[0,0,1]
	v_add_u32_e32 v66, v190, v182
	v_mad_i64_i32 v[66:67], s[6:7], v66, s72, v[116:117]
	v_lshl_add_u64 v[66:67], v[66:67], 0, v[130:131]
	global_store_dwordx2 v[66:67], v[68:69], off
	v_mov_b32_e32 v66, v222
	v_cvt_f32_i32_e32 v69, v62
	v_cvt_f32_i32_e32 v68, v54
; __device__ __forceinline__ unsigned cvt4_fp8(float a, float b, float c, float d) { int w = 0; w = __builtin_amdgcn_cvt_pk_fp8_f32(clamp448(a), clamp448(b), w, false); w = __builtin_amdgcn_cvt_pk_fp8_f32(clamp448(c), clamp448(d), w, true); return (unsigned)w; }
; __device__ __forceinline__ float sigmoidf_(float x) { return __builtin_amdgcn_rcpf(1.0f + __expf(-x)); }
; __device__ __forceinline__ float siluf_(float x) { return x * sigmoidf_(x); }
;     __device__ __forceinline__ void operator()(const AccT& acc, const Unit& u, int wr, int wc, int fr, int fq) const {
;     ...
;             for (int m = 0; m < 4; ++m) { const int rl = rl0 + ai * HALF + m * 16; const float rs = rs_p[rl]; f32x4 z0, z1;
;                 const i32x4v g0 = __builtin_bit_cast(i32x4v, acc[ai][0][m][0]), g1 = __builtin_bit_cast(i32x4v, acc[ai][0][m][1]), u0 = __builtin_bit_cast(i32x4v, acc[ai][1][m][0]), u1 = __builtin_bit_cast(i32x4v, acc[ai][1][m][1]);
; #pragma unroll
;                 for (int j = 0; j < 4; ++j) { z0[j] = siluf_((float)g0[j] * (rs * cg0[j])) * ((float)u0[j] * (rs * cu0[j])); z1[j] = siluf_((float)g1[j] * (rs * cg1[j])) * ((float)u1[j] * (rs * cu1[j])); }
;                 u32x2 w; w.x = cvt4_fp8(z0[0] * sout8, z0[1] * sout8, z0[2] * sout8, z0[3] * sout8); w.y = cvt4_fp8(z1[0] * sout8, z1[1] * sout8, z1[2] * sout8, z1[3] * sout8);
;                 *(u32x2*)(O + (size_t)(u.orow0 + rl) * ldo + cb) = w;
;                 __builtin_amdgcn_sched_barrier(0); }
	v_cvt_f32_i32_e32 v63, v63
	v_cvt_f32_i32_e32 v62, v55
	v_cvt_f32_i32_e32 v71, v58
	v_cvt_f32_i32_e32 v70, v50
	v_cvt_f32_i32_e32 v55, v59
	v_cvt_f32_i32_e32 v54, v51
	v_cvt_f32_i32_e32 v51, v64
	v_cvt_f32_i32_e32 v50, v56
	v_cvt_f32_i32_e32 v59, v60
	v_cvt_f32_i32_e32 v58, v52
	v_cvt_f32_i32_e32 v64, v57
	v_cvt_f32_i32_e32 v57, v61
	v_cvt_f32_i32_e32 v56, v53
	v_cvt_f32_i32_e32 v65, v65
	v_mov_b32_e32 v52, v163
	v_mov_b32_e32 v53, v163
	v_pk_mul_f32 v[60:61], v[114:115], v[66:67] op_sel_hi:[1,0]
	v_pk_mul_f32 v[74:75], v[122:123], v[66:67] op_sel_hi:[1,0]
	v_pk_mul_f32 v[72:73], v[118:119], v[66:67] op_sel_hi:[1,0]
	v_pk_mul_f32 v[76:77], v[124:125], v[66:67] op_sel_hi:[1,0]
	v_pk_mul_f32 v[78:79], v[126:127], v[66:67] op_sel_hi:[1,0]
	v_pk_mul_f32 v[80:81], v[128:129], v[66:67] op_sel_hi:[1,0]
	v_pk_mul_f32 v[82:83], v[134:135], v[66:67] op_sel_hi:[1,0]
	v_pk_mul_f32 v[66:67], v[120:121], v[66:67] op_sel_hi:[1,0]
	v_pk_mul_f32 v[60:61], v[60:61], v[68:69]
	v_pk_mul_f32 v[62:63], v[74:75], v[62:63]
	v_pk_mul_f32 v[68:69], v[72:73], v[70:71]
	v_pk_mul_f32 v[54:55], v[76:77], v[54:55]
	v_pk_mul_f32 v[50:51], v[78:79], v[50:51]
	v_pk_mul_f32 v[58:59], v[80:81], v[58:59]
	v_pk_mul_f32 v[56:57], v[66:67], v[56:57]
	v_mul_f32_e32 v66, 0xbfb8aa3b, v61
	v_mul_f32_e32 v70, 0xbfb8aa3b, v63
	v_mul_f32_e32 v67, 0xbfb8aa3b, v69
	v_mul_f32_e32 v71, 0xbfb8aa3b, v55
	v_mul_f32_e32 v72, 0xbfb8aa3b, v51
	v_mul_f32_e32 v73, 0xbfb8aa3b, v59
	v_mul_f32_e32 v75, 0xbfb8aa3b, v57
	v_exp_f32_e32 v66, v66
	v_exp_f32_e32 v70, v70
	v_exp_f32_e32 v67, v67
	v_exp_f32_e32 v71, v71
	v_exp_f32_e32 v72, v72
	v_exp_f32_e32 v73, v73
	v_exp_f32_e32 v75, v75
	v_pk_mul_f32 v[64:65], v[82:83], v[64:65]
	v_add_f32_e32 v66, 1.0, v66
	v_mul_f32_e32 v74, 0xbfb8aa3b, v65
	v_exp_f32_e32 v74, v74
	v_add_f32_e32 v70, 1.0, v70
	v_add_f32_e32 v67, 1.0, v67
	v_add_f32_e32 v71, 1.0, v71
	v_add_f32_e32 v72, 1.0, v72
	v_add_f32_e32 v73, 1.0, v73
	v_add_f32_e32 v75, 1.0, v75
	v_rcp_f32_e32 v66, v66
	v_rcp_f32_e32 v70, v70
	v_rcp_f32_e32 v67, v67
	v_rcp_f32_e32 v71, v71
	v_rcp_f32_e32 v72, v72
	v_rcp_f32_e32 v73, v73
	v_rcp_f32_e32 v75, v75
	v_add_f32_e32 v74, 1.0, v74
	v_rcp_f32_e32 v74, v74
	v_mul_f32_e32 v61, v61, v66
	v_mul_f32_e32 v63, v63, v70
	v_mul_f32_e32 v66, v69, v67
	v_mul_f32_e32 v55, v55, v71
	v_mul_f32_e32 v51, v51, v72
	v_mul_f32_e32 v59, v59, v73
	v_mul_f32_e32 v57, v57, v75
	v_mul_f32_e32 v60, v60, v61
	v_mul_f32_e32 v62, v62, v63
	v_mul_f32_e32 v61, v68, v66
	v_mul_f32_e32 v54, v54, v55
	v_mul_f32_e32 v50, v50, v51
	v_mul_f32_e32 v51, v58, v59
	v_mul_f32_e32 v56, v56, v57
	v_mul_f32_e32 v57, 4.0, v60
	v_mul_f32_e32 v58, 4.0, v62
	v_mul_f32_e32 v59, 4.0, v61
	v_mul_f32_e32 v54, 4.0, v54
	v_med3_f32 v57, v57, s71, v187
	v_med3_f32 v58, v58, s71, v187
	v_mul_f32_e32 v65, v65, v74
	v_med3_f32 v59, v59, s71, v187
	v_cvt_pk_fp8_f32 v52, v57, v58
	v_med3_f32 v54, v54, s71, v187
	v_mul_f32_e32 v55, v64, v65
	v_cvt_pk_fp8_f32 v53, v59, v54
	v_mul_f32_e32 v50, 4.0, v50
	v_mul_f32_e32 v55, 4.0, v55
	v_mul_f32_e32 v51, 4.0, v51
	v_mul_f32_e32 v56, 4.0, v56
	v_med3_f32 v50, v50, s71, v187
	v_med3_f32 v55, v55, s71, v187
	v_med3_f32 v51, v51, s71, v187
	v_cvt_pk_fp8_f32 v52, v50, v55 op_sel:[0,0,1]
	v_med3_f32 v50, v56, s71, v187
	v_cvt_pk_fp8_f32 v53, v51, v50 op_sel:[0,0,1]
	v_add_u32_e32 v50, 0x80, v136
	v_mad_i64_i32 v[50:51], s[6:7], v50, s72, v[116:117]
	v_lshl_add_u64 v[50:51], v[50:51], 0, v[130:131]
	global_store_dwordx2 v[50:51], v[52:53], off
	v_mov_b32_e32 v50, v223
	v_cvt_f32_i32_e32 v53, v46
	v_cvt_f32_i32_e32 v52, v38
	v_cvt_f32_i32_e32 v47, v47
	v_cvt_f32_i32_e32 v46, v39
	v_cvt_f32_i32_e32 v55, v42
	v_cvt_f32_i32_e32 v54, v34
	v_cvt_f32_i32_e32 v39, v43
	v_cvt_f32_i32_e32 v38, v35
	v_cvt_f32_i32_e32 v35, v48
	v_cvt_f32_i32_e32 v34, v40
	v_cvt_f32_i32_e32 v43, v44
	v_cvt_f32_i32_e32 v42, v36
	v_cvt_f32_i32_e32 v48, v41
	v_cvt_f32_i32_e32 v41, v45
	v_cvt_f32_i32_e32 v40, v37
	v_cvt_f32_i32_e32 v49, v49
	v_mov_b32_e32 v36, v163
	v_mov_b32_e32 v37, v163
	v_pk_mul_f32 v[44:45], v[114:115], v[50:51] op_sel_hi:[1,0]
	v_pk_mul_f32 v[58:59], v[122:123], v[50:51] op_sel_hi:[1,0]
	v_pk_mul_f32 v[56:57], v[118:119], v[50:51] op_sel_hi:[1,0]
	v_pk_mul_f32 v[60:61], v[124:125], v[50:51] op_sel_hi:[1,0]
	v_pk_mul_f32 v[62:63], v[126:127], v[50:51] op_sel_hi:[1,0]
	v_pk_mul_f32 v[64:65], v[128:129], v[50:51] op_sel_hi:[1,0]
	v_pk_mul_f32 v[66:67], v[134:135], v[50:51] op_sel_hi:[1,0]
	v_pk_mul_f32 v[50:51], v[120:121], v[50:51] op_sel_hi:[1,0]
	v_pk_mul_f32 v[44:45], v[44:45], v[52:53]
	v_pk_mul_f32 v[46:47], v[58:59], v[46:47]
	v_pk_mul_f32 v[52:53], v[56:57], v[54:55]
	v_pk_mul_f32 v[38:39], v[60:61], v[38:39]
	v_pk_mul_f32 v[34:35], v[62:63], v[34:35]
	v_pk_mul_f32 v[42:43], v[64:65], v[42:43]
	v_pk_mul_f32 v[40:41], v[50:51], v[40:41]
	v_mul_f32_e32 v50, 0xbfb8aa3b, v45
	v_mul_f32_e32 v54, 0xbfb8aa3b, v47
	v_mul_f32_e32 v51, 0xbfb8aa3b, v53
	v_mul_f32_e32 v55, 0xbfb8aa3b, v39
	v_mul_f32_e32 v56, 0xbfb8aa3b, v35
	v_mul_f32_e32 v57, 0xbfb8aa3b, v43
	v_mul_f32_e32 v59, 0xbfb8aa3b, v41
	v_exp_f32_e32 v50, v50
	v_exp_f32_e32 v54, v54
	v_exp_f32_e32 v51, v51
	v_exp_f32_e32 v55, v55
	v_exp_f32_e32 v56, v56
	v_exp_f32_e32 v57, v57
	v_exp_f32_e32 v59, v59
	v_pk_mul_f32 v[48:49], v[66:67], v[48:49]
	v_add_f32_e32 v50, 1.0, v50
	v_mul_f32_e32 v58, 0xbfb8aa3b, v49
	v_exp_f32_e32 v58, v58
	v_add_f32_e32 v54, 1.0, v54
	v_add_f32_e32 v51, 1.0, v51
	v_add_f32_e32 v55, 1.0, v55
	v_add_f32_e32 v56, 1.0, v56
	v_add_f32_e32 v57, 1.0, v57
	v_add_f32_e32 v59, 1.0, v59
	v_rcp_f32_e32 v50, v50
	v_rcp_f32_e32 v54, v54
	v_rcp_f32_e32 v51, v51
	v_rcp_f32_e32 v55, v55
	v_rcp_f32_e32 v56, v56
	v_rcp_f32_e32 v57, v57
; __device__ __forceinline__ unsigned cvt4_fp8(float a, float b, float c, float d) { int w = 0; w = __builtin_amdgcn_cvt_pk_fp8_f32(clamp448(a), clamp448(b), w, false); w = __builtin_amdgcn_cvt_pk_fp8_f32(clamp448(c), clamp448(d), w, true); return (unsigned)w; }
; __device__ __forceinline__ float sigmoidf_(float x) { return __builtin_amdgcn_rcpf(1.0f + __expf(-x)); }
; __device__ __forceinline__ float siluf_(float x) { return x * sigmoidf_(x); }
;     __device__ __forceinline__ void operator()(const AccT& acc, const Unit& u, int wr, int wc, int fr, int fq) const {
;     ...
;             for (int m = 0; m < 4; ++m) { const int rl = rl0 + ai * HALF + m * 16; const float rs = rs_p[rl]; f32x4 z0, z1;
;                 const i32x4v g0 = __builtin_bit_cast(i32x4v, acc[ai][0][m][0]), g1 = __builtin_bit_cast(i32x4v, acc[ai][0][m][1]), u0 = __builtin_bit_cast(i32x4v, acc[ai][1][m][0]), u1 = __builtin_bit_cast(i32x4v, acc[ai][1][m][1]);
; #pragma unroll
;                 for (int j = 0; j < 4; ++j) { z0[j] = siluf_((float)g0[j] * (rs * cg0[j])) * ((float)u0[j] * (rs * cu0[j])); z1[j] = siluf_((float)g1[j] * (rs * cg1[j])) * ((float)u1[j] * (rs * cu1[j])); }
;                 u32x2 w; w.x = cvt4_fp8(z0[0] * sout8, z0[1] * sout8, z0[2] * sout8, z0[3] * sout8); w.y = cvt4_fp8(z1[0] * sout8, z1[1] * sout8, z1[2] * sout8, z1[3] * sout8);
;                 *(u32x2*)(O + (size_t)(u.orow0 + rl) * ldo + cb) = w;
;                 __builtin_amdgcn_sched_barrier(0); }
	v_rcp_f32_e32 v59, v59
	v_add_f32_e32 v58, 1.0, v58
	v_rcp_f32_e32 v58, v58
	v_mul_f32_e32 v45, v45, v50
	v_mul_f32_e32 v47, v47, v54
	v_mul_f32_e32 v50, v53, v51
	v_mul_f32_e32 v39, v39, v55
	v_mul_f32_e32 v35, v35, v56
	v_mul_f32_e32 v43, v43, v57
	v_mul_f32_e32 v41, v41, v59
	v_mul_f32_e32 v44, v44, v45
	v_mul_f32_e32 v46, v46, v47
	v_mul_f32_e32 v45, v52, v50
	v_mul_f32_e32 v38, v38, v39
	v_mul_f32_e32 v34, v34, v35
	v_mul_f32_e32 v35, v42, v43
	v_mul_f32_e32 v40, v40, v41
	v_mul_f32_e32 v41, 4.0, v44
	v_mul_f32_e32 v42, 4.0, v46
	v_mul_f32_e32 v43, 4.0, v45
	v_mul_f32_e32 v38, 4.0, v38
	v_med3_f32 v41, v41, s71, v187
	v_med3_f32 v42, v42, s71, v187
	v_mul_f32_e32 v49, v49, v58
	v_med3_f32 v43, v43, s71, v187
	v_cvt_pk_fp8_f32 v36, v41, v42
	v_med3_f32 v38, v38, s71, v187
	v_mul_f32_e32 v39, v48, v49
	v_cvt_pk_fp8_f32 v37, v43, v38
	v_mul_f32_e32 v34, 4.0, v34
	v_mul_f32_e32 v39, 4.0, v39
	v_mul_f32_e32 v35, 4.0, v35
	v_mul_f32_e32 v40, 4.0, v40
	v_med3_f32 v34, v34, s71, v187
	v_med3_f32 v39, v39, s71, v187
	v_med3_f32 v35, v35, s71, v187
	v_cvt_pk_fp8_f32 v36, v34, v39 op_sel:[0,0,1]
	v_med3_f32 v34, v40, s71, v187
	v_cvt_pk_fp8_f32 v37, v35, v34 op_sel:[0,0,1]
	v_add_u32_e32 v34, 0x90, v136
	v_mad_i64_i32 v[34:35], s[6:7], v34, s72, v[116:117]
	v_lshl_add_u64 v[34:35], v[34:35], 0, v[130:131]
	global_store_dwordx2 v[34:35], v[36:37], off
	v_mov_b32_e32 v34, v224
	v_cvt_f32_i32_e32 v37, v30
	v_cvt_f32_i32_e32 v36, v22
	v_cvt_f32_i32_e32 v31, v31
	v_cvt_f32_i32_e32 v30, v23
	v_cvt_f32_i32_e32 v39, v26
	v_cvt_f32_i32_e32 v38, v18
	v_cvt_f32_i32_e32 v23, v27
	v_cvt_f32_i32_e32 v22, v19
	v_cvt_f32_i32_e32 v19, v32
	v_cvt_f32_i32_e32 v18, v24
	v_cvt_f32_i32_e32 v27, v28
	v_cvt_f32_i32_e32 v26, v20
	v_cvt_f32_i32_e32 v32, v25
	v_cvt_f32_i32_e32 v25, v29
	v_cvt_f32_i32_e32 v24, v21
	v_cvt_f32_i32_e32 v33, v33
	v_mov_b32_e32 v20, v163
	v_mov_b32_e32 v21, v163
	v_pk_mul_f32 v[28:29], v[114:115], v[34:35] op_sel_hi:[1,0]
	v_pk_mul_f32 v[42:43], v[122:123], v[34:35] op_sel_hi:[1,0]
	v_pk_mul_f32 v[40:41], v[118:119], v[34:35] op_sel_hi:[1,0]
	v_pk_mul_f32 v[44:45], v[124:125], v[34:35] op_sel_hi:[1,0]
	v_pk_mul_f32 v[46:47], v[126:127], v[34:35] op_sel_hi:[1,0]
	v_pk_mul_f32 v[48:49], v[128:129], v[34:35] op_sel_hi:[1,0]
	v_pk_mul_f32 v[50:51], v[134:135], v[34:35] op_sel_hi:[1,0]
	v_pk_mul_f32 v[34:35], v[120:121], v[34:35] op_sel_hi:[1,0]
	v_pk_mul_f32 v[28:29], v[28:29], v[36:37]
	v_pk_mul_f32 v[30:31], v[42:43], v[30:31]
	v_pk_mul_f32 v[36:37], v[40:41], v[38:39]
	v_pk_mul_f32 v[22:23], v[44:45], v[22:23]
	v_pk_mul_f32 v[18:19], v[46:47], v[18:19]
	v_pk_mul_f32 v[26:27], v[48:49], v[26:27]
	v_pk_mul_f32 v[24:25], v[34:35], v[24:25]
	v_mul_f32_e32 v34, 0xbfb8aa3b, v29
	v_mul_f32_e32 v38, 0xbfb8aa3b, v31
	v_mul_f32_e32 v35, 0xbfb8aa3b, v37
	v_mul_f32_e32 v39, 0xbfb8aa3b, v23
	v_mul_f32_e32 v40, 0xbfb8aa3b, v19
	v_mul_f32_e32 v41, 0xbfb8aa3b, v27
	v_mul_f32_e32 v43, 0xbfb8aa3b, v25
	v_exp_f32_e32 v34, v34
	v_exp_f32_e32 v38, v38
	v_exp_f32_e32 v35, v35
	v_exp_f32_e32 v39, v39
	v_exp_f32_e32 v40, v40
	v_exp_f32_e32 v41, v41
	v_exp_f32_e32 v43, v43
	v_pk_mul_f32 v[32:33], v[50:51], v[32:33]
	v_add_f32_e32 v34, 1.0, v34
	v_mul_f32_e32 v42, 0xbfb8aa3b, v33
	v_exp_f32_e32 v42, v42
	v_add_f32_e32 v38, 1.0, v38
	v_add_f32_e32 v35, 1.0, v35
	v_add_f32_e32 v39, 1.0, v39
	v_add_f32_e32 v40, 1.0, v40
	v_add_f32_e32 v41, 1.0, v41
	v_add_f32_e32 v43, 1.0, v43
	v_rcp_f32_e32 v34, v34
	v_rcp_f32_e32 v38, v38
	v_rcp_f32_e32 v35, v35
	v_rcp_f32_e32 v39, v39
	v_rcp_f32_e32 v40, v40
	v_rcp_f32_e32 v41, v41
	v_rcp_f32_e32 v43, v43
	v_add_f32_e32 v42, 1.0, v42
	v_rcp_f32_e32 v42, v42
	v_mul_f32_e32 v29, v29, v34
	v_mul_f32_e32 v31, v31, v38
	v_mul_f32_e32 v34, v37, v35
	v_mul_f32_e32 v23, v23, v39
	v_mul_f32_e32 v19, v19, v40
	v_mul_f32_e32 v27, v27, v41
	v_mul_f32_e32 v25, v25, v43
	v_mul_f32_e32 v28, v28, v29
	v_mul_f32_e32 v30, v30, v31
	v_mul_f32_e32 v29, v36, v34
	v_mul_f32_e32 v22, v22, v23
	v_mul_f32_e32 v18, v18, v19
	v_mul_f32_e32 v19, v26, v27
	v_mul_f32_e32 v24, v24, v25
	v_mul_f32_e32 v25, 4.0, v28
	v_mul_f32_e32 v26, 4.0, v30
	v_mul_f32_e32 v27, 4.0, v29
	v_mul_f32_e32 v22, 4.0, v22
	v_med3_f32 v25, v25, s71, v187
	v_med3_f32 v26, v26, s71, v187
	v_mul_f32_e32 v33, v33, v42
	v_med3_f32 v27, v27, s71, v187
	v_cvt_pk_fp8_f32 v20, v25, v26
; __device__ __forceinline__ unsigned cvt4_fp8(float a, float b, float c, float d) { int w = 0; w = __builtin_amdgcn_cvt_pk_fp8_f32(clamp448(a), clamp448(b), w, false); w = __builtin_amdgcn_cvt_pk_fp8_f32(clamp448(c), clamp448(d), w, true); return (unsigned)w; }
; __device__ __forceinline__ float siluf_(float x) { return x * sigmoidf_(x); }
;     __device__ __forceinline__ void operator()(const AccT& acc, const Unit& u, int wr, int wc, int fr, int fq) const {
;     ...
;             for (int m = 0; m < 4; ++m) { const int rl = rl0 + ai * HALF + m * 16; const float rs = rs_p[rl]; f32x4 z0, z1;
;                 const i32x4v g0 = __builtin_bit_cast(i32x4v, acc[ai][0][m][0]), g1 = __builtin_bit_cast(i32x4v, acc[ai][0][m][1]), u0 = __builtin_bit_cast(i32x4v, acc[ai][1][m][0]), u1 = __builtin_bit_cast(i32x4v, acc[ai][1][m][1]);
; #pragma unroll
;                 for (int j = 0; j < 4; ++j) { z0[j] = siluf_((float)g0[j] * (rs * cg0[j])) * ((float)u0[j] * (rs * cu0[j])); z1[j] = siluf_((float)g1[j] * (rs * cg1[j])) * ((float)u1[j] * (rs * cu1[j])); }
;                 u32x2 w; w.x = cvt4_fp8(z0[0] * sout8, z0[1] * sout8, z0[2] * sout8, z0[3] * sout8); w.y = cvt4_fp8(z1[0] * sout8, z1[1] * sout8, z1[2] * sout8, z1[3] * sout8);
;                 *(u32x2*)(O + (size_t)(u.orow0 + rl) * ldo + cb) = w;
;                 __builtin_amdgcn_sched_barrier(0); }
;     }
	v_med3_f32 v22, v22, s71, v187
	v_mul_f32_e32 v23, v32, v33
	v_cvt_pk_fp8_f32 v21, v27, v22
	v_mul_f32_e32 v18, 4.0, v18
	v_mul_f32_e32 v23, 4.0, v23
	v_mul_f32_e32 v19, 4.0, v19
	v_mul_f32_e32 v24, 4.0, v24
	v_med3_f32 v18, v18, s71, v187
	v_med3_f32 v23, v23, s71, v187
	v_med3_f32 v19, v19, s71, v187
	v_cvt_pk_fp8_f32 v20, v18, v23 op_sel:[0,0,1]
	v_med3_f32 v18, v24, s71, v187
	v_cvt_pk_fp8_f32 v21, v19, v18 op_sel:[0,0,1]
	v_add_u32_e32 v18, 0xa0, v136
	v_mad_i64_i32 v[18:19], s[4:5], v18, s72, v[116:117]
	v_lshl_add_u64 v[18:19], v[18:19], 0, v[130:131]
	global_store_dwordx2 v[18:19], v[20:21], off
	v_readfirstlane_b32 s4, v132
	v_readfirstlane_b32 s5, v133
	v_cvt_f32_i32_e32 v21, v14
	v_cvt_f32_i32_e32 v20, v6
	v_cvt_f32_i32_e32 v15, v15
	v_cvt_f32_i32_e32 v14, v7
	v_cvt_f32_i32_e32 v23, v10
	v_mov_b32_e32 v18, v225
	v_cvt_f32_i32_e32 v22, v2
	v_cvt_f32_i32_e32 v7, v11
	v_cvt_f32_i32_e32 v6, v3
	v_cvt_f32_i32_e32 v3, v16
	v_cvt_f32_i32_e32 v2, v8
	v_cvt_f32_i32_e32 v11, v12
	v_cvt_f32_i32_e32 v10, v4
	v_cvt_f32_i32_e32 v16, v9
	v_cvt_f32_i32_e32 v9, v13
	v_cvt_f32_i32_e32 v8, v5
	v_cvt_f32_i32_e32 v17, v17
	v_mov_b32_e32 v4, v163
	v_mov_b32_e32 v5, v163
	v_pk_mul_f32 v[12:13], v[114:115], v[18:19] op_sel_hi:[1,0]
	v_pk_mul_f32 v[26:27], v[122:123], v[18:19] op_sel_hi:[1,0]
	v_pk_mul_f32 v[24:25], v[118:119], v[18:19] op_sel_hi:[1,0]
	v_pk_mul_f32 v[28:29], v[124:125], v[18:19] op_sel_hi:[1,0]
	v_pk_mul_f32 v[30:31], v[126:127], v[18:19] op_sel_hi:[1,0]
	v_pk_mul_f32 v[32:33], v[128:129], v[18:19] op_sel_hi:[1,0]
	v_pk_mul_f32 v[34:35], v[134:135], v[18:19] op_sel_hi:[1,0]
	v_pk_mul_f32 v[18:19], v[120:121], v[18:19] op_sel_hi:[1,0]
	v_pk_mul_f32 v[12:13], v[12:13], v[20:21]
	v_pk_mul_f32 v[14:15], v[26:27], v[14:15]
	v_pk_mul_f32 v[20:21], v[24:25], v[22:23]
	v_pk_mul_f32 v[6:7], v[28:29], v[6:7]
	v_pk_mul_f32 v[2:3], v[30:31], v[2:3]
	v_pk_mul_f32 v[10:11], v[32:33], v[10:11]
	v_pk_mul_f32 v[8:9], v[18:19], v[8:9]
	v_mul_f32_e32 v18, 0xbfb8aa3b, v13
	v_mul_f32_e32 v22, 0xbfb8aa3b, v15
	v_mul_f32_e32 v19, 0xbfb8aa3b, v21
	v_mul_f32_e32 v23, 0xbfb8aa3b, v7
	v_mul_f32_e32 v24, 0xbfb8aa3b, v3
	v_mul_f32_e32 v25, 0xbfb8aa3b, v11
	v_mul_f32_e32 v27, 0xbfb8aa3b, v9
	v_exp_f32_e32 v18, v18
	v_exp_f32_e32 v22, v22
	v_exp_f32_e32 v19, v19
	v_exp_f32_e32 v23, v23
	v_exp_f32_e32 v24, v24
	v_exp_f32_e32 v25, v25
	v_exp_f32_e32 v27, v27
	v_pk_mul_f32 v[16:17], v[34:35], v[16:17]
	v_add_f32_e32 v18, 1.0, v18
	v_mul_f32_e32 v26, 0xbfb8aa3b, v17
	v_exp_f32_e32 v26, v26
	v_add_f32_e32 v22, 1.0, v22
	v_add_f32_e32 v19, 1.0, v19
	v_add_f32_e32 v23, 1.0, v23
	v_add_f32_e32 v24, 1.0, v24
	v_add_f32_e32 v25, 1.0, v25
	v_add_f32_e32 v27, 1.0, v27
	v_rcp_f32_e32 v18, v18
	v_rcp_f32_e32 v22, v22
	v_rcp_f32_e32 v19, v19
	v_rcp_f32_e32 v23, v23
	v_rcp_f32_e32 v24, v24
	v_rcp_f32_e32 v25, v25
	v_rcp_f32_e32 v27, v27
	v_add_f32_e32 v26, 1.0, v26
	v_rcp_f32_e32 v26, v26
	v_mul_f32_e32 v13, v13, v18
	v_mul_f32_e32 v15, v15, v22
	v_mul_f32_e32 v18, v21, v19
	v_mul_f32_e32 v7, v7, v23
	v_mul_f32_e32 v3, v3, v24
	v_mul_f32_e32 v11, v11, v25
	v_mul_f32_e32 v9, v9, v27
	v_mul_f32_e32 v12, v12, v13
	v_mul_f32_e32 v14, v14, v15
	v_mul_f32_e32 v13, v20, v18
	v_mul_f32_e32 v6, v6, v7
	v_mul_f32_e32 v2, v2, v3
	v_mul_f32_e32 v3, v10, v11
	v_mul_f32_e32 v8, v8, v9
	v_mul_f32_e32 v9, 4.0, v12
	v_mul_f32_e32 v10, 4.0, v14
	v_mul_f32_e32 v11, 4.0, v13
	v_mul_f32_e32 v6, 4.0, v6
	v_med3_f32 v9, v9, s71, v187
	v_med3_f32 v10, v10, s71, v187
	v_mul_f32_e32 v17, v17, v26
	v_cvt_pk_fp8_f32 v4, v9, v10
	v_med3_f32 v9, v11, s71, v187
	v_med3_f32 v6, v6, s71, v187
	v_mul_f32_e32 v7, v16, v17
	v_cvt_pk_fp8_f32 v5, v9, v6
	v_mul_f32_e32 v2, 4.0, v2
	v_mul_f32_e32 v7, 4.0, v7
	v_mul_f32_e32 v3, 4.0, v3
	v_mul_f32_e32 v8, 4.0, v8
	v_med3_f32 v2, v2, s71, v187
	v_med3_f32 v7, v7, s71, v187
	v_cvt_pk_fp8_f32 v4, v2, v7 op_sel:[0,0,1]
	v_med3_f32 v2, v3, s71, v187
	v_med3_f32 v3, v8, s71, v187
	v_cvt_pk_fp8_f32 v5, v2, v3 op_sel:[0,0,1]
	v_add_u32_e32 v2, 0xb0, v136
	v_mad_i64_i32 v[2:3], s[4:5], v2, s72, v[116:117]
	v_lshl_add_u64 v[2:3], v[2:3], 0, v[130:131]
	global_store_dwordx2 v[2:3], v[4:5], off
	s_and_b64 vcc, exec, s[2:3]
	s_mov_b64 s[2:3], -1
	s_cbranch_vccnz .LBB0_2537
	s_andn2_b64 vcc, exec, s[18:19]
	s_cbranch_vccnz .LBB0_2536
	s_barrier
	s_branch .LBB0_2536
